# v57 + copies in front of LDS-DMA loads removed + s_nop 0 after LDS waits in attention QK removed (all instruction-count trims stacked)
# baseline (speedup 1.0000x reference)
; #define PG8_STAGE(bufoff, gbase, voff) do { _Pragma("unroll") for (int _i = 0; _i < 2; ++_i) \
;         __builtin_amdgcn_global_load_lds((const __attribute__((address_space(1))) unsigned*)((const __attribute__((address_space(1))) char*)(gbase) + (unsigned)lnd_v((int)(voff)[_i])), (LAS unsigned*)(lds + (bufoff) + ldsw + _i * 8192), 16, 0, 0); } while (0)
; #define PG8_LDA(dst, b, h) do { _Pragma("unroll") for (int m = 0; m < 4; ++m) _Pragma("unroll") for (int k = 0; k < 2; ++k) dst[m][k] = *(const LAS bf16x8*)(lds + PG8_SA(b, h) + aoff + m * 2048 + k * 1024); } while (0)
; #define PG8_LDB(dst, b, h) do { _Pragma("unroll") for (int n = 0; n < 2; ++n) _Pragma("unroll") for (int k = 0; k < 2; ++k) dst[n][k] = *(const LAS bf16x8*)(lds + PG8_SB(b, h) + boff + n * 2048 + k * 1024); } while (0)
; #define PG8_MMA(ai, bj, At, Bt) do { __builtin_amdgcn_s_setprio(1); _Pragma("unroll") for (int m = 0; m < 4; ++m) _Pragma("unroll") for (int n = 0; n < 2; ++n) _Pragma("unroll") for (int k = 0; k < 2; ++k) \
;         acc[ai][bj][m][n] = __builtin_amdgcn_mfma_f32_16x16x32_bf16(Bt[n][k], At[m][k], acc[ai][bj][m][n], 0, 0, 0); __builtin_amdgcn_s_setprio(0); } while (0)
; #define PG8_WAIT_V(n) asm volatile("s_waitcnt vmcnt(" #n ")" ::: "memory")
; #define PG8_WAIT_L(n) asm volatile("s_waitcnt lgkmcnt(" #n ")" ::: "memory")
; #define PG8_BAR __builtin_amdgcn_s_barrier()
; #define PG8_SCHED __builtin_amdgcn_sched_barrier(0)
; template <class Desc, class Epi>
; __device__ __forceinline__ void gemm_phase(const int wv_, LAS unsigned char* lds, const Desc& d, const Epi& E) {
;     ...
;             PG8_LDB(B0, 0, 0); PG8_LDB(B1, 0, 1); PG8_SCHED; PG8_LDA(At, 0, 0); PG8_STAGE(PG8_SA(1, 1), a1, voffA1);
;             PG8_WAIT_V(8); PG8_WAIT_L(0); PG8_BAR; PG8_MMA(0, 0, At, B0); PG8_MMA(0, 1, At, B1); PG8_BAR; PG8_SCHED;
;             PG8_LDA(At, 0, 1); PG8_STAGE(PG8_SB(0, 0), b2, voffB); PG8_STAGE(PG8_SB(0, 1), b2 + hstepB, voffB); PG8_STAGE(PG8_SA(0, 0), a2, sA0);
;             PG8_WAIT_V(8); PG8_WAIT_L(0); PG8_BAR; PG8_MMA(1, 0, At, B0); PG8_MMA(1, 1, At, B1); PG8_BAR; PG8_SCHED;
.LBB0_662:
	ds_read_b128 v[154:157], v148
	ds_read_b128 v[158:161], v148 offset:1024
	ds_read_b128 v[162:165], v148 offset:2048
	ds_read_b128 v[166:169], v148 offset:3072
	ds_read_b128 v[170:173], v149
	ds_read_b128 v[174:177], v149 offset:1024
	ds_read_b128 v[178:181], v149 offset:2048
	ds_read_b128 v[182:185], v149 offset:3072
	s_add_u32 s2, s0, 0x80
	s_addc_u32 s3, s1, 0
	s_cmp_eq_u32 s60, 12
	s_cselect_b32 s3, s17, s3
	s_cselect_b32 s2, s16, s2
	s_cselect_b32 s27, s23, s59
	s_cselect_b32 s26, s22, s58
	s_mov_b32 m0, s42
	ds_read_b128 v[186:189], v150
	ds_read_b128 v[190:193], v150 offset:1024
	ds_read_b128 v[194:197], v150 offset:2048
	ds_read_b128 v[198:201], v150 offset:3072
	ds_read_b128 v[202:205], v150 offset:4096
	ds_read_b128 v[206:209], v150 offset:5120
	ds_read_b128 v[210:213], v150 offset:6144
	ds_read_b128 v[214:217], v150 offset:7168
	s_nop 0
	global_load_lds_dwordx4 v133, s[0:1]
	s_mov_b32 m0, s43
	s_nop 0
	global_load_lds_dwordx4 v136, s[0:1]
	s_waitcnt vmcnt(8)
	s_waitcnt lgkmcnt(0)
	s_barrier
	v_mfma_f32_16x16x32_bf16 v[124:127], v[154:157], v[186:189], v[124:127]
	v_mfma_f32_16x16x32_bf16 v[120:123], v[162:165], v[186:189], v[120:123]
	v_mfma_f32_16x16x32_bf16 v[108:111], v[154:157], v[194:197], v[108:111]
	v_mfma_f32_16x16x32_bf16 v[104:107], v[162:165], v[194:197], v[104:107]
	v_mfma_f32_16x16x32_bf16 v[92:95], v[154:157], v[202:205], v[92:95]
	v_mfma_f32_16x16x32_bf16 v[88:91], v[162:165], v[202:205], v[88:91]
	v_mfma_f32_16x16x32_bf16 v[76:79], v[154:157], v[210:213], v[76:79]
	v_mfma_f32_16x16x32_bf16 v[72:75], v[162:165], v[210:213], v[72:75]
	v_mfma_f32_16x16x32_bf16 v[124:127], v[158:161], v[190:193], v[124:127]
	v_mfma_f32_16x16x32_bf16 v[120:123], v[166:169], v[190:193], v[120:123]
	v_mfma_f32_16x16x32_bf16 v[108:111], v[158:161], v[198:201], v[108:111]
	v_mfma_f32_16x16x32_bf16 v[104:107], v[166:169], v[198:201], v[104:107]
	v_mfma_f32_16x16x32_bf16 v[92:95], v[158:161], v[206:209], v[92:95]
	v_mfma_f32_16x16x32_bf16 v[88:91], v[166:169], v[206:209], v[88:91]
	v_mfma_f32_16x16x32_bf16 v[76:79], v[158:161], v[214:217], v[76:79]
	v_mfma_f32_16x16x32_bf16 v[72:75], v[166:169], v[214:217], v[72:75]
	v_mfma_f32_16x16x32_bf16 v[116:119], v[170:173], v[186:189], v[116:119]
	v_mfma_f32_16x16x32_bf16 v[112:115], v[178:181], v[186:189], v[112:115]
	v_mfma_f32_16x16x32_bf16 v[100:103], v[170:173], v[194:197], v[100:103]
	v_mfma_f32_16x16x32_bf16 v[96:99], v[178:181], v[194:197], v[96:99]
	v_mfma_f32_16x16x32_bf16 v[84:87], v[170:173], v[202:205], v[84:87]
	v_mfma_f32_16x16x32_bf16 v[80:83], v[178:181], v[202:205], v[80:83]
	v_mfma_f32_16x16x32_bf16 v[68:71], v[170:173], v[210:213], v[68:71]
	v_mfma_f32_16x16x32_bf16 v[64:67], v[178:181], v[210:213], v[64:67]
	v_mfma_f32_16x16x32_bf16 v[116:119], v[174:177], v[190:193], v[116:119]
	v_mfma_f32_16x16x32_bf16 v[112:115], v[182:185], v[190:193], v[112:115]
	v_mfma_f32_16x16x32_bf16 v[100:103], v[174:177], v[198:201], v[100:103]
	v_mfma_f32_16x16x32_bf16 v[96:99], v[182:185], v[198:201], v[96:99]
	v_mfma_f32_16x16x32_bf16 v[84:87], v[174:177], v[206:209], v[84:87]
	v_mfma_f32_16x16x32_bf16 v[80:83], v[182:185], v[206:209], v[80:83]
	v_mfma_f32_16x16x32_bf16 v[68:71], v[174:177], v[214:217], v[68:71]
	v_mfma_f32_16x16x32_bf16 v[64:67], v[182:185], v[214:217], v[64:67]
	s_barrier
	s_mov_b32 m0, s44
	ds_read_b128 v[186:189], v150 offset:16384
	ds_read_b128 v[190:193], v150 offset:17408
	ds_read_b128 v[194:197], v150 offset:18432
	ds_read_b128 v[198:201], v150 offset:19456
	ds_read_b128 v[202:205], v150 offset:20480
	ds_read_b128 v[206:209], v150 offset:21504
	ds_read_b128 v[210:213], v150 offset:22528
	ds_read_b128 v[214:217], v150 offset:23552
	s_add_u32 s62, s26, 0x40000
	global_load_lds_dwordx4 v134, s[26:27]
	s_mov_b32 m0, s45
	s_addc_u32 s63, s27, 0
	global_load_lds_dwordx4 v137, s[26:27]
	s_mov_b32 m0, s46
	s_nop 0
	global_load_lds_dwordx4 v134, s[62:63]
	s_mov_b32 m0, s47
	s_nop 0
	global_load_lds_dwordx4 v137, s[62:63]
	s_mov_b32 m0, s36
	s_nop 0
	global_load_lds_dwordx4 v132, s[2:3]
	s_mov_b32 m0, s37
	s_nop 0
	global_load_lds_dwordx4 v135, s[2:3]
	s_waitcnt vmcnt(8)
	s_waitcnt lgkmcnt(0)
	s_barrier
	v_mfma_f32_16x16x32_bf16 v[60:63], v[154:157], v[186:189], v[60:63]
	v_mfma_f32_16x16x32_bf16 v[56:59], v[162:165], v[186:189], v[56:59]
	v_mfma_f32_16x16x32_bf16 v[44:47], v[154:157], v[194:197], v[44:47]
	v_mfma_f32_16x16x32_bf16 v[32:35], v[162:165], v[194:197], v[32:35]
	v_mfma_f32_16x16x32_bf16 v[16:19], v[154:157], v[202:205], v[16:19]
	v_mfma_f32_16x16x32_bf16 v[8:11], v[162:165], v[202:205], v[8:11]
	v_mfma_f32_16x16x32_bf16 v[4:7], v[154:157], v[210:213], v[4:7]
	v_mfma_f32_16x16x32_bf16 v[0:3], v[162:165], v[210:213], v[0:3]
	v_mfma_f32_16x16x32_bf16 v[60:63], v[158:161], v[190:193], v[60:63]
	v_mfma_f32_16x16x32_bf16 v[56:59], v[166:169], v[190:193], v[56:59]
	v_mfma_f32_16x16x32_bf16 v[44:47], v[158:161], v[198:201], v[44:47]
	v_mfma_f32_16x16x32_bf16 v[32:35], v[166:169], v[198:201], v[32:35]
	v_mfma_f32_16x16x32_bf16 v[16:19], v[158:161], v[206:209], v[16:19]
	v_mfma_f32_16x16x32_bf16 v[8:11], v[166:169], v[206:209], v[8:11]
	v_mfma_f32_16x16x32_bf16 v[4:7], v[158:161], v[214:217], v[4:7]
	v_mfma_f32_16x16x32_bf16 v[0:3], v[166:169], v[214:217], v[0:3]
	v_mfma_f32_16x16x32_bf16 v[52:55], v[170:173], v[186:189], v[52:55]
	v_mfma_f32_16x16x32_bf16 v[48:51], v[178:181], v[186:189], v[48:51]
	v_mfma_f32_16x16x32_bf16 v[28:31], v[170:173], v[194:197], v[28:31]
	v_mfma_f32_16x16x32_bf16 v[12:15], v[178:181], v[194:197], v[12:15]
	v_mfma_f32_16x16x32_bf16 v[36:39], v[170:173], v[202:205], v[36:39]
	v_mfma_f32_16x16x32_bf16 v[40:43], v[178:181], v[202:205], v[40:43]
	v_mfma_f32_16x16x32_bf16 v[20:23], v[170:173], v[210:213], v[20:23]
	v_mfma_f32_16x16x32_bf16 v[24:27], v[178:181], v[210:213], v[24:27]
	v_mfma_f32_16x16x32_bf16 v[52:55], v[174:177], v[190:193], v[52:55]
	v_mfma_f32_16x16x32_bf16 v[48:51], v[182:185], v[190:193], v[48:51]
	v_mfma_f32_16x16x32_bf16 v[28:31], v[174:177], v[198:201], v[28:31]
	v_mfma_f32_16x16x32_bf16 v[12:15], v[182:185], v[198:201], v[12:15]
	v_mfma_f32_16x16x32_bf16 v[36:39], v[174:177], v[206:209], v[36:39]
	v_mfma_f32_16x16x32_bf16 v[40:43], v[182:185], v[206:209], v[40:43]
	v_mfma_f32_16x16x32_bf16 v[20:23], v[174:177], v[214:217], v[20:23]
	v_mfma_f32_16x16x32_bf16 v[24:27], v[182:185], v[214:217], v[24:27]
	s_barrier
; #define PG8_STAGE(bufoff, gbase, voff) do { _Pragma("unroll") for (int _i = 0; _i < 2; ++_i) \
;         __builtin_amdgcn_global_load_lds((const __attribute__((address_space(1))) unsigned*)((const __attribute__((address_space(1))) char*)(gbase) + (unsigned)lnd_v((int)(voff)[_i])), (LAS unsigned*)(lds + (bufoff) + ldsw + _i * 8192), 16, 0, 0); } while (0)
; #define PG8_LDA(dst, b, h) do { _Pragma("unroll") for (int m = 0; m < 4; ++m) _Pragma("unroll") for (int k = 0; k < 2; ++k) dst[m][k] = *(const LAS bf16x8*)(lds + PG8_SA(b, h) + aoff + m * 2048 + k * 1024); } while (0)
; #define PG8_LDB(dst, b, h) do { _Pragma("unroll") for (int n = 0; n < 2; ++n) _Pragma("unroll") for (int k = 0; k < 2; ++k) dst[n][k] = *(const LAS bf16x8*)(lds + PG8_SB(b, h) + boff + n * 2048 + k * 1024); } while (0)
; #define PG8_MMA(ai, bj, At, Bt) do { __builtin_amdgcn_s_setprio(1); _Pragma("unroll") for (int m = 0; m < 4; ++m) _Pragma("unroll") for (int n = 0; n < 2; ++n) _Pragma("unroll") for (int k = 0; k < 2; ++k) \
;         acc[ai][bj][m][n] = __builtin_amdgcn_mfma_f32_16x16x32_bf16(Bt[n][k], At[m][k], acc[ai][bj][m][n], 0, 0, 0); __builtin_amdgcn_s_setprio(0); } while (0)
; #define PG8_WAIT_V(n) asm volatile("s_waitcnt vmcnt(" #n ")" ::: "memory")
; #define PG8_WAIT_L(n) asm volatile("s_waitcnt lgkmcnt(" #n ")" ::: "memory")
; #define PG8_BAR __builtin_amdgcn_s_barrier()
; #define PG8_SCHED __builtin_amdgcn_sched_barrier(0)
; template <class Desc, class Epi>
; __device__ __forceinline__ void gemm_phase(const int wv_, LAS unsigned char* lds, const Desc& d, const Epi& E) {
;     ...
;             PG8_LDB(B0, 1, 0); PG8_LDB(B1, 1, 1); PG8_SCHED; PG8_LDA(At, 1, 0); PG8_STAGE(PG8_SA(0, 1), a2, sA1);
;             PG8_WAIT_V(8); PG8_WAIT_L(0); PG8_BAR; PG8_MMA(0, 0, At, B0); PG8_MMA(0, 1, At, B1); PG8_BAR; PG8_SCHED;
;             PG8_LDA(At, 1, 1); PG8_STAGE(PG8_SB(1, 0), b3, voffB); PG8_STAGE(PG8_SB(1, 1), b3 + hstepB, voffB); PG8_STAGE(PG8_SA(1, 0), a3, sA0);
;             PG8_WAIT_V(8); PG8_WAIT_L(0); PG8_BAR; PG8_MMA(1, 0, At, B0); PG8_MMA(1, 1, At, B1); PG8_BAR; PG8_SCHED;
;         }
;         if (wr == 0) PG8_BAR;
	ds_read_b128 v[154:157], v151
	ds_read_b128 v[158:161], v151 offset:1024
	ds_read_b128 v[162:165], v151 offset:2048
	ds_read_b128 v[166:169], v151 offset:3072
	ds_read_b128 v[170:173], v152
	ds_read_b128 v[174:177], v152 offset:1024
	ds_read_b128 v[178:181], v152 offset:2048
	ds_read_b128 v[182:185], v152 offset:3072
	s_mov_b32 m0, s38
	ds_read_b128 v[186:189], v150 offset:32768
	ds_read_b128 v[190:193], v150 offset:33792
	ds_read_b128 v[194:197], v150 offset:34816
	ds_read_b128 v[198:201], v150 offset:35840
	ds_read_b128 v[202:205], v150 offset:36864
	ds_read_b128 v[206:209], v150 offset:37888
	ds_read_b128 v[210:213], v150 offset:38912
	ds_read_b128 v[214:217], v150 offset:39936
	s_nop 0
	global_load_lds_dwordx4 v133, s[2:3]
	s_mov_b32 m0, s39
	s_nop 0
	global_load_lds_dwordx4 v136, s[2:3]
	s_waitcnt vmcnt(8)
	s_waitcnt lgkmcnt(0)
	s_barrier
	v_mfma_f32_16x16x32_bf16 v[124:127], v[154:157], v[186:189], v[124:127]
	v_mfma_f32_16x16x32_bf16 v[120:123], v[162:165], v[186:189], v[120:123]
	v_mfma_f32_16x16x32_bf16 v[108:111], v[154:157], v[194:197], v[108:111]
	v_mfma_f32_16x16x32_bf16 v[104:107], v[162:165], v[194:197], v[104:107]
	v_mfma_f32_16x16x32_bf16 v[92:95], v[154:157], v[202:205], v[92:95]
	v_mfma_f32_16x16x32_bf16 v[88:91], v[162:165], v[202:205], v[88:91]
	v_mfma_f32_16x16x32_bf16 v[76:79], v[154:157], v[210:213], v[76:79]
	v_mfma_f32_16x16x32_bf16 v[72:75], v[162:165], v[210:213], v[72:75]
	v_mfma_f32_16x16x32_bf16 v[124:127], v[158:161], v[190:193], v[124:127]
	v_mfma_f32_16x16x32_bf16 v[120:123], v[166:169], v[190:193], v[120:123]
	v_mfma_f32_16x16x32_bf16 v[108:111], v[158:161], v[198:201], v[108:111]
	v_mfma_f32_16x16x32_bf16 v[104:107], v[166:169], v[198:201], v[104:107]
	v_mfma_f32_16x16x32_bf16 v[92:95], v[158:161], v[206:209], v[92:95]
	v_mfma_f32_16x16x32_bf16 v[88:91], v[166:169], v[206:209], v[88:91]
	v_mfma_f32_16x16x32_bf16 v[76:79], v[158:161], v[214:217], v[76:79]
	v_mfma_f32_16x16x32_bf16 v[72:75], v[166:169], v[214:217], v[72:75]
	v_mfma_f32_16x16x32_bf16 v[116:119], v[170:173], v[186:189], v[116:119]
	v_mfma_f32_16x16x32_bf16 v[112:115], v[178:181], v[186:189], v[112:115]
	v_mfma_f32_16x16x32_bf16 v[100:103], v[170:173], v[194:197], v[100:103]
	v_mfma_f32_16x16x32_bf16 v[96:99], v[178:181], v[194:197], v[96:99]
	v_mfma_f32_16x16x32_bf16 v[84:87], v[170:173], v[202:205], v[84:87]
	v_mfma_f32_16x16x32_bf16 v[80:83], v[178:181], v[202:205], v[80:83]
	v_mfma_f32_16x16x32_bf16 v[68:71], v[170:173], v[210:213], v[68:71]
	v_mfma_f32_16x16x32_bf16 v[64:67], v[178:181], v[210:213], v[64:67]
	v_mfma_f32_16x16x32_bf16 v[116:119], v[174:177], v[190:193], v[116:119]
	v_mfma_f32_16x16x32_bf16 v[112:115], v[182:185], v[190:193], v[112:115]
	v_mfma_f32_16x16x32_bf16 v[100:103], v[174:177], v[198:201], v[100:103]
	v_mfma_f32_16x16x32_bf16 v[96:99], v[182:185], v[198:201], v[96:99]
	v_mfma_f32_16x16x32_bf16 v[84:87], v[174:177], v[206:209], v[84:87]
	v_mfma_f32_16x16x32_bf16 v[80:83], v[182:185], v[206:209], v[80:83]
	v_mfma_f32_16x16x32_bf16 v[68:71], v[174:177], v[214:217], v[68:71]
	v_mfma_f32_16x16x32_bf16 v[64:67], v[182:185], v[214:217], v[64:67]
	s_barrier
	v_mov_b32_e32 v128, v134
	ds_read_b128 v[186:189], v150 offset:49152
	ds_read_b128 v[190:193], v150 offset:50176
	ds_read_b128 v[194:197], v150 offset:51200
	ds_read_b128 v[198:201], v150 offset:52224
	ds_read_b128 v[202:205], v150 offset:53248
	ds_read_b128 v[206:209], v150 offset:54272
	ds_read_b128 v[210:213], v150 offset:55296
	ds_read_b128 v[214:217], v150 offset:56320
	s_mov_b32 m0, s48
	v_lshl_add_u64 v[130:131], s[26:27], 0, v[128:129]
	v_lshl_add_u64 v[130:131], v[130:131], 0, s[8:9]
	v_mov_b32_e32 v128, v137
	global_load_lds_dwordx4 v[130:131], off
	s_mov_b32 m0, s49
	v_lshl_add_u64 v[130:131], s[26:27], 0, v[128:129]
	v_lshl_add_u64 v[130:131], v[130:131], 0, s[8:9]
	s_add_u32 s26, s26, 0x40080
	global_load_lds_dwordx4 v[130:131], off
	s_addc_u32 s27, s27, 0
	s_mov_b32 m0, s50
	s_nop 0
	global_load_lds_dwordx4 v134, s[26:27]
	s_mov_b32 m0, s51
	s_nop 0
	global_load_lds_dwordx4 v137, s[26:27]
	v_mov_b32_e32 v128, v132
	s_mov_b32 m0, s40
	v_lshl_add_u64 v[130:131], s[2:3], 0, v[128:129]
	v_lshl_add_u64 v[130:131], v[130:131], 0, s[8:9]
	v_mov_b32_e32 v128, v135
	global_load_lds_dwordx4 v[130:131], off
	s_mov_b32 m0, s41
	v_lshl_add_u64 v[130:131], s[2:3], 0, v[128:129]
	v_lshl_add_u64 v[130:131], v[130:131], 0, s[8:9]
	global_load_lds_dwordx4 v[130:131], off
	s_waitcnt vmcnt(8)
	s_waitcnt lgkmcnt(0)
	s_barrier
	v_mfma_f32_16x16x32_bf16 v[60:63], v[154:157], v[186:189], v[60:63]
	v_mfma_f32_16x16x32_bf16 v[56:59], v[162:165], v[186:189], v[56:59]
	v_mfma_f32_16x16x32_bf16 v[44:47], v[154:157], v[194:197], v[44:47]
	v_mfma_f32_16x16x32_bf16 v[32:35], v[162:165], v[194:197], v[32:35]
	v_mfma_f32_16x16x32_bf16 v[16:19], v[154:157], v[202:205], v[16:19]
	v_mfma_f32_16x16x32_bf16 v[8:11], v[162:165], v[202:205], v[8:11]
	v_mfma_f32_16x16x32_bf16 v[4:7], v[154:157], v[210:213], v[4:7]
	v_mfma_f32_16x16x32_bf16 v[0:3], v[162:165], v[210:213], v[0:3]
	v_mfma_f32_16x16x32_bf16 v[60:63], v[158:161], v[190:193], v[60:63]
	v_mfma_f32_16x16x32_bf16 v[56:59], v[166:169], v[190:193], v[56:59]
	v_mfma_f32_16x16x32_bf16 v[44:47], v[158:161], v[198:201], v[44:47]
	v_mfma_f32_16x16x32_bf16 v[32:35], v[166:169], v[198:201], v[32:35]
	v_mfma_f32_16x16x32_bf16 v[16:19], v[158:161], v[206:209], v[16:19]
	v_mfma_f32_16x16x32_bf16 v[8:11], v[166:169], v[206:209], v[8:11]
	v_mfma_f32_16x16x32_bf16 v[4:7], v[158:161], v[214:217], v[4:7]
	v_mfma_f32_16x16x32_bf16 v[0:3], v[166:169], v[214:217], v[0:3]
	v_mfma_f32_16x16x32_bf16 v[52:55], v[170:173], v[186:189], v[52:55]
	v_mfma_f32_16x16x32_bf16 v[48:51], v[178:181], v[186:189], v[48:51]
	v_mfma_f32_16x16x32_bf16 v[28:31], v[170:173], v[194:197], v[28:31]
	v_mfma_f32_16x16x32_bf16 v[12:15], v[178:181], v[194:197], v[12:15]
	v_mfma_f32_16x16x32_bf16 v[36:39], v[170:173], v[202:205], v[36:39]
	v_mfma_f32_16x16x32_bf16 v[40:43], v[178:181], v[202:205], v[40:43]
	v_mfma_f32_16x16x32_bf16 v[20:23], v[170:173], v[210:213], v[20:23]
	v_mfma_f32_16x16x32_bf16 v[24:27], v[178:181], v[210:213], v[24:27]
	v_mfma_f32_16x16x32_bf16 v[52:55], v[174:177], v[190:193], v[52:55]
	v_mfma_f32_16x16x32_bf16 v[48:51], v[182:185], v[190:193], v[48:51]
	v_mfma_f32_16x16x32_bf16 v[28:31], v[174:177], v[198:201], v[28:31]
	v_mfma_f32_16x16x32_bf16 v[12:15], v[182:185], v[198:201], v[12:15]
	v_mfma_f32_16x16x32_bf16 v[36:39], v[174:177], v[206:209], v[36:39]
	v_mfma_f32_16x16x32_bf16 v[40:43], v[182:185], v[206:209], v[40:43]
	v_mfma_f32_16x16x32_bf16 v[20:23], v[174:177], v[214:217], v[20:23]
	v_mfma_f32_16x16x32_bf16 v[24:27], v[182:185], v[214:217], v[24:27]
	s_barrier
	s_add_i32 s60, s60, 2
	s_add_u32 s0, s0, 0x100
	s_addc_u32 s1, s1, 0
	s_add_u32 s58, s58, 0x100
	s_addc_u32 s59, s59, 0
	s_cmp_gt_u32 s60, 13
	s_cbranch_scc0 .LBB0_662
	s_and_b64 vcc, exec, s[14:15]
	s_cbranch_vccz .LBB0_665
	s_barrier

; #define PG8_STAGE(bufoff, gbase, voff) do { _Pragma("unroll") for (int _i = 0; _i < 2; ++_i) \
;         __builtin_amdgcn_global_load_lds((const __attribute__((address_space(1))) unsigned*)((const __attribute__((address_space(1))) char*)(gbase) + (unsigned)lnd_v((int)(voff)[_i])), (LAS unsigned*)(lds + (bufoff) + ldsw + _i * 8192), 16, 0, 0); } while (0)
; #define PG8_LDA(dst, b, h) do { _Pragma("unroll") for (int m = 0; m < 4; ++m) _Pragma("unroll") for (int k = 0; k < 2; ++k) dst[m][k] = *(const LAS bf16x8*)(lds + PG8_SA(b, h) + aoff + m * 2048 + k * 1024); } while (0)
; #define PG8_LDB(dst, b, h) do { _Pragma("unroll") for (int n = 0; n < 2; ++n) _Pragma("unroll") for (int k = 0; k < 2; ++k) dst[n][k] = *(const LAS bf16x8*)(lds + PG8_SB(b, h) + boff + n * 2048 + k * 1024); } while (0)
; #define PG8_MMA(ai, bj, At, Bt) do { __builtin_amdgcn_s_setprio(1); _Pragma("unroll") for (int m = 0; m < 4; ++m) _Pragma("unroll") for (int n = 0; n < 2; ++n) _Pragma("unroll") for (int k = 0; k < 2; ++k) \
;         acc[ai][bj][m][n] = __builtin_amdgcn_mfma_f32_16x16x32_bf16(Bt[n][k], At[m][k], acc[ai][bj][m][n], 0, 0, 0); __builtin_amdgcn_s_setprio(0); } while (0)
; #define PG8_WAIT_V(n) asm volatile("s_waitcnt vmcnt(" #n ")" ::: "memory")
; #define PG8_WAIT_L(n) asm volatile("s_waitcnt lgkmcnt(" #n ")" ::: "memory")
; #define PG8_BAR __builtin_amdgcn_s_barrier()
; #define PG8_SCHED __builtin_amdgcn_sched_barrier(0)
; template <class Desc, class Epi>
; __device__ __forceinline__ void gemm_phase(const int wv_, LAS unsigned char* lds, const Desc& d, const Epi& E) {
;     ...
;             PG8_LDB(B0, 0, 0); PG8_LDB(B1, 0, 1); PG8_SCHED; PG8_LDA(At, 0, 0); PG8_STAGE(PG8_SA(1, 1), a1, voffA1);
;             PG8_WAIT_V(8); PG8_WAIT_L(0); PG8_BAR; PG8_MMA(0, 0, At, B0); PG8_MMA(0, 1, At, B1); PG8_BAR; PG8_SCHED;
;             PG8_LDA(At, 0, 1); PG8_STAGE(PG8_SB(0, 0), b2, voffB); PG8_STAGE(PG8_SB(0, 1), b2 + hstepB, voffB); PG8_STAGE(PG8_SA(0, 0), a2, sA0);
;             PG8_WAIT_V(8); PG8_WAIT_L(0); PG8_BAR; PG8_MMA(1, 0, At, B0); PG8_MMA(1, 1, At, B1); PG8_BAR; PG8_SCHED;
.LBB0_747:
	s_add_u32 s4, s2, 0x80
	s_addc_u32 s5, s3, 0
	s_add_i32 s63, 0, 0x10000
	s_cmp_eq_u32 s45, 12
	s_cselect_b32 s5, s47, s5
	s_cselect_b32 s4, s46, s4
	v_add_u32_e32 v96, s63, v139
	s_cselect_b32 s21, s49, s43
	s_cselect_b32 s20, s48, s29
	s_add_i32 s66, 0, 0x14000
	ds_read_b128 v[150:153], v96
	ds_read_b128 v[154:157], v96 offset:1024
	ds_read_b128 v[158:161], v96 offset:2048
	ds_read_b128 v[162:165], v96 offset:3072
	v_add_u32_e32 v96, s66, v139
	ds_read_b128 v[166:169], v96
	ds_read_b128 v[170:173], v96 offset:1024
	ds_read_b128 v[174:177], v96 offset:2048
	ds_read_b128 v[178:181], v96 offset:3072
	ds_read_b128 v[182:185], v149
	ds_read_b128 v[186:189], v149 offset:1024
	ds_read_b128 v[190:193], v149 offset:2048
	ds_read_b128 v[194:197], v149 offset:3072
	ds_read_b128 v[198:201], v149 offset:4096
	ds_read_b128 v[202:205], v149 offset:5120
	ds_read_b128 v[206:209], v149 offset:6144
	ds_read_b128 v[210:213], v149 offset:7168
	s_add_i32 m0, s55, 0xc000
	s_nop 0
	global_load_lds_dwordx4 v133, s[2:3]
	s_add_i32 m0, s55, 0xe000
	s_nop 0
	global_load_lds_dwordx4 v136, s[2:3]
	s_waitcnt vmcnt(8)
	s_waitcnt lgkmcnt(0)
	s_barrier
	v_mfma_f32_16x16x32_bf16 v[126:129], v[150:153], v[182:185], v[126:129]
	v_mfma_f32_16x16x32_bf16 v[122:125], v[158:161], v[182:185], v[122:125]
	v_mfma_f32_16x16x32_bf16 v[110:113], v[150:153], v[190:193], v[110:113]
	v_mfma_f32_16x16x32_bf16 v[106:109], v[158:161], v[190:193], v[106:109]
	v_mfma_f32_16x16x32_bf16 v[92:95], v[150:153], v[198:201], v[92:95]
	v_mfma_f32_16x16x32_bf16 v[88:91], v[158:161], v[198:201], v[88:91]
	v_mfma_f32_16x16x32_bf16 v[76:79], v[150:153], v[206:209], v[76:79]
	v_mfma_f32_16x16x32_bf16 v[72:75], v[158:161], v[206:209], v[72:75]
	v_mfma_f32_16x16x32_bf16 v[126:129], v[154:157], v[186:189], v[126:129]
	v_mfma_f32_16x16x32_bf16 v[122:125], v[162:165], v[186:189], v[122:125]
	v_mfma_f32_16x16x32_bf16 v[110:113], v[154:157], v[194:197], v[110:113]
	v_mfma_f32_16x16x32_bf16 v[106:109], v[162:165], v[194:197], v[106:109]
	v_mfma_f32_16x16x32_bf16 v[92:95], v[154:157], v[202:205], v[92:95]
	v_mfma_f32_16x16x32_bf16 v[88:91], v[162:165], v[202:205], v[88:91]
	v_mfma_f32_16x16x32_bf16 v[76:79], v[154:157], v[210:213], v[76:79]
	v_mfma_f32_16x16x32_bf16 v[72:75], v[162:165], v[210:213], v[72:75]
	v_mfma_f32_16x16x32_bf16 v[118:121], v[166:169], v[182:185], v[118:121]
	v_mfma_f32_16x16x32_bf16 v[114:117], v[174:177], v[182:185], v[114:117]
	v_mfma_f32_16x16x32_bf16 v[102:105], v[166:169], v[190:193], v[102:105]
	v_mfma_f32_16x16x32_bf16 v[98:101], v[174:177], v[190:193], v[98:101]
	v_mfma_f32_16x16x32_bf16 v[84:87], v[166:169], v[198:201], v[84:87]
	v_mfma_f32_16x16x32_bf16 v[80:83], v[174:177], v[198:201], v[80:83]
	v_mfma_f32_16x16x32_bf16 v[68:71], v[166:169], v[206:209], v[68:71]
	v_mfma_f32_16x16x32_bf16 v[64:67], v[174:177], v[206:209], v[64:67]
	v_mfma_f32_16x16x32_bf16 v[118:121], v[170:173], v[186:189], v[118:121]
	v_mfma_f32_16x16x32_bf16 v[114:117], v[178:181], v[186:189], v[114:117]
	v_mfma_f32_16x16x32_bf16 v[102:105], v[170:173], v[194:197], v[102:105]
	v_mfma_f32_16x16x32_bf16 v[98:101], v[178:181], v[194:197], v[98:101]
	v_mfma_f32_16x16x32_bf16 v[84:87], v[170:173], v[202:205], v[84:87]
	v_mfma_f32_16x16x32_bf16 v[80:83], v[178:181], v[202:205], v[80:83]
	v_mfma_f32_16x16x32_bf16 v[68:71], v[170:173], v[210:213], v[68:71]
	v_mfma_f32_16x16x32_bf16 v[64:67], v[178:181], v[210:213], v[64:67]
	s_barrier
	s_add_i32 s63, s63, s54
	ds_read_b128 v[182:185], v149 offset:16384
	ds_read_b128 v[186:189], v149 offset:17408
	ds_read_b128 v[190:193], v149 offset:18432
	ds_read_b128 v[194:197], v149 offset:19456
	ds_read_b128 v[198:201], v149 offset:20480
	ds_read_b128 v[202:205], v149 offset:21504
	ds_read_b128 v[206:209], v149 offset:22528
	ds_read_b128 v[210:213], v149 offset:23552
	s_mov_b32 m0, s63
	s_nop 0
	global_load_lds_dwordx4 v134, s[20:21]
	s_add_i32 m0, s63, 0x2000
	s_add_u32 s64, s20, 0x40000
	global_load_lds_dwordx4 v137, s[20:21]
	s_addc_u32 s65, s21, 0
	s_add_i32 s63, s66, s54
	s_mov_b32 m0, s63
	s_nop 0
	global_load_lds_dwordx4 v134, s[64:65]
	s_add_i32 m0, s63, 0x2000
	s_nop 0
	global_load_lds_dwordx4 v137, s[64:65]
	s_mov_b32 m0, s55
	s_nop 0
	global_load_lds_dwordx4 v132, s[4:5]
	s_mov_b32 m0, s56
	s_nop 0
	global_load_lds_dwordx4 v135, s[4:5]
	s_waitcnt vmcnt(8)
	s_waitcnt lgkmcnt(0)
	s_barrier
	v_mfma_f32_16x16x32_bf16 v[60:63], v[150:153], v[182:185], v[60:63]
	v_mfma_f32_16x16x32_bf16 v[56:59], v[158:161], v[182:185], v[56:59]
	v_mfma_f32_16x16x32_bf16 v[44:47], v[150:153], v[190:193], v[44:47]
	v_mfma_f32_16x16x32_bf16 v[32:35], v[158:161], v[190:193], v[32:35]
	v_mfma_f32_16x16x32_bf16 v[16:19], v[150:153], v[198:201], v[16:19]
	v_mfma_f32_16x16x32_bf16 v[8:11], v[158:161], v[198:201], v[8:11]
	v_mfma_f32_16x16x32_bf16 v[4:7], v[150:153], v[206:209], v[4:7]
	v_mfma_f32_16x16x32_bf16 v[0:3], v[158:161], v[206:209], v[0:3]
	v_mfma_f32_16x16x32_bf16 v[60:63], v[154:157], v[186:189], v[60:63]
	v_mfma_f32_16x16x32_bf16 v[56:59], v[162:165], v[186:189], v[56:59]
	v_mfma_f32_16x16x32_bf16 v[44:47], v[154:157], v[194:197], v[44:47]
	v_mfma_f32_16x16x32_bf16 v[32:35], v[162:165], v[194:197], v[32:35]
	v_mfma_f32_16x16x32_bf16 v[16:19], v[154:157], v[202:205], v[16:19]
	v_mfma_f32_16x16x32_bf16 v[8:11], v[162:165], v[202:205], v[8:11]
	v_mfma_f32_16x16x32_bf16 v[4:7], v[154:157], v[210:213], v[4:7]
	v_mfma_f32_16x16x32_bf16 v[0:3], v[162:165], v[210:213], v[0:3]
	v_mfma_f32_16x16x32_bf16 v[52:55], v[166:169], v[182:185], v[52:55]
	v_mfma_f32_16x16x32_bf16 v[48:51], v[174:177], v[182:185], v[48:51]
	v_mfma_f32_16x16x32_bf16 v[28:31], v[166:169], v[190:193], v[28:31]
	v_mfma_f32_16x16x32_bf16 v[12:15], v[174:177], v[190:193], v[12:15]
	v_mfma_f32_16x16x32_bf16 v[36:39], v[166:169], v[198:201], v[36:39]
	v_mfma_f32_16x16x32_bf16 v[40:43], v[174:177], v[198:201], v[40:43]
	v_mfma_f32_16x16x32_bf16 v[20:23], v[166:169], v[206:209], v[20:23]
	v_mfma_f32_16x16x32_bf16 v[24:27], v[174:177], v[206:209], v[24:27]
	v_mfma_f32_16x16x32_bf16 v[52:55], v[170:173], v[186:189], v[52:55]
	v_mfma_f32_16x16x32_bf16 v[48:51], v[178:181], v[186:189], v[48:51]
	v_mfma_f32_16x16x32_bf16 v[28:31], v[170:173], v[194:197], v[28:31]
	v_mfma_f32_16x16x32_bf16 v[12:15], v[178:181], v[194:197], v[12:15]
	v_mfma_f32_16x16x32_bf16 v[36:39], v[170:173], v[202:205], v[36:39]
	v_mfma_f32_16x16x32_bf16 v[40:43], v[178:181], v[202:205], v[40:43]
	v_mfma_f32_16x16x32_bf16 v[20:23], v[170:173], v[210:213], v[20:23]
	v_mfma_f32_16x16x32_bf16 v[24:27], v[178:181], v[210:213], v[24:27]
	s_barrier
; #define PG8_STAGE(bufoff, gbase, voff) do { _Pragma("unroll") for (int _i = 0; _i < 2; ++_i) \
;         __builtin_amdgcn_global_load_lds((const __attribute__((address_space(1))) unsigned*)((const __attribute__((address_space(1))) char*)(gbase) + (unsigned)lnd_v((int)(voff)[_i])), (LAS unsigned*)(lds + (bufoff) + ldsw + _i * 8192), 16, 0, 0); } while (0)
; #define PG8_LDA(dst, b, h) do { _Pragma("unroll") for (int m = 0; m < 4; ++m) _Pragma("unroll") for (int k = 0; k < 2; ++k) dst[m][k] = *(const LAS bf16x8*)(lds + PG8_SA(b, h) + aoff + m * 2048 + k * 1024); } while (0)
; #define PG8_LDB(dst, b, h) do { _Pragma("unroll") for (int n = 0; n < 2; ++n) _Pragma("unroll") for (int k = 0; k < 2; ++k) dst[n][k] = *(const LAS bf16x8*)(lds + PG8_SB(b, h) + boff + n * 2048 + k * 1024); } while (0)
; #define PG8_MMA(ai, bj, At, Bt) do { __builtin_amdgcn_s_setprio(1); _Pragma("unroll") for (int m = 0; m < 4; ++m) _Pragma("unroll") for (int n = 0; n < 2; ++n) _Pragma("unroll") for (int k = 0; k < 2; ++k) \
;         acc[ai][bj][m][n] = __builtin_amdgcn_mfma_f32_16x16x32_bf16(Bt[n][k], At[m][k], acc[ai][bj][m][n], 0, 0, 0); __builtin_amdgcn_s_setprio(0); } while (0)
; #define PG8_WAIT_V(n) asm volatile("s_waitcnt vmcnt(" #n ")" ::: "memory")
; #define PG8_WAIT_L(n) asm volatile("s_waitcnt lgkmcnt(" #n ")" ::: "memory")
; #define PG8_BAR __builtin_amdgcn_s_barrier()
; #define PG8_SCHED __builtin_amdgcn_sched_barrier(0)
; template <class Desc, class Epi>
; __device__ __forceinline__ void gemm_phase(const int wv_, LAS unsigned char* lds, const Desc& d, const Epi& E) {
;     ...
;             PG8_LDB(B0, 1, 0); PG8_LDB(B1, 1, 1); PG8_SCHED; PG8_LDA(At, 1, 0); PG8_STAGE(PG8_SA(0, 1), a2, sA1);
;             PG8_WAIT_V(8); PG8_WAIT_L(0); PG8_BAR; PG8_MMA(0, 0, At, B0); PG8_MMA(0, 1, At, B1); PG8_BAR; PG8_SCHED;
	s_add_i32 s63, 0, 0x18000
	v_add_u32_e32 v96, s63, v139
	s_add_i32 s64, 0, 0x1c000
	ds_read_b128 v[150:153], v96
	ds_read_b128 v[154:157], v96 offset:1024
	ds_read_b128 v[158:161], v96 offset:2048
	ds_read_b128 v[162:165], v96 offset:3072
	v_add_u32_e32 v96, s64, v139
	ds_read_b128 v[166:169], v96
	ds_read_b128 v[170:173], v96 offset:1024
	ds_read_b128 v[174:177], v96 offset:2048
	ds_read_b128 v[178:181], v96 offset:3072
	s_mov_b32 m0, s57
	ds_read_b128 v[182:185], v149 offset:32768
	ds_read_b128 v[186:189], v149 offset:33792
	ds_read_b128 v[190:193], v149 offset:34816
	ds_read_b128 v[194:197], v149 offset:35840
	ds_read_b128 v[198:201], v149 offset:36864
	ds_read_b128 v[202:205], v149 offset:37888
	ds_read_b128 v[206:209], v149 offset:38912
	ds_read_b128 v[210:213], v149 offset:39936
	s_nop 0
	global_load_lds_dwordx4 v133, s[4:5]
	s_mov_b32 m0, s58
	s_nop 0
	global_load_lds_dwordx4 v136, s[4:5]
	s_waitcnt vmcnt(8)
	s_waitcnt lgkmcnt(0)
	s_barrier
	v_mfma_f32_16x16x32_bf16 v[126:129], v[150:153], v[182:185], v[126:129]
	v_mfma_f32_16x16x32_bf16 v[122:125], v[158:161], v[182:185], v[122:125]
	v_mfma_f32_16x16x32_bf16 v[110:113], v[150:153], v[190:193], v[110:113]
	v_mfma_f32_16x16x32_bf16 v[106:109], v[158:161], v[190:193], v[106:109]
	v_mfma_f32_16x16x32_bf16 v[92:95], v[150:153], v[198:201], v[92:95]
	v_mfma_f32_16x16x32_bf16 v[88:91], v[158:161], v[198:201], v[88:91]
	v_mfma_f32_16x16x32_bf16 v[76:79], v[150:153], v[206:209], v[76:79]
	v_mfma_f32_16x16x32_bf16 v[72:75], v[158:161], v[206:209], v[72:75]
	v_mfma_f32_16x16x32_bf16 v[126:129], v[154:157], v[186:189], v[126:129]
	v_mfma_f32_16x16x32_bf16 v[122:125], v[162:165], v[186:189], v[122:125]
	v_mfma_f32_16x16x32_bf16 v[110:113], v[154:157], v[194:197], v[110:113]
	v_mfma_f32_16x16x32_bf16 v[106:109], v[162:165], v[194:197], v[106:109]
	v_mfma_f32_16x16x32_bf16 v[92:95], v[154:157], v[202:205], v[92:95]
	v_mfma_f32_16x16x32_bf16 v[88:91], v[162:165], v[202:205], v[88:91]
	v_mfma_f32_16x16x32_bf16 v[76:79], v[154:157], v[210:213], v[76:79]
	v_mfma_f32_16x16x32_bf16 v[72:75], v[162:165], v[210:213], v[72:75]
	v_mfma_f32_16x16x32_bf16 v[118:121], v[166:169], v[182:185], v[118:121]
	v_mfma_f32_16x16x32_bf16 v[114:117], v[174:177], v[182:185], v[114:117]
	v_mfma_f32_16x16x32_bf16 v[102:105], v[166:169], v[190:193], v[102:105]
	v_mfma_f32_16x16x32_bf16 v[98:101], v[174:177], v[190:193], v[98:101]
	v_mfma_f32_16x16x32_bf16 v[84:87], v[166:169], v[198:201], v[84:87]
	v_mfma_f32_16x16x32_bf16 v[80:83], v[174:177], v[198:201], v[80:83]
	v_mfma_f32_16x16x32_bf16 v[68:71], v[166:169], v[206:209], v[68:71]
	v_mfma_f32_16x16x32_bf16 v[64:67], v[174:177], v[206:209], v[64:67]
	v_mfma_f32_16x16x32_bf16 v[118:121], v[170:173], v[186:189], v[118:121]
	v_mfma_f32_16x16x32_bf16 v[114:117], v[178:181], v[186:189], v[114:117]
	v_mfma_f32_16x16x32_bf16 v[102:105], v[170:173], v[194:197], v[102:105]
	v_mfma_f32_16x16x32_bf16 v[98:101], v[178:181], v[194:197], v[98:101]
	v_mfma_f32_16x16x32_bf16 v[84:87], v[170:173], v[202:205], v[84:87]
	v_mfma_f32_16x16x32_bf16 v[80:83], v[178:181], v[202:205], v[80:83]
	v_mfma_f32_16x16x32_bf16 v[68:71], v[170:173], v[210:213], v[68:71]
	v_mfma_f32_16x16x32_bf16 v[64:67], v[178:181], v[210:213], v[64:67]
	s_barrier
; #define PG8_STAGE(bufoff, gbase, voff) do { _Pragma("unroll") for (int _i = 0; _i < 2; ++_i) \
;         __builtin_amdgcn_global_load_lds((const __attribute__((address_space(1))) unsigned*)((const __attribute__((address_space(1))) char*)(gbase) + (unsigned)lnd_v((int)(voff)[_i])), (LAS unsigned*)(lds + (bufoff) + ldsw + _i * 8192), 16, 0, 0); } while (0)
; #define PG8_LDA(dst, b, h) do { _Pragma("unroll") for (int m = 0; m < 4; ++m) _Pragma("unroll") for (int k = 0; k < 2; ++k) dst[m][k] = *(const LAS bf16x8*)(lds + PG8_SA(b, h) + aoff + m * 2048 + k * 1024); } while (0)
; #define PG8_MMA(ai, bj, At, Bt) do { __builtin_amdgcn_s_setprio(1); _Pragma("unroll") for (int m = 0; m < 4; ++m) _Pragma("unroll") for (int n = 0; n < 2; ++n) _Pragma("unroll") for (int k = 0; k < 2; ++k) \
;         acc[ai][bj][m][n] = __builtin_amdgcn_mfma_f32_16x16x32_bf16(Bt[n][k], At[m][k], acc[ai][bj][m][n], 0, 0, 0); __builtin_amdgcn_s_setprio(0); } while (0)
; #define PG8_WAIT_V(n) asm volatile("s_waitcnt vmcnt(" #n ")" ::: "memory")
; #define PG8_WAIT_L(n) asm volatile("s_waitcnt lgkmcnt(" #n ")" ::: "memory")
; #define PG8_BAR __builtin_amdgcn_s_barrier()
; #define PG8_SCHED __builtin_amdgcn_sched_barrier(0)
; template <class Desc, class Epi>
; __device__ __forceinline__ void gemm_phase(const int wv_, LAS unsigned char* lds, const Desc& d, const Epi& E) {
;     ...
;             PG8_LDA(At, 1, 1); PG8_STAGE(PG8_SB(1, 0), b3, voffB); PG8_STAGE(PG8_SB(1, 1), b3 + hstepB, voffB); PG8_STAGE(PG8_SA(1, 0), a3, sA0);
;             PG8_WAIT_V(8); PG8_WAIT_L(0); PG8_BAR; PG8_MMA(1, 0, At, B0); PG8_MMA(1, 1, At, B1); PG8_BAR; PG8_SCHED;
;         }
;         if (wr == 0) PG8_BAR;
	v_mov_b32_e32 v96, v134
	ds_read_b128 v[182:185], v149 offset:49152
	ds_read_b128 v[186:189], v149 offset:50176
	ds_read_b128 v[190:193], v149 offset:51200
	ds_read_b128 v[194:197], v149 offset:52224
	ds_read_b128 v[198:201], v149 offset:53248
	ds_read_b128 v[202:205], v149 offset:54272
	ds_read_b128 v[206:209], v149 offset:55296
	ds_read_b128 v[210:213], v149 offset:56320
	s_add_i32 s63, s63, s54
	v_lshl_add_u64 v[130:131], s[20:21], 0, v[96:97]
	v_lshl_add_u64 v[130:131], v[130:131], 0, s[30:31]
	s_mov_b32 m0, s63
	v_mov_b32_e32 v96, v137
	global_load_lds_dwordx4 v[130:131], off
	s_add_i32 m0, s63, 0x2000
	s_nop 0
	v_lshl_add_u64 v[130:131], s[20:21], 0, v[96:97]
	s_add_u32 s20, s20, 0x40080
	v_lshl_add_u64 v[130:131], v[130:131], 0, s[30:31]
	s_addc_u32 s21, s21, 0
	s_add_i32 s63, s64, s54
	global_load_lds_dwordx4 v[130:131], off
	s_mov_b32 m0, s63
	s_nop 0
	global_load_lds_dwordx4 v134, s[20:21]
	s_add_i32 m0, s63, 0x2000
	s_nop 0
	global_load_lds_dwordx4 v137, s[20:21]
	v_mov_b32_e32 v96, v132
	s_mov_b32 m0, s59
	v_lshl_add_u64 v[130:131], s[4:5], 0, v[96:97]
	v_lshl_add_u64 v[130:131], v[130:131], 0, s[30:31]
	v_mov_b32_e32 v96, v135
	global_load_lds_dwordx4 v[130:131], off
	s_mov_b32 m0, s60
	v_lshl_add_u64 v[130:131], s[4:5], 0, v[96:97]
	v_lshl_add_u64 v[130:131], v[130:131], 0, s[30:31]
	global_load_lds_dwordx4 v[130:131], off
	s_waitcnt vmcnt(8)
	s_waitcnt lgkmcnt(0)
	s_barrier
	v_mfma_f32_16x16x32_bf16 v[60:63], v[150:153], v[182:185], v[60:63]
	v_mfma_f32_16x16x32_bf16 v[56:59], v[158:161], v[182:185], v[56:59]
	v_mfma_f32_16x16x32_bf16 v[44:47], v[150:153], v[190:193], v[44:47]
	v_mfma_f32_16x16x32_bf16 v[32:35], v[158:161], v[190:193], v[32:35]
	v_mfma_f32_16x16x32_bf16 v[16:19], v[150:153], v[198:201], v[16:19]
	v_mfma_f32_16x16x32_bf16 v[8:11], v[158:161], v[198:201], v[8:11]
	v_mfma_f32_16x16x32_bf16 v[4:7], v[150:153], v[206:209], v[4:7]
	v_mfma_f32_16x16x32_bf16 v[0:3], v[158:161], v[206:209], v[0:3]
	v_mfma_f32_16x16x32_bf16 v[60:63], v[154:157], v[186:189], v[60:63]
	v_mfma_f32_16x16x32_bf16 v[56:59], v[162:165], v[186:189], v[56:59]
	v_mfma_f32_16x16x32_bf16 v[44:47], v[154:157], v[194:197], v[44:47]
	v_mfma_f32_16x16x32_bf16 v[32:35], v[162:165], v[194:197], v[32:35]
	v_mfma_f32_16x16x32_bf16 v[16:19], v[154:157], v[202:205], v[16:19]
	v_mfma_f32_16x16x32_bf16 v[8:11], v[162:165], v[202:205], v[8:11]
	v_mfma_f32_16x16x32_bf16 v[4:7], v[154:157], v[210:213], v[4:7]
	v_mfma_f32_16x16x32_bf16 v[0:3], v[162:165], v[210:213], v[0:3]
	v_mfma_f32_16x16x32_bf16 v[52:55], v[166:169], v[182:185], v[52:55]
	v_mfma_f32_16x16x32_bf16 v[48:51], v[174:177], v[182:185], v[48:51]
	v_mfma_f32_16x16x32_bf16 v[28:31], v[166:169], v[190:193], v[28:31]
	v_mfma_f32_16x16x32_bf16 v[12:15], v[174:177], v[190:193], v[12:15]
	v_mfma_f32_16x16x32_bf16 v[36:39], v[166:169], v[198:201], v[36:39]
	v_mfma_f32_16x16x32_bf16 v[40:43], v[174:177], v[198:201], v[40:43]
	v_mfma_f32_16x16x32_bf16 v[20:23], v[166:169], v[206:209], v[20:23]
	v_mfma_f32_16x16x32_bf16 v[24:27], v[174:177], v[206:209], v[24:27]
	v_mfma_f32_16x16x32_bf16 v[52:55], v[170:173], v[186:189], v[52:55]
	v_mfma_f32_16x16x32_bf16 v[48:51], v[178:181], v[186:189], v[48:51]
	v_mfma_f32_16x16x32_bf16 v[28:31], v[170:173], v[194:197], v[28:31]
	v_mfma_f32_16x16x32_bf16 v[12:15], v[178:181], v[194:197], v[12:15]
	v_mfma_f32_16x16x32_bf16 v[36:39], v[170:173], v[202:205], v[36:39]
	v_mfma_f32_16x16x32_bf16 v[40:43], v[178:181], v[202:205], v[40:43]
	v_mfma_f32_16x16x32_bf16 v[20:23], v[170:173], v[210:213], v[20:23]
	v_mfma_f32_16x16x32_bf16 v[24:27], v[178:181], v[210:213], v[24:27]
	s_barrier
	s_add_i32 s45, s45, 2
	s_add_u32 s2, s2, 0x100
	s_addc_u32 s3, s3, 0
	s_add_u32 s29, s29, 0x100
	s_addc_u32 s43, s43, 0
	s_cmp_gt_u32 s45, 13
	s_cbranch_scc0 .LBB0_747
	s_and_b64 vcc, exec, s[40:41]
	s_cbranch_vccz .LBB0_750
	s_barrier

; #define PG8_STAGE(bufoff, gbase, voff) do { _Pragma("unroll") for (int _i = 0; _i < 2; ++_i) \
;         __builtin_amdgcn_global_load_lds((const __attribute__((address_space(1))) unsigned*)((const __attribute__((address_space(1))) char*)(gbase) + (unsigned)lnd_v((int)(voff)[_i])), (LAS unsigned*)(lds + (bufoff) + ldsw + _i * 8192), 16, 0, 0); } while (0)
; #define PG8_LDA(dst, b, h) do { _Pragma("unroll") for (int m = 0; m < 4; ++m) _Pragma("unroll") for (int k = 0; k < 2; ++k) dst[m][k] = *(const LAS bf16x8*)(lds + PG8_SA(b, h) + aoff + m * 2048 + k * 1024); } while (0)
; #define PG8_LDB(dst, b, h) do { _Pragma("unroll") for (int n = 0; n < 2; ++n) _Pragma("unroll") for (int k = 0; k < 2; ++k) dst[n][k] = *(const LAS bf16x8*)(lds + PG8_SB(b, h) + boff + n * 2048 + k * 1024); } while (0)
; #define PG8_MMA(ai, bj, At, Bt) do { __builtin_amdgcn_s_setprio(1); _Pragma("unroll") for (int m = 0; m < 4; ++m) _Pragma("unroll") for (int n = 0; n < 2; ++n) _Pragma("unroll") for (int k = 0; k < 2; ++k) \
;         acc[ai][bj][m][n] = __builtin_amdgcn_mfma_f32_16x16x32_bf16(Bt[n][k], At[m][k], acc[ai][bj][m][n], 0, 0, 0); __builtin_amdgcn_s_setprio(0); } while (0)
; #define PG8_WAIT_V(n) asm volatile("s_waitcnt vmcnt(" #n ")" ::: "memory")
; #define PG8_WAIT_L(n) asm volatile("s_waitcnt lgkmcnt(" #n ")" ::: "memory")
; #define PG8_BAR __builtin_amdgcn_s_barrier()
; #define PG8_SCHED __builtin_amdgcn_sched_barrier(0)
; template <class Desc, class Epi>
; __device__ __forceinline__ void gemm_phase(const int wv_, LAS unsigned char* lds, const Desc& d, const Epi& E) {
;     ...
;             PG8_LDB(B0, 0, 0); PG8_LDB(B1, 0, 1); PG8_SCHED; PG8_LDA(At, 0, 0); PG8_STAGE(PG8_SA(1, 1), a1, voffA1);
;             PG8_WAIT_V(8); PG8_WAIT_L(0); PG8_BAR; PG8_MMA(0, 0, At, B0); PG8_MMA(0, 1, At, B1); PG8_BAR; PG8_SCHED;
;             PG8_LDA(At, 0, 1); PG8_STAGE(PG8_SB(0, 0), b2, voffB); PG8_STAGE(PG8_SB(0, 1), b2 + hstepB, voffB); PG8_STAGE(PG8_SA(0, 0), a2, sA0);
;             PG8_WAIT_V(8); PG8_WAIT_L(0); PG8_BAR; PG8_MMA(1, 0, At, B0); PG8_MMA(1, 1, At, B1); PG8_BAR; PG8_SCHED;
.LBB0_890:
	s_add_u32 s60, s58, s22
	s_addc_u32 s61, s59, 0
	s_add_u32 s23, s60, 0x100
	s_addc_u32 s24, s61, 0
	s_and_b64 s[4:5], s[20:21], exec
	s_cselect_b32 s4, s50, s23
	s_cselect_b32 s5, s51, s24
	s_add_u32 s22, s56, s22
	s_addc_u32 s23, s57, 0
	s_add_u32 s22, s22, 0x100
	s_addc_u32 s23, s23, 0
	s_add_i32 s82, 0, 0x10000
	s_and_b64 s[20:21], s[20:21], exec
	s_cselect_b32 s21, s53, s23
	s_cselect_b32 s20, s52, s22
	s_add_i32 s23, 0, 0x14000
	v_add_u32_e32 v96, s82, v210
	s_add_i32 s84, s82, s68
	ds_read_b128 v[130:133], v96
	ds_read_b128 v[134:137], v96 offset:1024
	ds_read_b128 v[138:141], v96 offset:2048
	ds_read_b128 v[142:145], v96 offset:3072
	v_add_u32_e32 v96, s23, v210
	s_add_i32 m0, s69, 0xc000
	s_add_i32 s85, s69, 0xe000
	s_add_i32 s80, s84, 0x2000
	ds_read_b128 v[146:149], v96
	ds_read_b128 v[150:153], v96 offset:1024
	ds_read_b128 v[154:157], v96 offset:2048
	ds_read_b128 v[158:161], v96 offset:3072
	s_add_u32 s24, s20, 0x10000
	s_addc_u32 s25, s21, 0
	s_add_i32 s78, 0, 0x18000
	s_add_i32 s81, s23, s68
	s_add_i32 s47, s78, s68
	s_add_i32 s79, s81, 0x2000
	s_add_i32 s49, 0, 0x1c000
	s_add_i32 s29, s47, 0x2000
	s_add_u32 s22, s20, 0x10080
	s_addc_u32 s23, s21, 0
	s_add_i32 s83, s49, s68
	s_add_i32 s82, s83, 0x2000
	v_mov_b32_e32 v96, v204
	ds_read_b128 v[162:165], v222
	ds_read_b128 v[166:169], v222 offset:1024
	ds_read_b128 v[170:173], v222 offset:2048
	ds_read_b128 v[174:177], v222 offset:3072
	ds_read_b128 v[178:181], v222 offset:4096
	ds_read_b128 v[182:185], v222 offset:5120
	ds_read_b128 v[188:191], v222 offset:6144
	ds_read_b128 v[192:195], v222 offset:7168
	s_nop 0
	v_lshl_add_u64 v[196:197], s[60:61], 0, v[96:97]
	v_lshl_add_u64 v[196:197], v[196:197], 0, s[30:31]
	v_mov_b32_e32 v96, v207
	global_load_lds_dwordx4 v[196:197], off
	s_mov_b32 m0, s85
	v_lshl_add_u64 v[196:197], s[60:61], 0, v[96:97]
	v_lshl_add_u64 v[196:197], v[196:197], 0, s[30:31]
	global_load_lds_dwordx4 v[196:197], off
	s_waitcnt vmcnt(8)
	s_waitcnt lgkmcnt(0)
	s_barrier
	v_mfma_f32_16x16x32_bf16 v[126:129], v[130:133], v[162:165], v[126:129]
	v_mfma_f32_16x16x32_bf16 v[122:125], v[138:141], v[162:165], v[122:125]
	v_mfma_f32_16x16x32_bf16 v[118:121], v[130:133], v[170:173], v[118:121]
	v_mfma_f32_16x16x32_bf16 v[114:117], v[138:141], v[170:173], v[114:117]
	v_mfma_f32_16x16x32_bf16 v[110:113], v[130:133], v[178:181], v[110:113]
	v_mfma_f32_16x16x32_bf16 v[106:109], v[138:141], v[178:181], v[106:109]
	v_mfma_f32_16x16x32_bf16 v[102:105], v[130:133], v[188:191], v[102:105]
	v_mfma_f32_16x16x32_bf16 v[98:101], v[138:141], v[188:191], v[98:101]
	v_mfma_f32_16x16x32_bf16 v[126:129], v[134:137], v[166:169], v[126:129]
	v_mfma_f32_16x16x32_bf16 v[122:125], v[142:145], v[166:169], v[122:125]
	v_mfma_f32_16x16x32_bf16 v[118:121], v[134:137], v[174:177], v[118:121]
	v_mfma_f32_16x16x32_bf16 v[114:117], v[142:145], v[174:177], v[114:117]
	v_mfma_f32_16x16x32_bf16 v[110:113], v[134:137], v[182:185], v[110:113]
	v_mfma_f32_16x16x32_bf16 v[106:109], v[142:145], v[182:185], v[106:109]
	v_mfma_f32_16x16x32_bf16 v[102:105], v[134:137], v[192:195], v[102:105]
	v_mfma_f32_16x16x32_bf16 v[98:101], v[142:145], v[192:195], v[98:101]
	v_mfma_f32_16x16x32_bf16 v[60:63], v[146:149], v[162:165], v[60:63]
	v_mfma_f32_16x16x32_bf16 v[56:59], v[154:157], v[162:165], v[56:59]
	v_mfma_f32_16x16x32_bf16 v[52:55], v[146:149], v[170:173], v[52:55]
	v_mfma_f32_16x16x32_bf16 v[48:51], v[154:157], v[170:173], v[48:51]
	v_mfma_f32_16x16x32_bf16 v[44:47], v[146:149], v[178:181], v[44:47]
	v_mfma_f32_16x16x32_bf16 v[40:43], v[154:157], v[178:181], v[40:43]
	v_mfma_f32_16x16x32_bf16 v[36:39], v[146:149], v[188:191], v[36:39]
	v_mfma_f32_16x16x32_bf16 v[32:35], v[154:157], v[188:191], v[32:35]
	v_mfma_f32_16x16x32_bf16 v[60:63], v[150:153], v[166:169], v[60:63]
	v_mfma_f32_16x16x32_bf16 v[56:59], v[158:161], v[166:169], v[56:59]
	v_mfma_f32_16x16x32_bf16 v[52:55], v[150:153], v[174:177], v[52:55]
	v_mfma_f32_16x16x32_bf16 v[48:51], v[158:161], v[174:177], v[48:51]
	v_mfma_f32_16x16x32_bf16 v[44:47], v[150:153], v[182:185], v[44:47]
	v_mfma_f32_16x16x32_bf16 v[40:43], v[158:161], v[182:185], v[40:43]
	v_mfma_f32_16x16x32_bf16 v[36:39], v[150:153], v[192:195], v[36:39]
	v_mfma_f32_16x16x32_bf16 v[32:35], v[158:161], v[192:195], v[32:35]
	s_barrier
	s_mov_b32 m0, s84
	ds_read_b128 v[162:165], v222 offset:16384
	ds_read_b128 v[166:169], v222 offset:17408
	ds_read_b128 v[170:173], v222 offset:18432
	ds_read_b128 v[174:177], v222 offset:19456
	ds_read_b128 v[178:181], v222 offset:20480
	ds_read_b128 v[182:185], v222 offset:21504
	ds_read_b128 v[188:191], v222 offset:22528
	ds_read_b128 v[192:195], v222 offset:23552
	s_nop 0
	global_load_lds_dwordx4 v205, s[20:21]
	s_mov_b32 m0, s80
	s_nop 0
	global_load_lds_dwordx4 v208, s[20:21]
	s_mov_b32 m0, s81
	s_nop 0
	global_load_lds_dwordx4 v205, s[24:25]
	s_mov_b32 m0, s79
	s_nop 0
	global_load_lds_dwordx4 v208, s[24:25]
	s_mov_b32 m0, s69
	s_nop 0
	global_load_lds_dwordx4 v187, s[4:5]
	s_mov_b32 m0, s70
	s_nop 0
	global_load_lds_dwordx4 v206, s[4:5]
	s_waitcnt vmcnt(8)
	s_waitcnt lgkmcnt(0)
	s_barrier
; #define PG8_STAGE(bufoff, gbase, voff) do { _Pragma("unroll") for (int _i = 0; _i < 2; ++_i) \
;         __builtin_amdgcn_global_load_lds((const __attribute__((address_space(1))) unsigned*)((const __attribute__((address_space(1))) char*)(gbase) + (unsigned)lnd_v((int)(voff)[_i])), (LAS unsigned*)(lds + (bufoff) + ldsw + _i * 8192), 16, 0, 0); } while (0)
; #define PG8_LDA(dst, b, h) do { _Pragma("unroll") for (int m = 0; m < 4; ++m) _Pragma("unroll") for (int k = 0; k < 2; ++k) dst[m][k] = *(const LAS bf16x8*)(lds + PG8_SA(b, h) + aoff + m * 2048 + k * 1024); } while (0)
; #define PG8_LDB(dst, b, h) do { _Pragma("unroll") for (int n = 0; n < 2; ++n) _Pragma("unroll") for (int k = 0; k < 2; ++k) dst[n][k] = *(const LAS bf16x8*)(lds + PG8_SB(b, h) + boff + n * 2048 + k * 1024); } while (0)
; #define PG8_MMA(ai, bj, At, Bt) do { __builtin_amdgcn_s_setprio(1); _Pragma("unroll") for (int m = 0; m < 4; ++m) _Pragma("unroll") for (int n = 0; n < 2; ++n) _Pragma("unroll") for (int k = 0; k < 2; ++k) \
;         acc[ai][bj][m][n] = __builtin_amdgcn_mfma_f32_16x16x32_bf16(Bt[n][k], At[m][k], acc[ai][bj][m][n], 0, 0, 0); __builtin_amdgcn_s_setprio(0); } while (0)
; #define PG8_WAIT_V(n) asm volatile("s_waitcnt vmcnt(" #n ")" ::: "memory")
; #define PG8_WAIT_L(n) asm volatile("s_waitcnt lgkmcnt(" #n ")" ::: "memory")
; #define PG8_BAR __builtin_amdgcn_s_barrier()
; #define PG8_SCHED __builtin_amdgcn_sched_barrier(0)
; template <class Desc, class Epi>
; __device__ __forceinline__ void gemm_phase(const int wv_, LAS unsigned char* lds, const Desc& d, const Epi& E) {
;     ...
;             PG8_WAIT_V(8); PG8_WAIT_L(0); PG8_BAR; PG8_MMA(1, 0, At, B0); PG8_MMA(1, 1, At, B1); PG8_BAR; PG8_SCHED;
;             PG8_LDB(B0, 1, 0); PG8_LDB(B1, 1, 1); PG8_SCHED; PG8_LDA(At, 1, 0); PG8_STAGE(PG8_SA(0, 1), a2, sA1);
;             PG8_WAIT_V(8); PG8_WAIT_L(0); PG8_BAR; PG8_MMA(0, 0, At, B0); PG8_MMA(0, 1, At, B1); PG8_BAR; PG8_SCHED;
	v_mfma_f32_16x16x32_bf16 v[92:95], v[130:133], v[162:165], v[92:95]
	v_mfma_f32_16x16x32_bf16 v[88:91], v[138:141], v[162:165], v[88:91]
	v_mfma_f32_16x16x32_bf16 v[84:87], v[130:133], v[170:173], v[84:87]
	v_mfma_f32_16x16x32_bf16 v[80:83], v[138:141], v[170:173], v[80:83]
	v_mfma_f32_16x16x32_bf16 v[76:79], v[130:133], v[178:181], v[76:79]
	v_mfma_f32_16x16x32_bf16 v[72:75], v[138:141], v[178:181], v[72:75]
	v_mfma_f32_16x16x32_bf16 v[68:71], v[130:133], v[188:191], v[68:71]
	v_mfma_f32_16x16x32_bf16 v[64:67], v[138:141], v[188:191], v[64:67]
	v_mfma_f32_16x16x32_bf16 v[92:95], v[134:137], v[166:169], v[92:95]
	v_mfma_f32_16x16x32_bf16 v[88:91], v[142:145], v[166:169], v[88:91]
	v_mfma_f32_16x16x32_bf16 v[84:87], v[134:137], v[174:177], v[84:87]
	v_mfma_f32_16x16x32_bf16 v[80:83], v[142:145], v[174:177], v[80:83]
	v_mfma_f32_16x16x32_bf16 v[76:79], v[134:137], v[182:185], v[76:79]
	v_mfma_f32_16x16x32_bf16 v[72:75], v[142:145], v[182:185], v[72:75]
	v_mfma_f32_16x16x32_bf16 v[68:71], v[134:137], v[192:195], v[68:71]
	v_mfma_f32_16x16x32_bf16 v[64:67], v[142:145], v[192:195], v[64:67]
	v_mfma_f32_16x16x32_bf16 v[28:31], v[146:149], v[162:165], v[28:31]
	v_mfma_f32_16x16x32_bf16 v[24:27], v[154:157], v[162:165], v[24:27]
	v_mfma_f32_16x16x32_bf16 v[12:15], v[146:149], v[170:173], v[12:15]
	v_mfma_f32_16x16x32_bf16 v[8:11], v[154:157], v[170:173], v[8:11]
	v_mfma_f32_16x16x32_bf16 v[20:23], v[146:149], v[178:181], v[20:23]
	v_mfma_f32_16x16x32_bf16 v[16:19], v[154:157], v[178:181], v[16:19]
	v_mfma_f32_16x16x32_bf16 v[4:7], v[146:149], v[188:191], v[4:7]
	v_mfma_f32_16x16x32_bf16 v[0:3], v[154:157], v[188:191], v[0:3]
	v_mfma_f32_16x16x32_bf16 v[28:31], v[150:153], v[166:169], v[28:31]
	v_mfma_f32_16x16x32_bf16 v[24:27], v[158:161], v[166:169], v[24:27]
	v_mfma_f32_16x16x32_bf16 v[12:15], v[150:153], v[174:177], v[12:15]
	v_mfma_f32_16x16x32_bf16 v[8:11], v[158:161], v[174:177], v[8:11]
	v_mfma_f32_16x16x32_bf16 v[20:23], v[150:153], v[182:185], v[20:23]
	v_mfma_f32_16x16x32_bf16 v[16:19], v[158:161], v[182:185], v[16:19]
	v_mfma_f32_16x16x32_bf16 v[4:7], v[150:153], v[192:195], v[4:7]
	v_mfma_f32_16x16x32_bf16 v[0:3], v[158:161], v[192:195], v[0:3]
	s_barrier
	v_add_u32_e32 v96, s78, v210
	ds_read_b128 v[130:133], v96
	ds_read_b128 v[134:137], v96 offset:1024
	ds_read_b128 v[138:141], v96 offset:2048
	ds_read_b128 v[142:145], v96 offset:3072
	v_add_u32_e32 v96, s49, v210
	ds_read_b128 v[146:149], v96
	ds_read_b128 v[150:153], v96 offset:1024
	ds_read_b128 v[154:157], v96 offset:2048
	ds_read_b128 v[158:161], v96 offset:3072
	s_mov_b32 m0, s71
	ds_read_b128 v[162:165], v222 offset:32768
	ds_read_b128 v[166:169], v222 offset:33792
	ds_read_b128 v[170:173], v222 offset:34816
	ds_read_b128 v[174:177], v222 offset:35840
	ds_read_b128 v[178:181], v222 offset:36864
	ds_read_b128 v[182:185], v222 offset:37888
	ds_read_b128 v[188:191], v222 offset:38912
	ds_read_b128 v[192:195], v222 offset:39936
	s_nop 0
	global_load_lds_dwordx4 v204, s[4:5]
	s_mov_b32 m0, s72
	s_nop 0
	global_load_lds_dwordx4 v207, s[4:5]
	s_waitcnt vmcnt(8)
	s_waitcnt lgkmcnt(0)
	s_barrier
	v_mfma_f32_16x16x32_bf16 v[126:129], v[130:133], v[162:165], v[126:129]
	v_mfma_f32_16x16x32_bf16 v[122:125], v[138:141], v[162:165], v[122:125]
	v_mfma_f32_16x16x32_bf16 v[118:121], v[130:133], v[170:173], v[118:121]
	v_mfma_f32_16x16x32_bf16 v[114:117], v[138:141], v[170:173], v[114:117]
	v_mfma_f32_16x16x32_bf16 v[110:113], v[130:133], v[178:181], v[110:113]
	v_mfma_f32_16x16x32_bf16 v[106:109], v[138:141], v[178:181], v[106:109]
	v_mfma_f32_16x16x32_bf16 v[102:105], v[130:133], v[188:191], v[102:105]
	v_mfma_f32_16x16x32_bf16 v[98:101], v[138:141], v[188:191], v[98:101]
	v_mfma_f32_16x16x32_bf16 v[126:129], v[134:137], v[166:169], v[126:129]
	v_mfma_f32_16x16x32_bf16 v[122:125], v[142:145], v[166:169], v[122:125]
	v_mfma_f32_16x16x32_bf16 v[118:121], v[134:137], v[174:177], v[118:121]
	v_mfma_f32_16x16x32_bf16 v[114:117], v[142:145], v[174:177], v[114:117]
	v_mfma_f32_16x16x32_bf16 v[110:113], v[134:137], v[182:185], v[110:113]
	v_mfma_f32_16x16x32_bf16 v[106:109], v[142:145], v[182:185], v[106:109]
	v_mfma_f32_16x16x32_bf16 v[102:105], v[134:137], v[192:195], v[102:105]
	v_mfma_f32_16x16x32_bf16 v[98:101], v[142:145], v[192:195], v[98:101]
	v_mfma_f32_16x16x32_bf16 v[60:63], v[146:149], v[162:165], v[60:63]
	v_mfma_f32_16x16x32_bf16 v[56:59], v[154:157], v[162:165], v[56:59]
	v_mfma_f32_16x16x32_bf16 v[52:55], v[146:149], v[170:173], v[52:55]
	v_mfma_f32_16x16x32_bf16 v[48:51], v[154:157], v[170:173], v[48:51]
	v_mfma_f32_16x16x32_bf16 v[44:47], v[146:149], v[178:181], v[44:47]
	v_mfma_f32_16x16x32_bf16 v[40:43], v[154:157], v[178:181], v[40:43]
	v_mfma_f32_16x16x32_bf16 v[36:39], v[146:149], v[188:191], v[36:39]
	v_mfma_f32_16x16x32_bf16 v[32:35], v[154:157], v[188:191], v[32:35]
	v_mfma_f32_16x16x32_bf16 v[60:63], v[150:153], v[166:169], v[60:63]
	v_mfma_f32_16x16x32_bf16 v[56:59], v[158:161], v[166:169], v[56:59]
	v_mfma_f32_16x16x32_bf16 v[52:55], v[150:153], v[174:177], v[52:55]
	v_mfma_f32_16x16x32_bf16 v[48:51], v[158:161], v[174:177], v[48:51]
	v_mfma_f32_16x16x32_bf16 v[44:47], v[150:153], v[182:185], v[44:47]
	v_mfma_f32_16x16x32_bf16 v[40:43], v[158:161], v[182:185], v[40:43]
	v_mfma_f32_16x16x32_bf16 v[36:39], v[150:153], v[192:195], v[36:39]
	v_mfma_f32_16x16x32_bf16 v[32:35], v[158:161], v[192:195], v[32:35]
	s_barrier
; #define PG8_STAGE(bufoff, gbase, voff) do { _Pragma("unroll") for (int _i = 0; _i < 2; ++_i) \
;         __builtin_amdgcn_global_load_lds((const __attribute__((address_space(1))) unsigned*)((const __attribute__((address_space(1))) char*)(gbase) + (unsigned)lnd_v((int)(voff)[_i])), (LAS unsigned*)(lds + (bufoff) + ldsw + _i * 8192), 16, 0, 0); } while (0)
; #define PG8_LDA(dst, b, h) do { _Pragma("unroll") for (int m = 0; m < 4; ++m) _Pragma("unroll") for (int k = 0; k < 2; ++k) dst[m][k] = *(const LAS bf16x8*)(lds + PG8_SA(b, h) + aoff + m * 2048 + k * 1024); } while (0)
; #define PG8_MMA(ai, bj, At, Bt) do { __builtin_amdgcn_s_setprio(1); _Pragma("unroll") for (int m = 0; m < 4; ++m) _Pragma("unroll") for (int n = 0; n < 2; ++n) _Pragma("unroll") for (int k = 0; k < 2; ++k) \
;         acc[ai][bj][m][n] = __builtin_amdgcn_mfma_f32_16x16x32_bf16(Bt[n][k], At[m][k], acc[ai][bj][m][n], 0, 0, 0); __builtin_amdgcn_s_setprio(0); } while (0)
; #define PG8_WAIT_V(n) asm volatile("s_waitcnt vmcnt(" #n ")" ::: "memory")
; #define PG8_WAIT_L(n) asm volatile("s_waitcnt lgkmcnt(" #n ")" ::: "memory")
; #define PG8_BAR __builtin_amdgcn_s_barrier()
; #define PG8_SCHED __builtin_amdgcn_sched_barrier(0)
; template <class Desc, class Epi>
; __device__ __forceinline__ void gemm_phase(const int wv_, LAS unsigned char* lds, const Desc& d, const Epi& E) {
;     ...
;             PG8_LDA(At, 1, 1); PG8_STAGE(PG8_SB(1, 0), b3, voffB); PG8_STAGE(PG8_SB(1, 1), b3 + hstepB, voffB); PG8_STAGE(PG8_SA(1, 0), a3, sA0);
;             PG8_WAIT_V(8); PG8_WAIT_L(0); PG8_BAR; PG8_MMA(1, 0, At, B0); PG8_MMA(1, 1, At, B1); PG8_BAR; PG8_SCHED;
;         }
;         if (wr == 0) PG8_BAR;
	v_mov_b32_e32 v96, v205
	ds_read_b128 v[162:165], v222 offset:49152
	ds_read_b128 v[166:169], v222 offset:50176
	ds_read_b128 v[170:173], v222 offset:51200
	ds_read_b128 v[174:177], v222 offset:52224
	ds_read_b128 v[178:181], v222 offset:53248
	ds_read_b128 v[182:185], v222 offset:54272
	ds_read_b128 v[188:191], v222 offset:55296
	ds_read_b128 v[192:195], v222 offset:56320
	s_mov_b32 m0, s47
	v_lshl_add_u64 v[196:197], s[20:21], 0, v[96:97]
	v_lshl_add_u64 v[196:197], v[196:197], 0, s[30:31]
	v_mov_b32_e32 v96, v208
	global_load_lds_dwordx4 v[196:197], off
	s_mov_b32 m0, s29
	v_lshl_add_u64 v[196:197], s[20:21], 0, v[96:97]
	v_lshl_add_u64 v[196:197], v[196:197], 0, s[30:31]
	global_load_lds_dwordx4 v[196:197], off
	s_mov_b32 m0, s83
	s_nop 0
	global_load_lds_dwordx4 v205, s[22:23]
	s_mov_b32 m0, s82
	s_nop 0
	global_load_lds_dwordx4 v208, s[22:23]
	v_mov_b32_e32 v96, v187
	s_mov_b32 m0, s74
	v_lshl_add_u64 v[196:197], s[4:5], 0, v[96:97]
	v_lshl_add_u64 v[196:197], v[196:197], 0, s[30:31]
	v_mov_b32_e32 v96, v206
	global_load_lds_dwordx4 v[196:197], off
	s_mov_b32 m0, s75
	v_lshl_add_u64 v[196:197], s[4:5], 0, v[96:97]
	v_lshl_add_u64 v[196:197], v[196:197], 0, s[30:31]
	global_load_lds_dwordx4 v[196:197], off
	s_waitcnt vmcnt(8)
	s_waitcnt lgkmcnt(0)
	s_barrier
	v_mfma_f32_16x16x32_bf16 v[92:95], v[130:133], v[162:165], v[92:95]
	v_mfma_f32_16x16x32_bf16 v[88:91], v[138:141], v[162:165], v[88:91]
	v_mfma_f32_16x16x32_bf16 v[84:87], v[130:133], v[170:173], v[84:87]
	v_mfma_f32_16x16x32_bf16 v[80:83], v[138:141], v[170:173], v[80:83]
	v_mfma_f32_16x16x32_bf16 v[76:79], v[130:133], v[178:181], v[76:79]
	v_mfma_f32_16x16x32_bf16 v[72:75], v[138:141], v[178:181], v[72:75]
	v_mfma_f32_16x16x32_bf16 v[68:71], v[130:133], v[188:191], v[68:71]
	v_mfma_f32_16x16x32_bf16 v[64:67], v[138:141], v[188:191], v[64:67]
	v_mfma_f32_16x16x32_bf16 v[92:95], v[134:137], v[166:169], v[92:95]
	v_mfma_f32_16x16x32_bf16 v[88:91], v[142:145], v[166:169], v[88:91]
	v_mfma_f32_16x16x32_bf16 v[84:87], v[134:137], v[174:177], v[84:87]
	v_mfma_f32_16x16x32_bf16 v[80:83], v[142:145], v[174:177], v[80:83]
	v_mfma_f32_16x16x32_bf16 v[76:79], v[134:137], v[182:185], v[76:79]
	v_mfma_f32_16x16x32_bf16 v[72:75], v[142:145], v[182:185], v[72:75]
	v_mfma_f32_16x16x32_bf16 v[68:71], v[134:137], v[192:195], v[68:71]
	v_mfma_f32_16x16x32_bf16 v[64:67], v[142:145], v[192:195], v[64:67]
	v_mfma_f32_16x16x32_bf16 v[28:31], v[146:149], v[162:165], v[28:31]
	v_mfma_f32_16x16x32_bf16 v[24:27], v[154:157], v[162:165], v[24:27]
	v_mfma_f32_16x16x32_bf16 v[12:15], v[146:149], v[170:173], v[12:15]
	v_mfma_f32_16x16x32_bf16 v[8:11], v[154:157], v[170:173], v[8:11]
	v_mfma_f32_16x16x32_bf16 v[20:23], v[146:149], v[178:181], v[20:23]
	v_mfma_f32_16x16x32_bf16 v[16:19], v[154:157], v[178:181], v[16:19]
	v_mfma_f32_16x16x32_bf16 v[4:7], v[146:149], v[188:191], v[4:7]
	v_mfma_f32_16x16x32_bf16 v[0:3], v[154:157], v[188:191], v[0:3]
	v_mfma_f32_16x16x32_bf16 v[28:31], v[150:153], v[166:169], v[28:31]
	v_mfma_f32_16x16x32_bf16 v[24:27], v[158:161], v[166:169], v[24:27]
	v_mfma_f32_16x16x32_bf16 v[12:15], v[150:153], v[174:177], v[12:15]
	v_mfma_f32_16x16x32_bf16 v[8:11], v[158:161], v[174:177], v[8:11]
	v_mfma_f32_16x16x32_bf16 v[20:23], v[150:153], v[182:185], v[20:23]
	v_mfma_f32_16x16x32_bf16 v[16:19], v[158:161], v[182:185], v[16:19]
	v_mfma_f32_16x16x32_bf16 v[4:7], v[150:153], v[192:195], v[4:7]
	v_mfma_f32_16x16x32_bf16 v[0:3], v[158:161], v[192:195], v[0:3]
	s_barrier
	s_movk_i32 s22, 0x100
	s_andn2_b64 vcc, exec, s[2:3]
	s_mov_b64 s[20:21], -1
	s_mov_b64 s[2:3], 0
	s_cbranch_vccz .LBB0_890
	s_and_b64 vcc, exec, s[44:45]
	s_cbranch_vccz .LBB0_893
	s_barrier

; #define PG8_STAGE(bufoff, gbase, voff) do { _Pragma("unroll") for (int _i = 0; _i < 2; ++_i) \
;         __builtin_amdgcn_global_load_lds((const __attribute__((address_space(1))) unsigned*)((const __attribute__((address_space(1))) char*)(gbase) + (unsigned)lnd_v((int)(voff)[_i])), (LAS unsigned*)(lds + (bufoff) + ldsw + _i * 8192), 16, 0, 0); } while (0)
; #define PG8_LDA(dst, b, h) do { _Pragma("unroll") for (int m = 0; m < 4; ++m) _Pragma("unroll") for (int k = 0; k < 2; ++k) dst[m][k] = *(const LAS bf16x8*)(lds + PG8_SA(b, h) + aoff + m * 2048 + k * 1024); } while (0)
; #define PG8_LDB(dst, b, h) do { _Pragma("unroll") for (int n = 0; n < 2; ++n) _Pragma("unroll") for (int k = 0; k < 2; ++k) dst[n][k] = *(const LAS bf16x8*)(lds + PG8_SB(b, h) + boff + n * 2048 + k * 1024); } while (0)
; #define PG8_MMA(ai, bj, At, Bt) do { __builtin_amdgcn_s_setprio(1); _Pragma("unroll") for (int m = 0; m < 4; ++m) _Pragma("unroll") for (int n = 0; n < 2; ++n) _Pragma("unroll") for (int k = 0; k < 2; ++k) \
;         acc[ai][bj][m][n] = __builtin_amdgcn_mfma_f32_16x16x32_bf16(Bt[n][k], At[m][k], acc[ai][bj][m][n], 0, 0, 0); __builtin_amdgcn_s_setprio(0); } while (0)
; #define PG8_WAIT_V(n) asm volatile("s_waitcnt vmcnt(" #n ")" ::: "memory")
; #define PG8_WAIT_L(n) asm volatile("s_waitcnt lgkmcnt(" #n ")" ::: "memory")
; #define PG8_BAR __builtin_amdgcn_s_barrier()
; #define PG8_SCHED __builtin_amdgcn_sched_barrier(0)
; template <class Desc, class Epi>
; __device__ __forceinline__ void gemm_phase(const int wv_, LAS unsigned char* lds, const Desc& d, const Epi& E) {
;     ...
;             PG8_LDB(B0, 0, 0); PG8_LDB(B1, 0, 1); PG8_SCHED; PG8_LDA(At, 0, 0); PG8_STAGE(PG8_SA(1, 1), a1, voffA1);
;             PG8_WAIT_V(8); PG8_WAIT_L(0); PG8_BAR; PG8_MMA(0, 0, At, B0); PG8_MMA(0, 1, At, B1); PG8_BAR; PG8_SCHED;
;             PG8_LDA(At, 0, 1); PG8_STAGE(PG8_SB(0, 0), b2, voffB); PG8_STAGE(PG8_SB(0, 1), b2 + hstepB, voffB); PG8_STAGE(PG8_SA(0, 0), a2, sA0);
;             PG8_WAIT_V(8); PG8_WAIT_L(0); PG8_BAR; PG8_MMA(1, 0, At, B0); PG8_MMA(1, 1, At, B1); PG8_BAR; PG8_SCHED;
.LBB0_917:
	s_add_u32 s54, s52, s22
	s_addc_u32 s55, s53, 0
	s_add_u32 s23, s54, 0x100
	s_addc_u32 s24, s55, 0
	s_and_b64 s[4:5], s[20:21], exec
	s_cselect_b32 s4, s44, s23
	s_cselect_b32 s5, s45, s24
	s_add_u32 s22, s50, s22
	s_addc_u32 s23, s51, 0
	s_add_u32 s22, s22, 0x100
	s_addc_u32 s23, s23, 0
	s_add_i32 s80, 0, 0x10000
	s_and_b64 s[20:21], s[20:21], exec
	s_cselect_b32 s21, s47, s23
	s_cselect_b32 s20, s46, s22
	s_add_i32 s23, 0, 0x14000
	v_add_u32_e32 v96, s80, v139
	s_add_i32 s82, s80, s60
	ds_read_b128 v[150:153], v96
	ds_read_b128 v[154:157], v96 offset:1024
	ds_read_b128 v[158:161], v96 offset:2048
	ds_read_b128 v[162:165], v96 offset:3072
	v_add_u32_e32 v96, s23, v139
	s_add_i32 m0, s61, 0xc000
	s_add_i32 s83, s61, 0xe000
	s_add_i32 s78, s82, 0x2000
	ds_read_b128 v[166:169], v96
	ds_read_b128 v[170:173], v96 offset:1024
	ds_read_b128 v[174:177], v96 offset:2048
	ds_read_b128 v[178:181], v96 offset:3072
	s_add_u32 s24, s20, 0x40000
	s_addc_u32 s25, s21, 0
	s_add_i32 s76, 0, 0x18000
	s_add_i32 s79, s23, s60
	s_add_i32 s74, s76, s60
	s_add_i32 s77, s79, 0x2000
	s_add_i32 s75, 0, 0x1c000
	s_add_i32 s29, s74, 0x2000
	s_add_u32 s22, s20, 0x40080
	s_addc_u32 s23, s21, 0
	s_add_i32 s81, s75, s60
	s_add_i32 s80, s81, 0x2000
	v_mov_b32_e32 v96, v133
	ds_read_b128 v[182:185], v149
	ds_read_b128 v[186:189], v149 offset:1024
	ds_read_b128 v[190:193], v149 offset:2048
	ds_read_b128 v[194:197], v149 offset:3072
	ds_read_b128 v[198:201], v149 offset:4096
	ds_read_b128 v[202:205], v149 offset:5120
	ds_read_b128 v[206:209], v149 offset:6144
	ds_read_b128 v[210:213], v149 offset:7168
	s_nop 0
	v_lshl_add_u64 v[130:131], s[54:55], 0, v[96:97]
	v_lshl_add_u64 v[130:131], v[130:131], 0, s[30:31]
	v_mov_b32_e32 v96, v136
	global_load_lds_dwordx4 v[130:131], off
	s_mov_b32 m0, s83
	v_lshl_add_u64 v[130:131], s[54:55], 0, v[96:97]
	v_lshl_add_u64 v[130:131], v[130:131], 0, s[30:31]
	global_load_lds_dwordx4 v[130:131], off
	s_waitcnt vmcnt(8)
	s_waitcnt lgkmcnt(0)
	s_barrier
	v_mfma_f32_16x16x32_bf16 v[126:129], v[150:153], v[182:185], v[126:129]
	v_mfma_f32_16x16x32_bf16 v[122:125], v[158:161], v[182:185], v[122:125]
	v_mfma_f32_16x16x32_bf16 v[110:113], v[150:153], v[190:193], v[110:113]
	v_mfma_f32_16x16x32_bf16 v[106:109], v[158:161], v[190:193], v[106:109]
	v_mfma_f32_16x16x32_bf16 v[92:95], v[150:153], v[198:201], v[92:95]
	v_mfma_f32_16x16x32_bf16 v[88:91], v[158:161], v[198:201], v[88:91]
	v_mfma_f32_16x16x32_bf16 v[76:79], v[150:153], v[206:209], v[76:79]
	v_mfma_f32_16x16x32_bf16 v[72:75], v[158:161], v[206:209], v[72:75]
	v_mfma_f32_16x16x32_bf16 v[126:129], v[154:157], v[186:189], v[126:129]
	v_mfma_f32_16x16x32_bf16 v[122:125], v[162:165], v[186:189], v[122:125]
	v_mfma_f32_16x16x32_bf16 v[110:113], v[154:157], v[194:197], v[110:113]
	v_mfma_f32_16x16x32_bf16 v[106:109], v[162:165], v[194:197], v[106:109]
	v_mfma_f32_16x16x32_bf16 v[92:95], v[154:157], v[202:205], v[92:95]
	v_mfma_f32_16x16x32_bf16 v[88:91], v[162:165], v[202:205], v[88:91]
	v_mfma_f32_16x16x32_bf16 v[76:79], v[154:157], v[210:213], v[76:79]
	v_mfma_f32_16x16x32_bf16 v[72:75], v[162:165], v[210:213], v[72:75]
	v_mfma_f32_16x16x32_bf16 v[118:121], v[166:169], v[182:185], v[118:121]
	v_mfma_f32_16x16x32_bf16 v[114:117], v[174:177], v[182:185], v[114:117]
	v_mfma_f32_16x16x32_bf16 v[102:105], v[166:169], v[190:193], v[102:105]
	v_mfma_f32_16x16x32_bf16 v[98:101], v[174:177], v[190:193], v[98:101]
	v_mfma_f32_16x16x32_bf16 v[84:87], v[166:169], v[198:201], v[84:87]
	v_mfma_f32_16x16x32_bf16 v[80:83], v[174:177], v[198:201], v[80:83]
	v_mfma_f32_16x16x32_bf16 v[68:71], v[166:169], v[206:209], v[68:71]
	v_mfma_f32_16x16x32_bf16 v[64:67], v[174:177], v[206:209], v[64:67]
	v_mfma_f32_16x16x32_bf16 v[118:121], v[170:173], v[186:189], v[118:121]
	v_mfma_f32_16x16x32_bf16 v[114:117], v[178:181], v[186:189], v[114:117]
	v_mfma_f32_16x16x32_bf16 v[102:105], v[170:173], v[194:197], v[102:105]
	v_mfma_f32_16x16x32_bf16 v[98:101], v[178:181], v[194:197], v[98:101]
	v_mfma_f32_16x16x32_bf16 v[84:87], v[170:173], v[202:205], v[84:87]
	v_mfma_f32_16x16x32_bf16 v[80:83], v[178:181], v[202:205], v[80:83]
	v_mfma_f32_16x16x32_bf16 v[68:71], v[170:173], v[210:213], v[68:71]
	v_mfma_f32_16x16x32_bf16 v[64:67], v[178:181], v[210:213], v[64:67]
	s_barrier
	s_mov_b32 m0, s82
	ds_read_b128 v[182:185], v149 offset:16384
	ds_read_b128 v[186:189], v149 offset:17408
	ds_read_b128 v[190:193], v149 offset:18432
	ds_read_b128 v[194:197], v149 offset:19456
	ds_read_b128 v[198:201], v149 offset:20480
	ds_read_b128 v[202:205], v149 offset:21504
	ds_read_b128 v[206:209], v149 offset:22528
	ds_read_b128 v[210:213], v149 offset:23552
	s_nop 0
	global_load_lds_dwordx4 v134, s[20:21]
	s_mov_b32 m0, s78
	s_nop 0
	global_load_lds_dwordx4 v137, s[20:21]
	s_mov_b32 m0, s79
	s_nop 0
	global_load_lds_dwordx4 v134, s[24:25]
	s_mov_b32 m0, s77
	s_nop 0
	global_load_lds_dwordx4 v137, s[24:25]
	s_mov_b32 m0, s61
	s_nop 0
	global_load_lds_dwordx4 v132, s[4:5]
	s_mov_b32 m0, s63
	s_nop 0
	global_load_lds_dwordx4 v135, s[4:5]
	s_waitcnt vmcnt(8)
	s_waitcnt lgkmcnt(0)
	s_barrier
; #define PG8_STAGE(bufoff, gbase, voff) do { _Pragma("unroll") for (int _i = 0; _i < 2; ++_i) \
;         __builtin_amdgcn_global_load_lds((const __attribute__((address_space(1))) unsigned*)((const __attribute__((address_space(1))) char*)(gbase) + (unsigned)lnd_v((int)(voff)[_i])), (LAS unsigned*)(lds + (bufoff) + ldsw + _i * 8192), 16, 0, 0); } while (0)
; #define PG8_LDA(dst, b, h) do { _Pragma("unroll") for (int m = 0; m < 4; ++m) _Pragma("unroll") for (int k = 0; k < 2; ++k) dst[m][k] = *(const LAS bf16x8*)(lds + PG8_SA(b, h) + aoff + m * 2048 + k * 1024); } while (0)
; #define PG8_LDB(dst, b, h) do { _Pragma("unroll") for (int n = 0; n < 2; ++n) _Pragma("unroll") for (int k = 0; k < 2; ++k) dst[n][k] = *(const LAS bf16x8*)(lds + PG8_SB(b, h) + boff + n * 2048 + k * 1024); } while (0)
; #define PG8_MMA(ai, bj, At, Bt) do { __builtin_amdgcn_s_setprio(1); _Pragma("unroll") for (int m = 0; m < 4; ++m) _Pragma("unroll") for (int n = 0; n < 2; ++n) _Pragma("unroll") for (int k = 0; k < 2; ++k) \
;         acc[ai][bj][m][n] = __builtin_amdgcn_mfma_f32_16x16x32_bf16(Bt[n][k], At[m][k], acc[ai][bj][m][n], 0, 0, 0); __builtin_amdgcn_s_setprio(0); } while (0)
; #define PG8_WAIT_V(n) asm volatile("s_waitcnt vmcnt(" #n ")" ::: "memory")
; #define PG8_WAIT_L(n) asm volatile("s_waitcnt lgkmcnt(" #n ")" ::: "memory")
; #define PG8_BAR __builtin_amdgcn_s_barrier()
; #define PG8_SCHED __builtin_amdgcn_sched_barrier(0)
; template <class Desc, class Epi>
; __device__ __forceinline__ void gemm_phase(const int wv_, LAS unsigned char* lds, const Desc& d, const Epi& E) {
;     ...
;             PG8_WAIT_V(8); PG8_WAIT_L(0); PG8_BAR; PG8_MMA(1, 0, At, B0); PG8_MMA(1, 1, At, B1); PG8_BAR; PG8_SCHED;
;             PG8_LDB(B0, 1, 0); PG8_LDB(B1, 1, 1); PG8_SCHED; PG8_LDA(At, 1, 0); PG8_STAGE(PG8_SA(0, 1), a2, sA1);
;             PG8_WAIT_V(8); PG8_WAIT_L(0); PG8_BAR; PG8_MMA(0, 0, At, B0); PG8_MMA(0, 1, At, B1); PG8_BAR; PG8_SCHED;
	v_mfma_f32_16x16x32_bf16 v[60:63], v[150:153], v[182:185], v[60:63]
	v_mfma_f32_16x16x32_bf16 v[56:59], v[158:161], v[182:185], v[56:59]
	v_mfma_f32_16x16x32_bf16 v[44:47], v[150:153], v[190:193], v[44:47]
	v_mfma_f32_16x16x32_bf16 v[32:35], v[158:161], v[190:193], v[32:35]
	v_mfma_f32_16x16x32_bf16 v[16:19], v[150:153], v[198:201], v[16:19]
	v_mfma_f32_16x16x32_bf16 v[8:11], v[158:161], v[198:201], v[8:11]
	v_mfma_f32_16x16x32_bf16 v[4:7], v[150:153], v[206:209], v[4:7]
	v_mfma_f32_16x16x32_bf16 v[0:3], v[158:161], v[206:209], v[0:3]
	v_mfma_f32_16x16x32_bf16 v[60:63], v[154:157], v[186:189], v[60:63]
	v_mfma_f32_16x16x32_bf16 v[56:59], v[162:165], v[186:189], v[56:59]
	v_mfma_f32_16x16x32_bf16 v[44:47], v[154:157], v[194:197], v[44:47]
	v_mfma_f32_16x16x32_bf16 v[32:35], v[162:165], v[194:197], v[32:35]
	v_mfma_f32_16x16x32_bf16 v[16:19], v[154:157], v[202:205], v[16:19]
	v_mfma_f32_16x16x32_bf16 v[8:11], v[162:165], v[202:205], v[8:11]
	v_mfma_f32_16x16x32_bf16 v[4:7], v[154:157], v[210:213], v[4:7]
	v_mfma_f32_16x16x32_bf16 v[0:3], v[162:165], v[210:213], v[0:3]
	v_mfma_f32_16x16x32_bf16 v[52:55], v[166:169], v[182:185], v[52:55]
	v_mfma_f32_16x16x32_bf16 v[48:51], v[174:177], v[182:185], v[48:51]
	v_mfma_f32_16x16x32_bf16 v[28:31], v[166:169], v[190:193], v[28:31]
	v_mfma_f32_16x16x32_bf16 v[12:15], v[174:177], v[190:193], v[12:15]
	v_mfma_f32_16x16x32_bf16 v[36:39], v[166:169], v[198:201], v[36:39]
	v_mfma_f32_16x16x32_bf16 v[40:43], v[174:177], v[198:201], v[40:43]
	v_mfma_f32_16x16x32_bf16 v[20:23], v[166:169], v[206:209], v[20:23]
	v_mfma_f32_16x16x32_bf16 v[24:27], v[174:177], v[206:209], v[24:27]
	v_mfma_f32_16x16x32_bf16 v[52:55], v[170:173], v[186:189], v[52:55]
	v_mfma_f32_16x16x32_bf16 v[48:51], v[178:181], v[186:189], v[48:51]
	v_mfma_f32_16x16x32_bf16 v[28:31], v[170:173], v[194:197], v[28:31]
	v_mfma_f32_16x16x32_bf16 v[12:15], v[178:181], v[194:197], v[12:15]
	v_mfma_f32_16x16x32_bf16 v[36:39], v[170:173], v[202:205], v[36:39]
	v_mfma_f32_16x16x32_bf16 v[40:43], v[178:181], v[202:205], v[40:43]
	v_mfma_f32_16x16x32_bf16 v[20:23], v[170:173], v[210:213], v[20:23]
	v_mfma_f32_16x16x32_bf16 v[24:27], v[178:181], v[210:213], v[24:27]
	s_barrier
	v_add_u32_e32 v96, s76, v139
	ds_read_b128 v[150:153], v96
	ds_read_b128 v[154:157], v96 offset:1024
	ds_read_b128 v[158:161], v96 offset:2048
	ds_read_b128 v[162:165], v96 offset:3072
	v_add_u32_e32 v96, s75, v139
	ds_read_b128 v[166:169], v96
	ds_read_b128 v[170:173], v96 offset:1024
	ds_read_b128 v[174:177], v96 offset:2048
	ds_read_b128 v[178:181], v96 offset:3072
	s_mov_b32 m0, s64
	ds_read_b128 v[182:185], v149 offset:32768
	ds_read_b128 v[186:189], v149 offset:33792
	ds_read_b128 v[190:193], v149 offset:34816
	ds_read_b128 v[194:197], v149 offset:35840
	ds_read_b128 v[198:201], v149 offset:36864
	ds_read_b128 v[202:205], v149 offset:37888
	ds_read_b128 v[206:209], v149 offset:38912
	ds_read_b128 v[210:213], v149 offset:39936
	s_nop 0
	global_load_lds_dwordx4 v133, s[4:5]
	s_mov_b32 m0, s65
	s_nop 0
	global_load_lds_dwordx4 v136, s[4:5]
	s_waitcnt vmcnt(8)
	s_waitcnt lgkmcnt(0)
	s_barrier
	v_mfma_f32_16x16x32_bf16 v[126:129], v[150:153], v[182:185], v[126:129]
	v_mfma_f32_16x16x32_bf16 v[122:125], v[158:161], v[182:185], v[122:125]
	v_mfma_f32_16x16x32_bf16 v[110:113], v[150:153], v[190:193], v[110:113]
	v_mfma_f32_16x16x32_bf16 v[106:109], v[158:161], v[190:193], v[106:109]
	v_mfma_f32_16x16x32_bf16 v[92:95], v[150:153], v[198:201], v[92:95]
	v_mfma_f32_16x16x32_bf16 v[88:91], v[158:161], v[198:201], v[88:91]
	v_mfma_f32_16x16x32_bf16 v[76:79], v[150:153], v[206:209], v[76:79]
	v_mfma_f32_16x16x32_bf16 v[72:75], v[158:161], v[206:209], v[72:75]
	v_mfma_f32_16x16x32_bf16 v[126:129], v[154:157], v[186:189], v[126:129]
	v_mfma_f32_16x16x32_bf16 v[122:125], v[162:165], v[186:189], v[122:125]
	v_mfma_f32_16x16x32_bf16 v[110:113], v[154:157], v[194:197], v[110:113]
	v_mfma_f32_16x16x32_bf16 v[106:109], v[162:165], v[194:197], v[106:109]
	v_mfma_f32_16x16x32_bf16 v[92:95], v[154:157], v[202:205], v[92:95]
	v_mfma_f32_16x16x32_bf16 v[88:91], v[162:165], v[202:205], v[88:91]
	v_mfma_f32_16x16x32_bf16 v[76:79], v[154:157], v[210:213], v[76:79]
	v_mfma_f32_16x16x32_bf16 v[72:75], v[162:165], v[210:213], v[72:75]
	v_mfma_f32_16x16x32_bf16 v[118:121], v[166:169], v[182:185], v[118:121]
	v_mfma_f32_16x16x32_bf16 v[114:117], v[174:177], v[182:185], v[114:117]
	v_mfma_f32_16x16x32_bf16 v[102:105], v[166:169], v[190:193], v[102:105]
	v_mfma_f32_16x16x32_bf16 v[98:101], v[174:177], v[190:193], v[98:101]
	v_mfma_f32_16x16x32_bf16 v[84:87], v[166:169], v[198:201], v[84:87]
	v_mfma_f32_16x16x32_bf16 v[80:83], v[174:177], v[198:201], v[80:83]
	v_mfma_f32_16x16x32_bf16 v[68:71], v[166:169], v[206:209], v[68:71]
	v_mfma_f32_16x16x32_bf16 v[64:67], v[174:177], v[206:209], v[64:67]
	v_mfma_f32_16x16x32_bf16 v[118:121], v[170:173], v[186:189], v[118:121]
	v_mfma_f32_16x16x32_bf16 v[114:117], v[178:181], v[186:189], v[114:117]
	v_mfma_f32_16x16x32_bf16 v[102:105], v[170:173], v[194:197], v[102:105]
	v_mfma_f32_16x16x32_bf16 v[98:101], v[178:181], v[194:197], v[98:101]
	v_mfma_f32_16x16x32_bf16 v[84:87], v[170:173], v[202:205], v[84:87]
	v_mfma_f32_16x16x32_bf16 v[80:83], v[178:181], v[202:205], v[80:83]
	v_mfma_f32_16x16x32_bf16 v[68:71], v[170:173], v[210:213], v[68:71]
	v_mfma_f32_16x16x32_bf16 v[64:67], v[178:181], v[210:213], v[64:67]
	s_barrier
; #define PG8_STAGE(bufoff, gbase, voff) do { _Pragma("unroll") for (int _i = 0; _i < 2; ++_i) \
;         __builtin_amdgcn_global_load_lds((const __attribute__((address_space(1))) unsigned*)((const __attribute__((address_space(1))) char*)(gbase) + (unsigned)lnd_v((int)(voff)[_i])), (LAS unsigned*)(lds + (bufoff) + ldsw + _i * 8192), 16, 0, 0); } while (0)
; #define PG8_LDA(dst, b, h) do { _Pragma("unroll") for (int m = 0; m < 4; ++m) _Pragma("unroll") for (int k = 0; k < 2; ++k) dst[m][k] = *(const LAS bf16x8*)(lds + PG8_SA(b, h) + aoff + m * 2048 + k * 1024); } while (0)
; #define PG8_MMA(ai, bj, At, Bt) do { __builtin_amdgcn_s_setprio(1); _Pragma("unroll") for (int m = 0; m < 4; ++m) _Pragma("unroll") for (int n = 0; n < 2; ++n) _Pragma("unroll") for (int k = 0; k < 2; ++k) \
;         acc[ai][bj][m][n] = __builtin_amdgcn_mfma_f32_16x16x32_bf16(Bt[n][k], At[m][k], acc[ai][bj][m][n], 0, 0, 0); __builtin_amdgcn_s_setprio(0); } while (0)
; #define PG8_WAIT_V(n) asm volatile("s_waitcnt vmcnt(" #n ")" ::: "memory")
; #define PG8_WAIT_L(n) asm volatile("s_waitcnt lgkmcnt(" #n ")" ::: "memory")
; #define PG8_BAR __builtin_amdgcn_s_barrier()
; #define PG8_SCHED __builtin_amdgcn_sched_barrier(0)
; template <class Desc, class Epi>
; __device__ __forceinline__ void gemm_phase(const int wv_, LAS unsigned char* lds, const Desc& d, const Epi& E) {
;     ...
;             PG8_LDA(At, 1, 1); PG8_STAGE(PG8_SB(1, 0), b3, voffB); PG8_STAGE(PG8_SB(1, 1), b3 + hstepB, voffB); PG8_STAGE(PG8_SA(1, 0), a3, sA0);
;             PG8_WAIT_V(8); PG8_WAIT_L(0); PG8_BAR; PG8_MMA(1, 0, At, B0); PG8_MMA(1, 1, At, B1); PG8_BAR; PG8_SCHED;
;         }
;         if (wr == 0) PG8_BAR;
	v_mov_b32_e32 v96, v134
	ds_read_b128 v[182:185], v149 offset:49152
	ds_read_b128 v[186:189], v149 offset:50176
	ds_read_b128 v[190:193], v149 offset:51200
	ds_read_b128 v[194:197], v149 offset:52224
	ds_read_b128 v[198:201], v149 offset:53248
	ds_read_b128 v[202:205], v149 offset:54272
	ds_read_b128 v[206:209], v149 offset:55296
	ds_read_b128 v[210:213], v149 offset:56320
	s_mov_b32 m0, s74
	v_lshl_add_u64 v[130:131], s[20:21], 0, v[96:97]
	v_lshl_add_u64 v[130:131], v[130:131], 0, s[30:31]
	v_mov_b32_e32 v96, v137
	global_load_lds_dwordx4 v[130:131], off
	s_mov_b32 m0, s29
	v_lshl_add_u64 v[130:131], s[20:21], 0, v[96:97]
	v_lshl_add_u64 v[130:131], v[130:131], 0, s[30:31]
	global_load_lds_dwordx4 v[130:131], off
	s_mov_b32 m0, s81
	s_nop 0
	global_load_lds_dwordx4 v134, s[22:23]
	s_mov_b32 m0, s80
	s_nop 0
	global_load_lds_dwordx4 v137, s[22:23]
	v_mov_b32_e32 v96, v132
	s_mov_b32 m0, s68
	v_lshl_add_u64 v[130:131], s[4:5], 0, v[96:97]
	v_lshl_add_u64 v[130:131], v[130:131], 0, s[30:31]
	v_mov_b32_e32 v96, v135
	global_load_lds_dwordx4 v[130:131], off
	s_mov_b32 m0, s69
	v_lshl_add_u64 v[130:131], s[4:5], 0, v[96:97]
	v_lshl_add_u64 v[130:131], v[130:131], 0, s[30:31]
	global_load_lds_dwordx4 v[130:131], off
	s_waitcnt vmcnt(8)
	s_waitcnt lgkmcnt(0)
	s_barrier
	v_mfma_f32_16x16x32_bf16 v[60:63], v[150:153], v[182:185], v[60:63]
	v_mfma_f32_16x16x32_bf16 v[56:59], v[158:161], v[182:185], v[56:59]
	v_mfma_f32_16x16x32_bf16 v[44:47], v[150:153], v[190:193], v[44:47]
	v_mfma_f32_16x16x32_bf16 v[32:35], v[158:161], v[190:193], v[32:35]
	v_mfma_f32_16x16x32_bf16 v[16:19], v[150:153], v[198:201], v[16:19]
	v_mfma_f32_16x16x32_bf16 v[8:11], v[158:161], v[198:201], v[8:11]
	v_mfma_f32_16x16x32_bf16 v[4:7], v[150:153], v[206:209], v[4:7]
	v_mfma_f32_16x16x32_bf16 v[0:3], v[158:161], v[206:209], v[0:3]
	v_mfma_f32_16x16x32_bf16 v[60:63], v[154:157], v[186:189], v[60:63]
	v_mfma_f32_16x16x32_bf16 v[56:59], v[162:165], v[186:189], v[56:59]
	v_mfma_f32_16x16x32_bf16 v[44:47], v[154:157], v[194:197], v[44:47]
	v_mfma_f32_16x16x32_bf16 v[32:35], v[162:165], v[194:197], v[32:35]
	v_mfma_f32_16x16x32_bf16 v[16:19], v[154:157], v[202:205], v[16:19]
	v_mfma_f32_16x16x32_bf16 v[8:11], v[162:165], v[202:205], v[8:11]
	v_mfma_f32_16x16x32_bf16 v[4:7], v[154:157], v[210:213], v[4:7]
	v_mfma_f32_16x16x32_bf16 v[0:3], v[162:165], v[210:213], v[0:3]
	v_mfma_f32_16x16x32_bf16 v[52:55], v[166:169], v[182:185], v[52:55]
	v_mfma_f32_16x16x32_bf16 v[48:51], v[174:177], v[182:185], v[48:51]
	v_mfma_f32_16x16x32_bf16 v[28:31], v[166:169], v[190:193], v[28:31]
	v_mfma_f32_16x16x32_bf16 v[12:15], v[174:177], v[190:193], v[12:15]
	v_mfma_f32_16x16x32_bf16 v[36:39], v[166:169], v[198:201], v[36:39]
	v_mfma_f32_16x16x32_bf16 v[40:43], v[174:177], v[198:201], v[40:43]
	v_mfma_f32_16x16x32_bf16 v[20:23], v[166:169], v[206:209], v[20:23]
	v_mfma_f32_16x16x32_bf16 v[24:27], v[174:177], v[206:209], v[24:27]
	v_mfma_f32_16x16x32_bf16 v[52:55], v[170:173], v[186:189], v[52:55]
	v_mfma_f32_16x16x32_bf16 v[48:51], v[178:181], v[186:189], v[48:51]
	v_mfma_f32_16x16x32_bf16 v[28:31], v[170:173], v[194:197], v[28:31]
	v_mfma_f32_16x16x32_bf16 v[12:15], v[178:181], v[194:197], v[12:15]
	v_mfma_f32_16x16x32_bf16 v[36:39], v[170:173], v[202:205], v[36:39]
	v_mfma_f32_16x16x32_bf16 v[40:43], v[178:181], v[202:205], v[40:43]
	v_mfma_f32_16x16x32_bf16 v[20:23], v[170:173], v[210:213], v[20:23]
	v_mfma_f32_16x16x32_bf16 v[24:27], v[178:181], v[210:213], v[24:27]
	s_barrier
	s_movk_i32 s22, 0x100
	s_andn2_b64 vcc, exec, s[2:3]
	s_mov_b64 s[20:21], -1
	s_mov_b64 s[2:3], 0
	s_cbranch_vccz .LBB0_917
	s_and_b64 vcc, exec, s[42:43]
	s_cbranch_vccz .LBB0_920
	s_barrier

; #define PG8_STAGE(bufoff, gbase, voff) do { _Pragma("unroll") for (int _i = 0; _i < 2; ++_i) \
;         __builtin_amdgcn_global_load_lds((const __attribute__((address_space(1))) unsigned*)((const __attribute__((address_space(1))) char*)(gbase) + (unsigned)lnd_v((int)(voff)[_i])), (LAS unsigned*)(lds + (bufoff) + ldsw + _i * 8192), 16, 0, 0); } while (0)
; #define PG8_LDA(dst, b, h) do { _Pragma("unroll") for (int m = 0; m < 4; ++m) _Pragma("unroll") for (int k = 0; k < 2; ++k) dst[m][k] = *(const LAS bf16x8*)(lds + PG8_SA(b, h) + aoff + m * 2048 + k * 1024); } while (0)
; #define PG8_LDB(dst, b, h) do { _Pragma("unroll") for (int n = 0; n < 2; ++n) _Pragma("unroll") for (int k = 0; k < 2; ++k) dst[n][k] = *(const LAS bf16x8*)(lds + PG8_SB(b, h) + boff + n * 2048 + k * 1024); } while (0)
; #define PG8_MMA(ai, bj, At, Bt) do { __builtin_amdgcn_s_setprio(1); _Pragma("unroll") for (int m = 0; m < 4; ++m) _Pragma("unroll") for (int n = 0; n < 2; ++n) _Pragma("unroll") for (int k = 0; k < 2; ++k) \
;         acc[ai][bj][m][n] = __builtin_amdgcn_mfma_f32_16x16x32_bf16(Bt[n][k], At[m][k], acc[ai][bj][m][n], 0, 0, 0); __builtin_amdgcn_s_setprio(0); } while (0)
; #define PG8_WAIT_V(n) asm volatile("s_waitcnt vmcnt(" #n ")" ::: "memory")
; #define PG8_WAIT_L(n) asm volatile("s_waitcnt lgkmcnt(" #n ")" ::: "memory")
; #define PG8_BAR __builtin_amdgcn_s_barrier()
; #define PG8_SCHED __builtin_amdgcn_sched_barrier(0)
; template <class Desc, class Epi>
; __device__ __forceinline__ void gemm_phase(const int wv_, LAS unsigned char* lds, const Desc& d, const Epi& E) {
;     ...
;             PG8_LDB(B0, 0, 0); PG8_LDB(B1, 0, 1); PG8_SCHED; PG8_LDA(At, 0, 0); PG8_STAGE(PG8_SA(1, 1), a1, voffA1);
;             PG8_WAIT_V(8); PG8_WAIT_L(0); PG8_BAR; PG8_MMA(0, 0, At, B0); PG8_MMA(0, 1, At, B1); PG8_BAR; PG8_SCHED;
;             PG8_LDA(At, 0, 1); PG8_STAGE(PG8_SB(0, 0), b2, voffB); PG8_STAGE(PG8_SB(0, 1), b2 + hstepB, voffB); PG8_STAGE(PG8_SA(0, 0), a2, sA0);
;             PG8_WAIT_V(8); PG8_WAIT_L(0); PG8_BAR; PG8_MMA(1, 0, At, B0); PG8_MMA(1, 1, At, B1); PG8_BAR; PG8_SCHED;
.LBB0_937:
	s_add_u32 s52, s50, s22
	s_addc_u32 s53, s51, 0
	s_add_u32 s23, s52, 0x100
	s_addc_u32 s24, s53, 0
	s_and_b64 s[4:5], s[20:21], exec
	s_cselect_b32 s4, s42, s23
	s_cselect_b32 s5, s43, s24
	s_add_u32 s22, s48, s22
	s_addc_u32 s23, s49, 0
	s_add_u32 s22, s22, 0x100
	s_addc_u32 s23, s23, 0
	s_add_i32 s77, 0, 0x10000
	s_and_b64 s[20:21], s[20:21], exec
	s_cselect_b32 s21, s45, s23
	s_cselect_b32 s20, s44, s22
	s_add_i32 s23, 0, 0x14000
	v_add_u32_e32 v96, s77, v139
	s_add_i32 s79, s77, s59
	ds_read_b128 v[150:153], v96
	ds_read_b128 v[154:157], v96 offset:1024
	ds_read_b128 v[158:161], v96 offset:2048
	ds_read_b128 v[162:165], v96 offset:3072
	v_add_u32_e32 v96, s23, v139
	s_add_i32 m0, s60, 0xc000
	s_add_i32 s80, s60, 0xe000
	s_add_i32 s75, s79, 0x2000
	ds_read_b128 v[166:169], v96
	ds_read_b128 v[170:173], v96 offset:1024
	ds_read_b128 v[174:177], v96 offset:2048
	ds_read_b128 v[178:181], v96 offset:3072
	s_add_u32 s24, s20, 0x40000
	s_addc_u32 s25, s21, 0
	s_add_i32 s73, 0, 0x18000
	s_add_i32 s76, s23, s59
	s_add_i32 s71, s73, s59
	s_add_i32 s74, s76, 0x2000
	s_add_i32 s72, 0, 0x1c000
	s_add_i32 s29, s71, 0x2000
	s_add_u32 s22, s20, 0x40080
	s_addc_u32 s23, s21, 0
	s_add_i32 s78, s72, s59
	s_add_i32 s77, s78, 0x2000
	v_mov_b32_e32 v96, v133
	ds_read_b128 v[182:185], v149
	ds_read_b128 v[186:189], v149 offset:1024
	ds_read_b128 v[190:193], v149 offset:2048
	ds_read_b128 v[194:197], v149 offset:3072
	ds_read_b128 v[198:201], v149 offset:4096
	ds_read_b128 v[202:205], v149 offset:5120
	ds_read_b128 v[206:209], v149 offset:6144
	ds_read_b128 v[210:213], v149 offset:7168
	s_nop 0
	v_lshl_add_u64 v[130:131], s[52:53], 0, v[96:97]
	v_lshl_add_u64 v[130:131], v[130:131], 0, s[30:31]
	v_mov_b32_e32 v96, v136
	global_load_lds_dwordx4 v[130:131], off
	s_mov_b32 m0, s80
	v_lshl_add_u64 v[130:131], s[52:53], 0, v[96:97]
	v_lshl_add_u64 v[130:131], v[130:131], 0, s[30:31]
	global_load_lds_dwordx4 v[130:131], off
	s_waitcnt vmcnt(8)
	s_waitcnt lgkmcnt(0)
	s_barrier
	v_mfma_f32_16x16x32_bf16 v[126:129], v[150:153], v[182:185], v[126:129]
	v_mfma_f32_16x16x32_bf16 v[122:125], v[158:161], v[182:185], v[122:125]
	v_mfma_f32_16x16x32_bf16 v[110:113], v[150:153], v[190:193], v[110:113]
	v_mfma_f32_16x16x32_bf16 v[106:109], v[158:161], v[190:193], v[106:109]
	v_mfma_f32_16x16x32_bf16 v[92:95], v[150:153], v[198:201], v[92:95]
	v_mfma_f32_16x16x32_bf16 v[88:91], v[158:161], v[198:201], v[88:91]
	v_mfma_f32_16x16x32_bf16 v[76:79], v[150:153], v[206:209], v[76:79]
	v_mfma_f32_16x16x32_bf16 v[72:75], v[158:161], v[206:209], v[72:75]
	v_mfma_f32_16x16x32_bf16 v[126:129], v[154:157], v[186:189], v[126:129]
	v_mfma_f32_16x16x32_bf16 v[122:125], v[162:165], v[186:189], v[122:125]
	v_mfma_f32_16x16x32_bf16 v[110:113], v[154:157], v[194:197], v[110:113]
	v_mfma_f32_16x16x32_bf16 v[106:109], v[162:165], v[194:197], v[106:109]
	v_mfma_f32_16x16x32_bf16 v[92:95], v[154:157], v[202:205], v[92:95]
	v_mfma_f32_16x16x32_bf16 v[88:91], v[162:165], v[202:205], v[88:91]
	v_mfma_f32_16x16x32_bf16 v[76:79], v[154:157], v[210:213], v[76:79]
	v_mfma_f32_16x16x32_bf16 v[72:75], v[162:165], v[210:213], v[72:75]
	v_mfma_f32_16x16x32_bf16 v[118:121], v[166:169], v[182:185], v[118:121]
	v_mfma_f32_16x16x32_bf16 v[114:117], v[174:177], v[182:185], v[114:117]
	v_mfma_f32_16x16x32_bf16 v[102:105], v[166:169], v[190:193], v[102:105]
	v_mfma_f32_16x16x32_bf16 v[98:101], v[174:177], v[190:193], v[98:101]
	v_mfma_f32_16x16x32_bf16 v[84:87], v[166:169], v[198:201], v[84:87]
	v_mfma_f32_16x16x32_bf16 v[80:83], v[174:177], v[198:201], v[80:83]
	v_mfma_f32_16x16x32_bf16 v[68:71], v[166:169], v[206:209], v[68:71]
	v_mfma_f32_16x16x32_bf16 v[64:67], v[174:177], v[206:209], v[64:67]
	v_mfma_f32_16x16x32_bf16 v[118:121], v[170:173], v[186:189], v[118:121]
	v_mfma_f32_16x16x32_bf16 v[114:117], v[178:181], v[186:189], v[114:117]
	v_mfma_f32_16x16x32_bf16 v[102:105], v[170:173], v[194:197], v[102:105]
	v_mfma_f32_16x16x32_bf16 v[98:101], v[178:181], v[194:197], v[98:101]
	v_mfma_f32_16x16x32_bf16 v[84:87], v[170:173], v[202:205], v[84:87]
	v_mfma_f32_16x16x32_bf16 v[80:83], v[178:181], v[202:205], v[80:83]
	v_mfma_f32_16x16x32_bf16 v[68:71], v[170:173], v[210:213], v[68:71]
	v_mfma_f32_16x16x32_bf16 v[64:67], v[178:181], v[210:213], v[64:67]
	s_barrier
	s_mov_b32 m0, s79
	ds_read_b128 v[182:185], v149 offset:16384
	ds_read_b128 v[186:189], v149 offset:17408
	ds_read_b128 v[190:193], v149 offset:18432
	ds_read_b128 v[194:197], v149 offset:19456
	ds_read_b128 v[198:201], v149 offset:20480
	ds_read_b128 v[202:205], v149 offset:21504
	ds_read_b128 v[206:209], v149 offset:22528
	ds_read_b128 v[210:213], v149 offset:23552
	s_nop 0
	global_load_lds_dwordx4 v134, s[20:21]
	s_mov_b32 m0, s75
	s_nop 0
	global_load_lds_dwordx4 v137, s[20:21]
	s_mov_b32 m0, s76
	s_nop 0
	global_load_lds_dwordx4 v134, s[24:25]
	s_mov_b32 m0, s74
	s_nop 0
	global_load_lds_dwordx4 v137, s[24:25]
	s_mov_b32 m0, s60
	s_nop 0
	global_load_lds_dwordx4 v132, s[4:5]
	s_mov_b32 m0, s61
	s_nop 0
	global_load_lds_dwordx4 v135, s[4:5]
	s_waitcnt vmcnt(8)
	s_waitcnt lgkmcnt(0)
	s_barrier
; #define PG8_STAGE(bufoff, gbase, voff) do { _Pragma("unroll") for (int _i = 0; _i < 2; ++_i) \
;         __builtin_amdgcn_global_load_lds((const __attribute__((address_space(1))) unsigned*)((const __attribute__((address_space(1))) char*)(gbase) + (unsigned)lnd_v((int)(voff)[_i])), (LAS unsigned*)(lds + (bufoff) + ldsw + _i * 8192), 16, 0, 0); } while (0)
; #define PG8_LDA(dst, b, h) do { _Pragma("unroll") for (int m = 0; m < 4; ++m) _Pragma("unroll") for (int k = 0; k < 2; ++k) dst[m][k] = *(const LAS bf16x8*)(lds + PG8_SA(b, h) + aoff + m * 2048 + k * 1024); } while (0)
; #define PG8_LDB(dst, b, h) do { _Pragma("unroll") for (int n = 0; n < 2; ++n) _Pragma("unroll") for (int k = 0; k < 2; ++k) dst[n][k] = *(const LAS bf16x8*)(lds + PG8_SB(b, h) + boff + n * 2048 + k * 1024); } while (0)
; #define PG8_MMA(ai, bj, At, Bt) do { __builtin_amdgcn_s_setprio(1); _Pragma("unroll") for (int m = 0; m < 4; ++m) _Pragma("unroll") for (int n = 0; n < 2; ++n) _Pragma("unroll") for (int k = 0; k < 2; ++k) \
;         acc[ai][bj][m][n] = __builtin_amdgcn_mfma_f32_16x16x32_bf16(Bt[n][k], At[m][k], acc[ai][bj][m][n], 0, 0, 0); __builtin_amdgcn_s_setprio(0); } while (0)
; #define PG8_WAIT_V(n) asm volatile("s_waitcnt vmcnt(" #n ")" ::: "memory")
; #define PG8_WAIT_L(n) asm volatile("s_waitcnt lgkmcnt(" #n ")" ::: "memory")
; #define PG8_BAR __builtin_amdgcn_s_barrier()
; #define PG8_SCHED __builtin_amdgcn_sched_barrier(0)
; template <class Desc, class Epi>
; __device__ __forceinline__ void gemm_phase(const int wv_, LAS unsigned char* lds, const Desc& d, const Epi& E) {
;     ...
;             PG8_WAIT_V(8); PG8_WAIT_L(0); PG8_BAR; PG8_MMA(1, 0, At, B0); PG8_MMA(1, 1, At, B1); PG8_BAR; PG8_SCHED;
;             PG8_LDB(B0, 1, 0); PG8_LDB(B1, 1, 1); PG8_SCHED; PG8_LDA(At, 1, 0); PG8_STAGE(PG8_SA(0, 1), a2, sA1);
;             PG8_WAIT_V(8); PG8_WAIT_L(0); PG8_BAR; PG8_MMA(0, 0, At, B0); PG8_MMA(0, 1, At, B1); PG8_BAR; PG8_SCHED;
	v_mfma_f32_16x16x32_bf16 v[60:63], v[150:153], v[182:185], v[60:63]
	v_mfma_f32_16x16x32_bf16 v[56:59], v[158:161], v[182:185], v[56:59]
	v_mfma_f32_16x16x32_bf16 v[44:47], v[150:153], v[190:193], v[44:47]
	v_mfma_f32_16x16x32_bf16 v[32:35], v[158:161], v[190:193], v[32:35]
	v_mfma_f32_16x16x32_bf16 v[16:19], v[150:153], v[198:201], v[16:19]
	v_mfma_f32_16x16x32_bf16 v[8:11], v[158:161], v[198:201], v[8:11]
	v_mfma_f32_16x16x32_bf16 v[4:7], v[150:153], v[206:209], v[4:7]
	v_mfma_f32_16x16x32_bf16 v[0:3], v[158:161], v[206:209], v[0:3]
	v_mfma_f32_16x16x32_bf16 v[60:63], v[154:157], v[186:189], v[60:63]
	v_mfma_f32_16x16x32_bf16 v[56:59], v[162:165], v[186:189], v[56:59]
	v_mfma_f32_16x16x32_bf16 v[44:47], v[154:157], v[194:197], v[44:47]
	v_mfma_f32_16x16x32_bf16 v[32:35], v[162:165], v[194:197], v[32:35]
	v_mfma_f32_16x16x32_bf16 v[16:19], v[154:157], v[202:205], v[16:19]
	v_mfma_f32_16x16x32_bf16 v[8:11], v[162:165], v[202:205], v[8:11]
	v_mfma_f32_16x16x32_bf16 v[4:7], v[154:157], v[210:213], v[4:7]
	v_mfma_f32_16x16x32_bf16 v[0:3], v[162:165], v[210:213], v[0:3]
	v_mfma_f32_16x16x32_bf16 v[52:55], v[166:169], v[182:185], v[52:55]
	v_mfma_f32_16x16x32_bf16 v[48:51], v[174:177], v[182:185], v[48:51]
	v_mfma_f32_16x16x32_bf16 v[28:31], v[166:169], v[190:193], v[28:31]
	v_mfma_f32_16x16x32_bf16 v[12:15], v[174:177], v[190:193], v[12:15]
	v_mfma_f32_16x16x32_bf16 v[36:39], v[166:169], v[198:201], v[36:39]
	v_mfma_f32_16x16x32_bf16 v[40:43], v[174:177], v[198:201], v[40:43]
	v_mfma_f32_16x16x32_bf16 v[20:23], v[166:169], v[206:209], v[20:23]
	v_mfma_f32_16x16x32_bf16 v[24:27], v[174:177], v[206:209], v[24:27]
	v_mfma_f32_16x16x32_bf16 v[52:55], v[170:173], v[186:189], v[52:55]
	v_mfma_f32_16x16x32_bf16 v[48:51], v[178:181], v[186:189], v[48:51]
	v_mfma_f32_16x16x32_bf16 v[28:31], v[170:173], v[194:197], v[28:31]
	v_mfma_f32_16x16x32_bf16 v[12:15], v[178:181], v[194:197], v[12:15]
	v_mfma_f32_16x16x32_bf16 v[36:39], v[170:173], v[202:205], v[36:39]
	v_mfma_f32_16x16x32_bf16 v[40:43], v[178:181], v[202:205], v[40:43]
	v_mfma_f32_16x16x32_bf16 v[20:23], v[170:173], v[210:213], v[20:23]
	v_mfma_f32_16x16x32_bf16 v[24:27], v[178:181], v[210:213], v[24:27]
	s_barrier
	v_add_u32_e32 v96, s73, v139
	ds_read_b128 v[150:153], v96
	ds_read_b128 v[154:157], v96 offset:1024
	ds_read_b128 v[158:161], v96 offset:2048
	ds_read_b128 v[162:165], v96 offset:3072
	v_add_u32_e32 v96, s72, v139
	ds_read_b128 v[166:169], v96
	ds_read_b128 v[170:173], v96 offset:1024
	ds_read_b128 v[174:177], v96 offset:2048
	ds_read_b128 v[178:181], v96 offset:3072
	s_mov_b32 m0, s63
	ds_read_b128 v[182:185], v149 offset:32768
	ds_read_b128 v[186:189], v149 offset:33792
	ds_read_b128 v[190:193], v149 offset:34816
	ds_read_b128 v[194:197], v149 offset:35840
	ds_read_b128 v[198:201], v149 offset:36864
	ds_read_b128 v[202:205], v149 offset:37888
	ds_read_b128 v[206:209], v149 offset:38912
	ds_read_b128 v[210:213], v149 offset:39936
	s_nop 0
	global_load_lds_dwordx4 v133, s[4:5]
	s_mov_b32 m0, s64
	s_nop 0
	global_load_lds_dwordx4 v136, s[4:5]
	s_waitcnt vmcnt(8)
	s_waitcnt lgkmcnt(0)
	s_barrier
	v_mfma_f32_16x16x32_bf16 v[126:129], v[150:153], v[182:185], v[126:129]
	v_mfma_f32_16x16x32_bf16 v[122:125], v[158:161], v[182:185], v[122:125]
	v_mfma_f32_16x16x32_bf16 v[110:113], v[150:153], v[190:193], v[110:113]
	v_mfma_f32_16x16x32_bf16 v[106:109], v[158:161], v[190:193], v[106:109]
	v_mfma_f32_16x16x32_bf16 v[92:95], v[150:153], v[198:201], v[92:95]
	v_mfma_f32_16x16x32_bf16 v[88:91], v[158:161], v[198:201], v[88:91]
	v_mfma_f32_16x16x32_bf16 v[76:79], v[150:153], v[206:209], v[76:79]
	v_mfma_f32_16x16x32_bf16 v[72:75], v[158:161], v[206:209], v[72:75]
	v_mfma_f32_16x16x32_bf16 v[126:129], v[154:157], v[186:189], v[126:129]
	v_mfma_f32_16x16x32_bf16 v[122:125], v[162:165], v[186:189], v[122:125]
	v_mfma_f32_16x16x32_bf16 v[110:113], v[154:157], v[194:197], v[110:113]
	v_mfma_f32_16x16x32_bf16 v[106:109], v[162:165], v[194:197], v[106:109]
	v_mfma_f32_16x16x32_bf16 v[92:95], v[154:157], v[202:205], v[92:95]
	v_mfma_f32_16x16x32_bf16 v[88:91], v[162:165], v[202:205], v[88:91]
	v_mfma_f32_16x16x32_bf16 v[76:79], v[154:157], v[210:213], v[76:79]
	v_mfma_f32_16x16x32_bf16 v[72:75], v[162:165], v[210:213], v[72:75]
	v_mfma_f32_16x16x32_bf16 v[118:121], v[166:169], v[182:185], v[118:121]
	v_mfma_f32_16x16x32_bf16 v[114:117], v[174:177], v[182:185], v[114:117]
	v_mfma_f32_16x16x32_bf16 v[102:105], v[166:169], v[190:193], v[102:105]
	v_mfma_f32_16x16x32_bf16 v[98:101], v[174:177], v[190:193], v[98:101]
	v_mfma_f32_16x16x32_bf16 v[84:87], v[166:169], v[198:201], v[84:87]
	v_mfma_f32_16x16x32_bf16 v[80:83], v[174:177], v[198:201], v[80:83]
	v_mfma_f32_16x16x32_bf16 v[68:71], v[166:169], v[206:209], v[68:71]
	v_mfma_f32_16x16x32_bf16 v[64:67], v[174:177], v[206:209], v[64:67]
	v_mfma_f32_16x16x32_bf16 v[118:121], v[170:173], v[186:189], v[118:121]
	v_mfma_f32_16x16x32_bf16 v[114:117], v[178:181], v[186:189], v[114:117]
	v_mfma_f32_16x16x32_bf16 v[102:105], v[170:173], v[194:197], v[102:105]
	v_mfma_f32_16x16x32_bf16 v[98:101], v[178:181], v[194:197], v[98:101]
	v_mfma_f32_16x16x32_bf16 v[84:87], v[170:173], v[202:205], v[84:87]
	v_mfma_f32_16x16x32_bf16 v[80:83], v[178:181], v[202:205], v[80:83]
	v_mfma_f32_16x16x32_bf16 v[68:71], v[170:173], v[210:213], v[68:71]
	v_mfma_f32_16x16x32_bf16 v[64:67], v[178:181], v[210:213], v[64:67]
	s_barrier
; #define PG8_STAGE(bufoff, gbase, voff) do { _Pragma("unroll") for (int _i = 0; _i < 2; ++_i) \
;         __builtin_amdgcn_global_load_lds((const __attribute__((address_space(1))) unsigned*)((const __attribute__((address_space(1))) char*)(gbase) + (unsigned)lnd_v((int)(voff)[_i])), (LAS unsigned*)(lds + (bufoff) + ldsw + _i * 8192), 16, 0, 0); } while (0)
; #define PG8_LDA(dst, b, h) do { _Pragma("unroll") for (int m = 0; m < 4; ++m) _Pragma("unroll") for (int k = 0; k < 2; ++k) dst[m][k] = *(const LAS bf16x8*)(lds + PG8_SA(b, h) + aoff + m * 2048 + k * 1024); } while (0)
; #define PG8_MMA(ai, bj, At, Bt) do { __builtin_amdgcn_s_setprio(1); _Pragma("unroll") for (int m = 0; m < 4; ++m) _Pragma("unroll") for (int n = 0; n < 2; ++n) _Pragma("unroll") for (int k = 0; k < 2; ++k) \
;         acc[ai][bj][m][n] = __builtin_amdgcn_mfma_f32_16x16x32_bf16(Bt[n][k], At[m][k], acc[ai][bj][m][n], 0, 0, 0); __builtin_amdgcn_s_setprio(0); } while (0)
; #define PG8_WAIT_V(n) asm volatile("s_waitcnt vmcnt(" #n ")" ::: "memory")
; #define PG8_WAIT_L(n) asm volatile("s_waitcnt lgkmcnt(" #n ")" ::: "memory")
; #define PG8_BAR __builtin_amdgcn_s_barrier()
; #define PG8_SCHED __builtin_amdgcn_sched_barrier(0)
; template <class Desc, class Epi>
; __device__ __forceinline__ void gemm_phase(const int wv_, LAS unsigned char* lds, const Desc& d, const Epi& E) {
;     ...
;             PG8_LDA(At, 1, 1); PG8_STAGE(PG8_SB(1, 0), b3, voffB); PG8_STAGE(PG8_SB(1, 1), b3 + hstepB, voffB); PG8_STAGE(PG8_SA(1, 0), a3, sA0);
;             PG8_WAIT_V(8); PG8_WAIT_L(0); PG8_BAR; PG8_MMA(1, 0, At, B0); PG8_MMA(1, 1, At, B1); PG8_BAR; PG8_SCHED;
;         }
;         if (wr == 0) PG8_BAR;
	v_mov_b32_e32 v96, v134
	ds_read_b128 v[182:185], v149 offset:49152
	ds_read_b128 v[186:189], v149 offset:50176
	ds_read_b128 v[190:193], v149 offset:51200
	ds_read_b128 v[194:197], v149 offset:52224
	ds_read_b128 v[198:201], v149 offset:53248
	ds_read_b128 v[202:205], v149 offset:54272
	ds_read_b128 v[206:209], v149 offset:55296
	ds_read_b128 v[210:213], v149 offset:56320
	s_mov_b32 m0, s71
	v_lshl_add_u64 v[130:131], s[20:21], 0, v[96:97]
	v_lshl_add_u64 v[130:131], v[130:131], 0, s[30:31]
	v_mov_b32_e32 v96, v137
	global_load_lds_dwordx4 v[130:131], off
	s_mov_b32 m0, s29
	v_lshl_add_u64 v[130:131], s[20:21], 0, v[96:97]
	v_lshl_add_u64 v[130:131], v[130:131], 0, s[30:31]
	global_load_lds_dwordx4 v[130:131], off
	s_mov_b32 m0, s78
	s_nop 0
	global_load_lds_dwordx4 v134, s[22:23]
	s_mov_b32 m0, s77
	s_nop 0
	global_load_lds_dwordx4 v137, s[22:23]
	v_mov_b32_e32 v96, v132
	s_mov_b32 m0, s65
	v_lshl_add_u64 v[130:131], s[4:5], 0, v[96:97]
	v_lshl_add_u64 v[130:131], v[130:131], 0, s[30:31]
	v_mov_b32_e32 v96, v135
	global_load_lds_dwordx4 v[130:131], off
	s_mov_b32 m0, s66
	v_lshl_add_u64 v[130:131], s[4:5], 0, v[96:97]
	v_lshl_add_u64 v[130:131], v[130:131], 0, s[30:31]
	global_load_lds_dwordx4 v[130:131], off
	s_waitcnt vmcnt(8)
	s_waitcnt lgkmcnt(0)
	s_barrier
	v_mfma_f32_16x16x32_bf16 v[60:63], v[150:153], v[182:185], v[60:63]
	v_mfma_f32_16x16x32_bf16 v[56:59], v[158:161], v[182:185], v[56:59]
	v_mfma_f32_16x16x32_bf16 v[44:47], v[150:153], v[190:193], v[44:47]
	v_mfma_f32_16x16x32_bf16 v[32:35], v[158:161], v[190:193], v[32:35]
	v_mfma_f32_16x16x32_bf16 v[16:19], v[150:153], v[198:201], v[16:19]
	v_mfma_f32_16x16x32_bf16 v[8:11], v[158:161], v[198:201], v[8:11]
	v_mfma_f32_16x16x32_bf16 v[4:7], v[150:153], v[206:209], v[4:7]
	v_mfma_f32_16x16x32_bf16 v[0:3], v[158:161], v[206:209], v[0:3]
	v_mfma_f32_16x16x32_bf16 v[60:63], v[154:157], v[186:189], v[60:63]
	v_mfma_f32_16x16x32_bf16 v[56:59], v[162:165], v[186:189], v[56:59]
	v_mfma_f32_16x16x32_bf16 v[44:47], v[154:157], v[194:197], v[44:47]
	v_mfma_f32_16x16x32_bf16 v[32:35], v[162:165], v[194:197], v[32:35]
	v_mfma_f32_16x16x32_bf16 v[16:19], v[154:157], v[202:205], v[16:19]
	v_mfma_f32_16x16x32_bf16 v[8:11], v[162:165], v[202:205], v[8:11]
	v_mfma_f32_16x16x32_bf16 v[4:7], v[154:157], v[210:213], v[4:7]
	v_mfma_f32_16x16x32_bf16 v[0:3], v[162:165], v[210:213], v[0:3]
	v_mfma_f32_16x16x32_bf16 v[52:55], v[166:169], v[182:185], v[52:55]
	v_mfma_f32_16x16x32_bf16 v[48:51], v[174:177], v[182:185], v[48:51]
	v_mfma_f32_16x16x32_bf16 v[28:31], v[166:169], v[190:193], v[28:31]
	v_mfma_f32_16x16x32_bf16 v[12:15], v[174:177], v[190:193], v[12:15]
	v_mfma_f32_16x16x32_bf16 v[36:39], v[166:169], v[198:201], v[36:39]
	v_mfma_f32_16x16x32_bf16 v[40:43], v[174:177], v[198:201], v[40:43]
	v_mfma_f32_16x16x32_bf16 v[20:23], v[166:169], v[206:209], v[20:23]
	v_mfma_f32_16x16x32_bf16 v[24:27], v[174:177], v[206:209], v[24:27]
	v_mfma_f32_16x16x32_bf16 v[52:55], v[170:173], v[186:189], v[52:55]
	v_mfma_f32_16x16x32_bf16 v[48:51], v[178:181], v[186:189], v[48:51]
	v_mfma_f32_16x16x32_bf16 v[28:31], v[170:173], v[194:197], v[28:31]
	v_mfma_f32_16x16x32_bf16 v[12:15], v[178:181], v[194:197], v[12:15]
	v_mfma_f32_16x16x32_bf16 v[36:39], v[170:173], v[202:205], v[36:39]
	v_mfma_f32_16x16x32_bf16 v[40:43], v[178:181], v[202:205], v[40:43]
	v_mfma_f32_16x16x32_bf16 v[20:23], v[170:173], v[210:213], v[20:23]
	v_mfma_f32_16x16x32_bf16 v[24:27], v[178:181], v[210:213], v[24:27]
	s_barrier
	s_movk_i32 s22, 0x100
	s_andn2_b64 vcc, exec, s[2:3]
	s_mov_b64 s[20:21], -1
	s_mov_b64 s[2:3], 0
	s_cbranch_vccz .LBB0_937
	s_and_b64 vcc, exec, s[40:41]
	s_cbranch_vccz .LBB0_940
	s_barrier

; #define PG8_STAGE(bufoff, gbase, voff) do { _Pragma("unroll") for (int _i = 0; _i < 2; ++_i) \
;         __builtin_amdgcn_global_load_lds((const __attribute__((address_space(1))) unsigned*)((const __attribute__((address_space(1))) char*)(gbase) + (unsigned)lnd_v((int)(voff)[_i])), (LAS unsigned*)(lds + (bufoff) + ldsw + _i * 8192), 16, 0, 0); } while (0)
; #define PG8_LDA(dst, b, h) do { _Pragma("unroll") for (int m = 0; m < 4; ++m) _Pragma("unroll") for (int k = 0; k < 2; ++k) dst[m][k] = *(const LAS bf16x8*)(lds + PG8_SA(b, h) + aoff + m * 2048 + k * 1024); } while (0)
; #define PG8_LDB(dst, b, h) do { _Pragma("unroll") for (int n = 0; n < 2; ++n) _Pragma("unroll") for (int k = 0; k < 2; ++k) dst[n][k] = *(const LAS bf16x8*)(lds + PG8_SB(b, h) + boff + n * 2048 + k * 1024); } while (0)
; #define PG8_MMA(ai, bj, At, Bt) do { __builtin_amdgcn_s_setprio(1); _Pragma("unroll") for (int m = 0; m < 4; ++m) _Pragma("unroll") for (int n = 0; n < 2; ++n) _Pragma("unroll") for (int k = 0; k < 2; ++k) \
;         acc[ai][bj][m][n] = __builtin_amdgcn_mfma_f32_16x16x32_bf16(Bt[n][k], At[m][k], acc[ai][bj][m][n], 0, 0, 0); __builtin_amdgcn_s_setprio(0); } while (0)
; #define PG8_WAIT_V(n) asm volatile("s_waitcnt vmcnt(" #n ")" ::: "memory")
; #define PG8_WAIT_L(n) asm volatile("s_waitcnt lgkmcnt(" #n ")" ::: "memory")
; #define PG8_BAR __builtin_amdgcn_s_barrier()
; #define PG8_SCHED __builtin_amdgcn_sched_barrier(0)
; template <class Desc, class Epi>
; __device__ __forceinline__ void gemm_phase(const int wv_, LAS unsigned char* lds, const Desc& d, const Epi& E) {
;     ...
;             PG8_LDB(B0, 0, 0); PG8_LDB(B1, 0, 1); PG8_SCHED; PG8_LDA(At, 0, 0); PG8_STAGE(PG8_SA(1, 1), a1, voffA1);
;             PG8_WAIT_V(8); PG8_WAIT_L(0); PG8_BAR; PG8_MMA(0, 0, At, B0); PG8_MMA(0, 1, At, B1); PG8_BAR; PG8_SCHED;
;             PG8_LDA(At, 0, 1); PG8_STAGE(PG8_SB(0, 0), b2, voffB); PG8_STAGE(PG8_SB(0, 1), b2 + hstepB, voffB); PG8_STAGE(PG8_SA(0, 0), a2, sA0);
;             PG8_WAIT_V(8); PG8_WAIT_L(0); PG8_BAR; PG8_MMA(1, 0, At, B0); PG8_MMA(1, 1, At, B1); PG8_BAR; PG8_SCHED;
.LBB0_1075:
	s_add_u32 s4, s2, 0x80
	s_addc_u32 s5, s3, 0
	s_add_i32 s47, 0, 0x10000
	s_cmp_eq_u32 s29, 12
	s_cselect_b32 s5, s51, s5
	s_cselect_b32 s4, s50, s4
	v_add_u32_e32 v96, s47, v226
	s_cselect_b32 s21, s53, s26
	s_cselect_b32 s20, s52, s1
	s_add_i32 s49, 0, 0x14000
	ds_read_b128 v[118:121], v96
	ds_read_b128 v[126:129], v96 offset:1024
	ds_read_b128 v[130:133], v96 offset:2048
	ds_read_b128 v[134:137], v96 offset:3072
	v_add_u32_e32 v96, s49, v226
	ds_read_b128 v[142:145], v96
	ds_read_b128 v[150:153], v96 offset:1024
	ds_read_b128 v[154:157], v96 offset:2048
	ds_read_b128 v[158:161], v96 offset:3072
	ds_read_b128 v[162:165], v231
	ds_read_b128 v[166:169], v231 offset:1024
	ds_read_b128 v[170:173], v231 offset:2048
	ds_read_b128 v[174:177], v231 offset:3072
	ds_read_b128 v[178:181], v231 offset:4096
	ds_read_b128 v[182:185], v231 offset:5120
	ds_read_b128 v[186:189], v231 offset:6144
	ds_read_b128 v[190:193], v231 offset:7168
	s_add_i32 m0, s60, 0xc000
	s_nop 0
	global_load_lds_dwordx4 v220, s[2:3]
	s_add_i32 m0, s60, 0xe000
	s_nop 0
	global_load_lds_dwordx4 v223, s[2:3]
	s_waitcnt vmcnt(8)
	s_waitcnt lgkmcnt(0)
	s_barrier
	v_mfma_f32_16x16x32_bf16 v[146:149], v[118:121], v[162:165], v[146:149]
	v_mfma_f32_16x16x32_bf16 v[138:141], v[130:133], v[162:165], v[138:141]
	v_mfma_f32_16x16x32_bf16 v[110:113], v[118:121], v[170:173], v[110:113]
	v_mfma_f32_16x16x32_bf16 v[106:109], v[130:133], v[170:173], v[106:109]
	v_mfma_f32_16x16x32_bf16 v[92:95], v[118:121], v[178:181], v[92:95]
	v_mfma_f32_16x16x32_bf16 v[88:91], v[130:133], v[178:181], v[88:91]
	v_mfma_f32_16x16x32_bf16 v[76:79], v[118:121], v[186:189], v[76:79]
	v_mfma_f32_16x16x32_bf16 v[72:75], v[130:133], v[186:189], v[72:75]
	v_mfma_f32_16x16x32_bf16 v[146:149], v[126:129], v[166:169], v[146:149]
	v_mfma_f32_16x16x32_bf16 v[138:141], v[134:137], v[166:169], v[138:141]
	v_mfma_f32_16x16x32_bf16 v[110:113], v[126:129], v[174:177], v[110:113]
	v_mfma_f32_16x16x32_bf16 v[106:109], v[134:137], v[174:177], v[106:109]
	v_mfma_f32_16x16x32_bf16 v[92:95], v[126:129], v[182:185], v[92:95]
	v_mfma_f32_16x16x32_bf16 v[88:91], v[134:137], v[182:185], v[88:91]
	v_mfma_f32_16x16x32_bf16 v[76:79], v[126:129], v[190:193], v[76:79]
	v_mfma_f32_16x16x32_bf16 v[72:75], v[134:137], v[190:193], v[72:75]
	v_mfma_f32_16x16x32_bf16 v[122:125], v[142:145], v[162:165], v[122:125]
	v_mfma_f32_16x16x32_bf16 v[114:117], v[154:157], v[162:165], v[114:117]
	v_mfma_f32_16x16x32_bf16 v[102:105], v[142:145], v[170:173], v[102:105]
	v_mfma_f32_16x16x32_bf16 v[98:101], v[154:157], v[170:173], v[98:101]
	v_mfma_f32_16x16x32_bf16 v[84:87], v[142:145], v[178:181], v[84:87]
	v_mfma_f32_16x16x32_bf16 v[80:83], v[154:157], v[178:181], v[80:83]
	v_mfma_f32_16x16x32_bf16 v[68:71], v[142:145], v[186:189], v[68:71]
	v_mfma_f32_16x16x32_bf16 v[64:67], v[154:157], v[186:189], v[64:67]
	v_mfma_f32_16x16x32_bf16 v[122:125], v[150:153], v[166:169], v[122:125]
	v_mfma_f32_16x16x32_bf16 v[114:117], v[158:161], v[166:169], v[114:117]
	v_mfma_f32_16x16x32_bf16 v[102:105], v[150:153], v[174:177], v[102:105]
	v_mfma_f32_16x16x32_bf16 v[98:101], v[158:161], v[174:177], v[98:101]
	v_mfma_f32_16x16x32_bf16 v[84:87], v[150:153], v[182:185], v[84:87]
	v_mfma_f32_16x16x32_bf16 v[80:83], v[158:161], v[182:185], v[80:83]
	v_mfma_f32_16x16x32_bf16 v[68:71], v[150:153], v[190:193], v[68:71]
	v_mfma_f32_16x16x32_bf16 v[64:67], v[158:161], v[190:193], v[64:67]
	s_barrier
	s_add_i32 s47, s47, s59
	ds_read_b128 v[162:165], v231 offset:16384
	ds_read_b128 v[166:169], v231 offset:17408
	ds_read_b128 v[170:173], v231 offset:18432
	ds_read_b128 v[174:177], v231 offset:19456
	ds_read_b128 v[178:181], v231 offset:20480
	ds_read_b128 v[182:185], v231 offset:21504
	ds_read_b128 v[186:189], v231 offset:22528
	ds_read_b128 v[190:193], v231 offset:23552
	s_mov_b32 m0, s47
	s_nop 0
	global_load_lds_dwordx4 v221, s[20:21]
	s_add_i32 m0, s47, 0x2000
	s_add_u32 s70, s20, 0x40000
	global_load_lds_dwordx4 v224, s[20:21]
	s_addc_u32 s71, s21, 0
	s_add_i32 s47, s49, s59
	s_mov_b32 m0, s47
	s_nop 0
	global_load_lds_dwordx4 v221, s[70:71]
	s_add_i32 m0, s47, 0x2000
	s_nop 0
	global_load_lds_dwordx4 v224, s[70:71]
	s_mov_b32 m0, s60
	s_nop 0
	global_load_lds_dwordx4 v219, s[4:5]
	s_mov_b32 m0, s62
	s_nop 0
	global_load_lds_dwordx4 v222, s[4:5]
	s_waitcnt vmcnt(8)
	s_waitcnt lgkmcnt(0)
	s_barrier
	v_mfma_f32_16x16x32_bf16 v[60:63], v[118:121], v[162:165], v[60:63]
	v_mfma_f32_16x16x32_bf16 v[56:59], v[130:133], v[162:165], v[56:59]
	v_mfma_f32_16x16x32_bf16 v[44:47], v[118:121], v[170:173], v[44:47]
	v_mfma_f32_16x16x32_bf16 v[40:43], v[130:133], v[170:173], v[40:43]
	v_mfma_f32_16x16x32_bf16 v[20:23], v[118:121], v[178:181], v[20:23]
	v_mfma_f32_16x16x32_bf16 v[16:19], v[130:133], v[178:181], v[16:19]
	v_mfma_f32_16x16x32_bf16 v[4:7], v[118:121], v[186:189], v[4:7]
	v_mfma_f32_16x16x32_bf16 v[0:3], v[130:133], v[186:189], v[0:3]
	v_mfma_f32_16x16x32_bf16 v[60:63], v[126:129], v[166:169], v[60:63]
	v_mfma_f32_16x16x32_bf16 v[56:59], v[134:137], v[166:169], v[56:59]
	v_mfma_f32_16x16x32_bf16 v[44:47], v[126:129], v[174:177], v[44:47]
	v_mfma_f32_16x16x32_bf16 v[40:43], v[134:137], v[174:177], v[40:43]
	v_mfma_f32_16x16x32_bf16 v[20:23], v[126:129], v[182:185], v[20:23]
	v_mfma_f32_16x16x32_bf16 v[16:19], v[134:137], v[182:185], v[16:19]
	v_mfma_f32_16x16x32_bf16 v[4:7], v[126:129], v[190:193], v[4:7]
	v_mfma_f32_16x16x32_bf16 v[0:3], v[134:137], v[190:193], v[0:3]
	v_mfma_f32_16x16x32_bf16 v[52:55], v[142:145], v[162:165], v[52:55]
	v_mfma_f32_16x16x32_bf16 v[48:51], v[154:157], v[162:165], v[48:51]
	v_mfma_f32_16x16x32_bf16 v[36:39], v[142:145], v[170:173], v[36:39]
	v_mfma_f32_16x16x32_bf16 v[32:35], v[154:157], v[170:173], v[32:35]
	v_mfma_f32_16x16x32_bf16 v[28:31], v[142:145], v[178:181], v[28:31]
	v_mfma_f32_16x16x32_bf16 v[24:27], v[154:157], v[178:181], v[24:27]
	v_mfma_f32_16x16x32_bf16 v[12:15], v[142:145], v[186:189], v[12:15]
	v_mfma_f32_16x16x32_bf16 v[8:11], v[154:157], v[186:189], v[8:11]
	v_mfma_f32_16x16x32_bf16 v[52:55], v[150:153], v[166:169], v[52:55]
	v_mfma_f32_16x16x32_bf16 v[48:51], v[158:161], v[166:169], v[48:51]
	v_mfma_f32_16x16x32_bf16 v[36:39], v[150:153], v[174:177], v[36:39]
	v_mfma_f32_16x16x32_bf16 v[32:35], v[158:161], v[174:177], v[32:35]
	v_mfma_f32_16x16x32_bf16 v[28:31], v[150:153], v[182:185], v[28:31]
	v_mfma_f32_16x16x32_bf16 v[24:27], v[158:161], v[182:185], v[24:27]
	v_mfma_f32_16x16x32_bf16 v[12:15], v[150:153], v[190:193], v[12:15]
	v_mfma_f32_16x16x32_bf16 v[8:11], v[158:161], v[190:193], v[8:11]
	s_barrier
; #define PG8_STAGE(bufoff, gbase, voff) do { _Pragma("unroll") for (int _i = 0; _i < 2; ++_i) \
;         __builtin_amdgcn_global_load_lds((const __attribute__((address_space(1))) unsigned*)((const __attribute__((address_space(1))) char*)(gbase) + (unsigned)lnd_v((int)(voff)[_i])), (LAS unsigned*)(lds + (bufoff) + ldsw + _i * 8192), 16, 0, 0); } while (0)
; #define PG8_LDA(dst, b, h) do { _Pragma("unroll") for (int m = 0; m < 4; ++m) _Pragma("unroll") for (int k = 0; k < 2; ++k) dst[m][k] = *(const LAS bf16x8*)(lds + PG8_SA(b, h) + aoff + m * 2048 + k * 1024); } while (0)
; #define PG8_LDB(dst, b, h) do { _Pragma("unroll") for (int n = 0; n < 2; ++n) _Pragma("unroll") for (int k = 0; k < 2; ++k) dst[n][k] = *(const LAS bf16x8*)(lds + PG8_SB(b, h) + boff + n * 2048 + k * 1024); } while (0)
; #define PG8_MMA(ai, bj, At, Bt) do { __builtin_amdgcn_s_setprio(1); _Pragma("unroll") for (int m = 0; m < 4; ++m) _Pragma("unroll") for (int n = 0; n < 2; ++n) _Pragma("unroll") for (int k = 0; k < 2; ++k) \
;         acc[ai][bj][m][n] = __builtin_amdgcn_mfma_f32_16x16x32_bf16(Bt[n][k], At[m][k], acc[ai][bj][m][n], 0, 0, 0); __builtin_amdgcn_s_setprio(0); } while (0)
; #define PG8_WAIT_V(n) asm volatile("s_waitcnt vmcnt(" #n ")" ::: "memory")
; #define PG8_WAIT_L(n) asm volatile("s_waitcnt lgkmcnt(" #n ")" ::: "memory")
; #define PG8_BAR __builtin_amdgcn_s_barrier()
; #define PG8_SCHED __builtin_amdgcn_sched_barrier(0)
; template <class Desc, class Epi>
; __device__ __forceinline__ void gemm_phase(const int wv_, LAS unsigned char* lds, const Desc& d, const Epi& E) {
;     ...
;             PG8_LDB(B0, 1, 0); PG8_LDB(B1, 1, 1); PG8_SCHED; PG8_LDA(At, 1, 0); PG8_STAGE(PG8_SA(0, 1), a2, sA1);
;             PG8_WAIT_V(8); PG8_WAIT_L(0); PG8_BAR; PG8_MMA(0, 0, At, B0); PG8_MMA(0, 1, At, B1); PG8_BAR; PG8_SCHED;
	s_add_i32 s47, 0, 0x18000
	v_add_u32_e32 v96, s47, v226
	s_add_i32 s49, 0, 0x1c000
	ds_read_b128 v[118:121], v96
	ds_read_b128 v[126:129], v96 offset:1024
	ds_read_b128 v[130:133], v96 offset:2048
	ds_read_b128 v[134:137], v96 offset:3072
	v_add_u32_e32 v96, s49, v226
	ds_read_b128 v[142:145], v96
	ds_read_b128 v[150:153], v96 offset:1024
	ds_read_b128 v[154:157], v96 offset:2048
	ds_read_b128 v[158:161], v96 offset:3072
	s_mov_b32 m0, s63
	ds_read_b128 v[162:165], v231 offset:32768
	ds_read_b128 v[166:169], v231 offset:33792
	ds_read_b128 v[170:173], v231 offset:34816
	ds_read_b128 v[174:177], v231 offset:35840
	ds_read_b128 v[178:181], v231 offset:36864
	ds_read_b128 v[182:185], v231 offset:37888
	ds_read_b128 v[186:189], v231 offset:38912
	ds_read_b128 v[190:193], v231 offset:39936
	s_nop 0
	global_load_lds_dwordx4 v220, s[4:5]
	s_mov_b32 m0, s64
	s_nop 0
	global_load_lds_dwordx4 v223, s[4:5]
	s_waitcnt vmcnt(8)
	s_waitcnt lgkmcnt(0)
	s_barrier
	v_mfma_f32_16x16x32_bf16 v[146:149], v[118:121], v[162:165], v[146:149]
	v_mfma_f32_16x16x32_bf16 v[138:141], v[130:133], v[162:165], v[138:141]
	v_mfma_f32_16x16x32_bf16 v[110:113], v[118:121], v[170:173], v[110:113]
	v_mfma_f32_16x16x32_bf16 v[106:109], v[130:133], v[170:173], v[106:109]
	v_mfma_f32_16x16x32_bf16 v[92:95], v[118:121], v[178:181], v[92:95]
	v_mfma_f32_16x16x32_bf16 v[88:91], v[130:133], v[178:181], v[88:91]
	v_mfma_f32_16x16x32_bf16 v[76:79], v[118:121], v[186:189], v[76:79]
	v_mfma_f32_16x16x32_bf16 v[72:75], v[130:133], v[186:189], v[72:75]
	v_mfma_f32_16x16x32_bf16 v[146:149], v[126:129], v[166:169], v[146:149]
	v_mfma_f32_16x16x32_bf16 v[138:141], v[134:137], v[166:169], v[138:141]
	v_mfma_f32_16x16x32_bf16 v[110:113], v[126:129], v[174:177], v[110:113]
	v_mfma_f32_16x16x32_bf16 v[106:109], v[134:137], v[174:177], v[106:109]
	v_mfma_f32_16x16x32_bf16 v[92:95], v[126:129], v[182:185], v[92:95]
	v_mfma_f32_16x16x32_bf16 v[88:91], v[134:137], v[182:185], v[88:91]
	v_mfma_f32_16x16x32_bf16 v[76:79], v[126:129], v[190:193], v[76:79]
	v_mfma_f32_16x16x32_bf16 v[72:75], v[134:137], v[190:193], v[72:75]
	v_mfma_f32_16x16x32_bf16 v[122:125], v[142:145], v[162:165], v[122:125]
	v_mfma_f32_16x16x32_bf16 v[114:117], v[154:157], v[162:165], v[114:117]
	v_mfma_f32_16x16x32_bf16 v[102:105], v[142:145], v[170:173], v[102:105]
	v_mfma_f32_16x16x32_bf16 v[98:101], v[154:157], v[170:173], v[98:101]
	v_mfma_f32_16x16x32_bf16 v[84:87], v[142:145], v[178:181], v[84:87]
	v_mfma_f32_16x16x32_bf16 v[80:83], v[154:157], v[178:181], v[80:83]
	v_mfma_f32_16x16x32_bf16 v[68:71], v[142:145], v[186:189], v[68:71]
	v_mfma_f32_16x16x32_bf16 v[64:67], v[154:157], v[186:189], v[64:67]
	v_mfma_f32_16x16x32_bf16 v[122:125], v[150:153], v[166:169], v[122:125]
	v_mfma_f32_16x16x32_bf16 v[114:117], v[158:161], v[166:169], v[114:117]
	v_mfma_f32_16x16x32_bf16 v[102:105], v[150:153], v[174:177], v[102:105]
	v_mfma_f32_16x16x32_bf16 v[98:101], v[158:161], v[174:177], v[98:101]
	v_mfma_f32_16x16x32_bf16 v[84:87], v[150:153], v[182:185], v[84:87]
	v_mfma_f32_16x16x32_bf16 v[80:83], v[158:161], v[182:185], v[80:83]
	v_mfma_f32_16x16x32_bf16 v[68:71], v[150:153], v[190:193], v[68:71]
	v_mfma_f32_16x16x32_bf16 v[64:67], v[158:161], v[190:193], v[64:67]
	s_barrier
; #define PG8_STAGE(bufoff, gbase, voff) do { _Pragma("unroll") for (int _i = 0; _i < 2; ++_i) \
;         __builtin_amdgcn_global_load_lds((const __attribute__((address_space(1))) unsigned*)((const __attribute__((address_space(1))) char*)(gbase) + (unsigned)lnd_v((int)(voff)[_i])), (LAS unsigned*)(lds + (bufoff) + ldsw + _i * 8192), 16, 0, 0); } while (0)
; #define PG8_LDA(dst, b, h) do { _Pragma("unroll") for (int m = 0; m < 4; ++m) _Pragma("unroll") for (int k = 0; k < 2; ++k) dst[m][k] = *(const LAS bf16x8*)(lds + PG8_SA(b, h) + aoff + m * 2048 + k * 1024); } while (0)
; #define PG8_MMA(ai, bj, At, Bt) do { __builtin_amdgcn_s_setprio(1); _Pragma("unroll") for (int m = 0; m < 4; ++m) _Pragma("unroll") for (int n = 0; n < 2; ++n) _Pragma("unroll") for (int k = 0; k < 2; ++k) \
;         acc[ai][bj][m][n] = __builtin_amdgcn_mfma_f32_16x16x32_bf16(Bt[n][k], At[m][k], acc[ai][bj][m][n], 0, 0, 0); __builtin_amdgcn_s_setprio(0); } while (0)
; #define PG8_WAIT_V(n) asm volatile("s_waitcnt vmcnt(" #n ")" ::: "memory")
; #define PG8_WAIT_L(n) asm volatile("s_waitcnt lgkmcnt(" #n ")" ::: "memory")
; #define PG8_BAR __builtin_amdgcn_s_barrier()
; #define PG8_SCHED __builtin_amdgcn_sched_barrier(0)
; template <class Desc, class Epi>
; __device__ __forceinline__ void gemm_phase(const int wv_, LAS unsigned char* lds, const Desc& d, const Epi& E) {
;     ...
;             PG8_LDA(At, 1, 1); PG8_STAGE(PG8_SB(1, 0), b3, voffB); PG8_STAGE(PG8_SB(1, 1), b3 + hstepB, voffB); PG8_STAGE(PG8_SA(1, 0), a3, sA0);
;             PG8_WAIT_V(8); PG8_WAIT_L(0); PG8_BAR; PG8_MMA(1, 0, At, B0); PG8_MMA(1, 1, At, B1); PG8_BAR; PG8_SCHED;
;         }
;         if (wr == 0) PG8_BAR;
	v_mov_b32_e32 v96, v221
	ds_read_b128 v[162:165], v231 offset:49152
	ds_read_b128 v[166:169], v231 offset:50176
	ds_read_b128 v[170:173], v231 offset:51200
	ds_read_b128 v[174:177], v231 offset:52224
	ds_read_b128 v[178:181], v231 offset:53248
	ds_read_b128 v[182:185], v231 offset:54272
	ds_read_b128 v[186:189], v231 offset:55296
	ds_read_b128 v[190:193], v231 offset:56320
	s_add_i32 s47, s47, s59
	v_lshl_add_u64 v[194:195], s[20:21], 0, v[96:97]
	v_lshl_add_u64 v[194:195], v[194:195], 0, s[30:31]
	s_mov_b32 m0, s47
	v_mov_b32_e32 v96, v224
	global_load_lds_dwordx4 v[194:195], off
	s_add_i32 m0, s47, 0x2000
	s_nop 0
	v_lshl_add_u64 v[194:195], s[20:21], 0, v[96:97]
	s_add_u32 s20, s20, 0x40080
	v_lshl_add_u64 v[194:195], v[194:195], 0, s[30:31]
	s_addc_u32 s21, s21, 0
	s_add_i32 s47, s49, s59
	global_load_lds_dwordx4 v[194:195], off
	s_mov_b32 m0, s47
	s_nop 0
	global_load_lds_dwordx4 v221, s[20:21]
	s_add_i32 m0, s47, 0x2000
	s_nop 0
	global_load_lds_dwordx4 v224, s[20:21]
	v_mov_b32_e32 v96, v219
	s_mov_b32 m0, s66
	v_lshl_add_u64 v[194:195], s[4:5], 0, v[96:97]
	v_lshl_add_u64 v[194:195], v[194:195], 0, s[30:31]
	v_mov_b32_e32 v96, v222
	global_load_lds_dwordx4 v[194:195], off
	s_mov_b32 m0, s67
	v_lshl_add_u64 v[194:195], s[4:5], 0, v[96:97]
	v_lshl_add_u64 v[194:195], v[194:195], 0, s[30:31]
	global_load_lds_dwordx4 v[194:195], off
	s_waitcnt vmcnt(8)
	s_waitcnt lgkmcnt(0)
	s_barrier
	v_mfma_f32_16x16x32_bf16 v[60:63], v[118:121], v[162:165], v[60:63]
	v_mfma_f32_16x16x32_bf16 v[56:59], v[130:133], v[162:165], v[56:59]
	v_mfma_f32_16x16x32_bf16 v[44:47], v[118:121], v[170:173], v[44:47]
	v_mfma_f32_16x16x32_bf16 v[40:43], v[130:133], v[170:173], v[40:43]
	v_mfma_f32_16x16x32_bf16 v[20:23], v[118:121], v[178:181], v[20:23]
	v_mfma_f32_16x16x32_bf16 v[16:19], v[130:133], v[178:181], v[16:19]
	v_mfma_f32_16x16x32_bf16 v[4:7], v[118:121], v[186:189], v[4:7]
	v_mfma_f32_16x16x32_bf16 v[0:3], v[130:133], v[186:189], v[0:3]
	v_mfma_f32_16x16x32_bf16 v[60:63], v[126:129], v[166:169], v[60:63]
	v_mfma_f32_16x16x32_bf16 v[56:59], v[134:137], v[166:169], v[56:59]
	v_mfma_f32_16x16x32_bf16 v[44:47], v[126:129], v[174:177], v[44:47]
	v_mfma_f32_16x16x32_bf16 v[40:43], v[134:137], v[174:177], v[40:43]
	v_mfma_f32_16x16x32_bf16 v[20:23], v[126:129], v[182:185], v[20:23]
	v_mfma_f32_16x16x32_bf16 v[16:19], v[134:137], v[182:185], v[16:19]
	v_mfma_f32_16x16x32_bf16 v[4:7], v[126:129], v[190:193], v[4:7]
	v_mfma_f32_16x16x32_bf16 v[0:3], v[134:137], v[190:193], v[0:3]
	v_mfma_f32_16x16x32_bf16 v[52:55], v[142:145], v[162:165], v[52:55]
	v_mfma_f32_16x16x32_bf16 v[48:51], v[154:157], v[162:165], v[48:51]
	v_mfma_f32_16x16x32_bf16 v[36:39], v[142:145], v[170:173], v[36:39]
	v_mfma_f32_16x16x32_bf16 v[32:35], v[154:157], v[170:173], v[32:35]
	v_mfma_f32_16x16x32_bf16 v[28:31], v[142:145], v[178:181], v[28:31]
	v_mfma_f32_16x16x32_bf16 v[24:27], v[154:157], v[178:181], v[24:27]
	v_mfma_f32_16x16x32_bf16 v[12:15], v[142:145], v[186:189], v[12:15]
	v_mfma_f32_16x16x32_bf16 v[8:11], v[154:157], v[186:189], v[8:11]
	v_mfma_f32_16x16x32_bf16 v[52:55], v[150:153], v[166:169], v[52:55]
	v_mfma_f32_16x16x32_bf16 v[48:51], v[158:161], v[166:169], v[48:51]
	v_mfma_f32_16x16x32_bf16 v[36:39], v[150:153], v[174:177], v[36:39]
	v_mfma_f32_16x16x32_bf16 v[32:35], v[158:161], v[174:177], v[32:35]
	v_mfma_f32_16x16x32_bf16 v[28:31], v[150:153], v[182:185], v[28:31]
	v_mfma_f32_16x16x32_bf16 v[24:27], v[158:161], v[182:185], v[24:27]
	v_mfma_f32_16x16x32_bf16 v[12:15], v[150:153], v[190:193], v[12:15]
	v_mfma_f32_16x16x32_bf16 v[8:11], v[158:161], v[190:193], v[8:11]
	s_barrier
	s_add_i32 s29, s29, 2
	s_add_u32 s2, s2, 0x100
	s_addc_u32 s3, s3, 0
	s_add_u32 s1, s1, 0x100
	s_addc_u32 s26, s26, 0
	s_cmp_gt_u32 s29, 13
	s_cbranch_scc0 .LBB0_1075
	s_and_b64 vcc, exec, s[44:45]
	s_cbranch_vccz .LBB0_1078
	s_barrier

; #define PG8_STAGE(bufoff, gbase, voff) do { _Pragma("unroll") for (int _i = 0; _i < 2; ++_i) \
;         __builtin_amdgcn_global_load_lds((const __attribute__((address_space(1))) unsigned*)((const __attribute__((address_space(1))) char*)(gbase) + (unsigned)lnd_v((int)(voff)[_i])), (LAS unsigned*)(lds + (bufoff) + ldsw + _i * 8192), 16, 0, 0); } while (0)
; #define PG8_LDA(dst, b, h) do { _Pragma("unroll") for (int m = 0; m < 4; ++m) _Pragma("unroll") for (int k = 0; k < 2; ++k) dst[m][k] = *(const LAS bf16x8*)(lds + PG8_SA(b, h) + aoff + m * 2048 + k * 1024); } while (0)
; #define PG8_LDB(dst, b, h) do { _Pragma("unroll") for (int n = 0; n < 2; ++n) _Pragma("unroll") for (int k = 0; k < 2; ++k) dst[n][k] = *(const LAS bf16x8*)(lds + PG8_SB(b, h) + boff + n * 2048 + k * 1024); } while (0)
; #define PG8_MMA(ai, bj, At, Bt) do { __builtin_amdgcn_s_setprio(1); _Pragma("unroll") for (int m = 0; m < 4; ++m) _Pragma("unroll") for (int n = 0; n < 2; ++n) _Pragma("unroll") for (int k = 0; k < 2; ++k) \
;         acc[ai][bj][m][n] = __builtin_amdgcn_mfma_f32_16x16x32_bf16(Bt[n][k], At[m][k], acc[ai][bj][m][n], 0, 0, 0); __builtin_amdgcn_s_setprio(0); } while (0)
; #define PG8_WAIT_V(n) asm volatile("s_waitcnt vmcnt(" #n ")" ::: "memory")
; #define PG8_WAIT_L(n) asm volatile("s_waitcnt lgkmcnt(" #n ")" ::: "memory")
; #define PG8_BAR __builtin_amdgcn_s_barrier()
; #define PG8_SCHED __builtin_amdgcn_sched_barrier(0)
; template <class Desc, class Epi>
; __device__ __forceinline__ void gemm_phase(const int wv_, LAS unsigned char* lds, const Desc& d, const Epi& E) {
;     ...
;             PG8_LDB(B0, 0, 0); PG8_LDB(B1, 0, 1); PG8_SCHED; PG8_LDA(At, 0, 0); PG8_STAGE(PG8_SA(1, 1), a1, voffA1);
;             PG8_WAIT_V(8); PG8_WAIT_L(0); PG8_BAR; PG8_MMA(0, 0, At, B0); PG8_MMA(0, 1, At, B1); PG8_BAR; PG8_SCHED;
;             PG8_LDA(At, 0, 1); PG8_STAGE(PG8_SB(0, 0), b2, voffB); PG8_STAGE(PG8_SB(0, 1), b2 + hstepB, voffB); PG8_STAGE(PG8_SA(0, 0), a2, sA0);
;             PG8_WAIT_V(8); PG8_WAIT_L(0); PG8_BAR; PG8_MMA(1, 0, At, B0); PG8_MMA(1, 1, At, B1); PG8_BAR; PG8_SCHED;
.LBB0_1161:
	s_add_u32 s4, s2, 0x80
	s_addc_u32 s5, s3, 0
	s_add_i32 s65, 0, 0x10000
	s_cmp_eq_u32 s45, 12
	s_cselect_b32 s5, s47, s5
	s_cselect_b32 s4, s46, s4
	v_add_u32_e32 v96, s65, v197
	s_cselect_b32 s21, s49, s29
	s_cselect_b32 s20, s48, s1
	s_add_i32 s68, 0, 0x14000
	ds_read_b128 v[130:133], v96
	ds_read_b128 v[134:137], v96 offset:1024
	ds_read_b128 v[138:141], v96 offset:2048
	ds_read_b128 v[142:145], v96 offset:3072
	v_add_u32_e32 v96, s68, v197
	ds_read_b128 v[146:149], v96
	ds_read_b128 v[150:153], v96 offset:1024
	ds_read_b128 v[154:157], v96 offset:2048
	ds_read_b128 v[158:161], v96 offset:3072
	ds_read_b128 v[162:165], v228
	ds_read_b128 v[166:169], v228 offset:1024
	ds_read_b128 v[170:173], v228 offset:2048
	ds_read_b128 v[174:177], v228 offset:3072
	ds_read_b128 v[178:181], v228 offset:4096
	ds_read_b128 v[182:185], v228 offset:5120
	ds_read_b128 v[186:189], v228 offset:6144
	ds_read_b128 v[230:233], v228 offset:7168
	s_add_i32 m0, s55, 0xc000
	s_nop 0
	global_load_lds_dwordx4 v191, s[2:3]
	s_add_i32 m0, s55, 0xe000
	s_nop 0
	global_load_lds_dwordx4 v194, s[2:3]
	s_waitcnt vmcnt(8)
	s_waitcnt lgkmcnt(0)
	s_barrier
	v_mfma_f32_16x16x32_bf16 v[126:129], v[130:133], v[162:165], v[126:129]
	v_mfma_f32_16x16x32_bf16 v[122:125], v[138:141], v[162:165], v[122:125]
	v_mfma_f32_16x16x32_bf16 v[114:117], v[130:133], v[170:173], v[114:117]
	v_mfma_f32_16x16x32_bf16 v[106:109], v[138:141], v[170:173], v[106:109]
	v_mfma_f32_16x16x32_bf16 v[98:101], v[130:133], v[178:181], v[98:101]
	v_mfma_f32_16x16x32_bf16 v[88:91], v[138:141], v[178:181], v[88:91]
	v_mfma_f32_16x16x32_bf16 v[80:83], v[130:133], v[186:189], v[80:83]
	v_mfma_f32_16x16x32_bf16 v[72:75], v[138:141], v[186:189], v[72:75]
	v_mfma_f32_16x16x32_bf16 v[126:129], v[134:137], v[166:169], v[126:129]
	v_mfma_f32_16x16x32_bf16 v[122:125], v[142:145], v[166:169], v[122:125]
	v_mfma_f32_16x16x32_bf16 v[114:117], v[134:137], v[174:177], v[114:117]
	v_mfma_f32_16x16x32_bf16 v[106:109], v[142:145], v[174:177], v[106:109]
	v_mfma_f32_16x16x32_bf16 v[98:101], v[134:137], v[182:185], v[98:101]
	v_mfma_f32_16x16x32_bf16 v[88:91], v[142:145], v[182:185], v[88:91]
	v_mfma_f32_16x16x32_bf16 v[80:83], v[134:137], v[230:233], v[80:83]
	v_mfma_f32_16x16x32_bf16 v[72:75], v[142:145], v[230:233], v[72:75]
	v_mfma_f32_16x16x32_bf16 v[118:121], v[146:149], v[162:165], v[118:121]
	v_mfma_f32_16x16x32_bf16 v[110:113], v[154:157], v[162:165], v[110:113]
	v_mfma_f32_16x16x32_bf16 v[102:105], v[146:149], v[170:173], v[102:105]
	v_mfma_f32_16x16x32_bf16 v[92:95], v[154:157], v[170:173], v[92:95]
	v_mfma_f32_16x16x32_bf16 v[84:87], v[146:149], v[178:181], v[84:87]
	v_mfma_f32_16x16x32_bf16 v[76:79], v[154:157], v[178:181], v[76:79]
	v_mfma_f32_16x16x32_bf16 v[68:71], v[146:149], v[186:189], v[68:71]
	v_mfma_f32_16x16x32_bf16 v[64:67], v[154:157], v[186:189], v[64:67]
	v_mfma_f32_16x16x32_bf16 v[118:121], v[150:153], v[166:169], v[118:121]
	v_mfma_f32_16x16x32_bf16 v[110:113], v[158:161], v[166:169], v[110:113]
	v_mfma_f32_16x16x32_bf16 v[102:105], v[150:153], v[174:177], v[102:105]
	v_mfma_f32_16x16x32_bf16 v[92:95], v[158:161], v[174:177], v[92:95]
	v_mfma_f32_16x16x32_bf16 v[84:87], v[150:153], v[182:185], v[84:87]
	v_mfma_f32_16x16x32_bf16 v[76:79], v[158:161], v[182:185], v[76:79]
	v_mfma_f32_16x16x32_bf16 v[68:71], v[150:153], v[230:233], v[68:71]
	v_mfma_f32_16x16x32_bf16 v[64:67], v[158:161], v[230:233], v[64:67]
	s_barrier
	s_add_i32 s65, s65, s54
	ds_read_b128 v[162:165], v228 offset:16384
	ds_read_b128 v[166:169], v228 offset:17408
	ds_read_b128 v[170:173], v228 offset:18432
	ds_read_b128 v[174:177], v228 offset:19456
	ds_read_b128 v[178:181], v228 offset:20480
	ds_read_b128 v[182:185], v228 offset:21504
	ds_read_b128 v[186:189], v228 offset:22528
	ds_read_b128 v[230:233], v228 offset:23552
	s_mov_b32 m0, s65
	s_nop 0
	global_load_lds_dwordx4 v192, s[20:21]
	s_add_i32 m0, s65, 0x2000
	s_add_u32 s66, s20, 0x40000
	global_load_lds_dwordx4 v195, s[20:21]
	s_addc_u32 s67, s21, 0
	s_add_i32 s65, s68, s54
	s_mov_b32 m0, s65
	s_nop 0
	global_load_lds_dwordx4 v192, s[66:67]
	s_add_i32 m0, s65, 0x2000
	s_nop 0
	global_load_lds_dwordx4 v195, s[66:67]
	s_mov_b32 m0, s55
	s_nop 0
	global_load_lds_dwordx4 v190, s[4:5]
	s_mov_b32 m0, s56
	s_nop 0
	global_load_lds_dwordx4 v193, s[4:5]
	s_waitcnt vmcnt(8)
	s_waitcnt lgkmcnt(0)
	s_barrier
	v_mfma_f32_16x16x32_bf16 v[60:63], v[130:133], v[162:165], v[60:63]
	v_mfma_f32_16x16x32_bf16 v[56:59], v[138:141], v[162:165], v[56:59]
	v_mfma_f32_16x16x32_bf16 v[40:43], v[130:133], v[170:173], v[40:43]
	v_mfma_f32_16x16x32_bf16 v[32:35], v[138:141], v[170:173], v[32:35]
	v_mfma_f32_16x16x32_bf16 v[16:19], v[130:133], v[178:181], v[16:19]
	v_mfma_f32_16x16x32_bf16 v[8:11], v[138:141], v[178:181], v[8:11]
	v_mfma_f32_16x16x32_bf16 v[4:7], v[130:133], v[186:189], v[4:7]
	v_mfma_f32_16x16x32_bf16 v[0:3], v[138:141], v[186:189], v[0:3]
	v_mfma_f32_16x16x32_bf16 v[60:63], v[134:137], v[166:169], v[60:63]
	v_mfma_f32_16x16x32_bf16 v[56:59], v[142:145], v[166:169], v[56:59]
	v_mfma_f32_16x16x32_bf16 v[40:43], v[134:137], v[174:177], v[40:43]
	v_mfma_f32_16x16x32_bf16 v[32:35], v[142:145], v[174:177], v[32:35]
	v_mfma_f32_16x16x32_bf16 v[16:19], v[134:137], v[182:185], v[16:19]
	v_mfma_f32_16x16x32_bf16 v[8:11], v[142:145], v[182:185], v[8:11]
	v_mfma_f32_16x16x32_bf16 v[4:7], v[134:137], v[230:233], v[4:7]
	v_mfma_f32_16x16x32_bf16 v[0:3], v[142:145], v[230:233], v[0:3]
	v_mfma_f32_16x16x32_bf16 v[44:47], v[146:149], v[162:165], v[44:47]
	v_mfma_f32_16x16x32_bf16 v[36:39], v[154:157], v[162:165], v[36:39]
	v_mfma_f32_16x16x32_bf16 v[20:23], v[146:149], v[170:173], v[20:23]
	v_mfma_f32_16x16x32_bf16 v[12:15], v[154:157], v[170:173], v[12:15]
	v_mfma_f32_16x16x32_bf16 v[52:55], v[146:149], v[178:181], v[52:55]
	v_mfma_f32_16x16x32_bf16 v[48:51], v[154:157], v[178:181], v[48:51]
	v_mfma_f32_16x16x32_bf16 v[28:31], v[146:149], v[186:189], v[28:31]
	v_mfma_f32_16x16x32_bf16 v[24:27], v[154:157], v[186:189], v[24:27]
	v_mfma_f32_16x16x32_bf16 v[44:47], v[150:153], v[166:169], v[44:47]
	v_mfma_f32_16x16x32_bf16 v[36:39], v[158:161], v[166:169], v[36:39]
	v_mfma_f32_16x16x32_bf16 v[20:23], v[150:153], v[174:177], v[20:23]
	v_mfma_f32_16x16x32_bf16 v[12:15], v[158:161], v[174:177], v[12:15]
	v_mfma_f32_16x16x32_bf16 v[52:55], v[150:153], v[182:185], v[52:55]
	v_mfma_f32_16x16x32_bf16 v[48:51], v[158:161], v[182:185], v[48:51]
	v_mfma_f32_16x16x32_bf16 v[28:31], v[150:153], v[230:233], v[28:31]
	v_mfma_f32_16x16x32_bf16 v[24:27], v[158:161], v[230:233], v[24:27]
	s_barrier
; #define PG8_STAGE(bufoff, gbase, voff) do { _Pragma("unroll") for (int _i = 0; _i < 2; ++_i) \
;         __builtin_amdgcn_global_load_lds((const __attribute__((address_space(1))) unsigned*)((const __attribute__((address_space(1))) char*)(gbase) + (unsigned)lnd_v((int)(voff)[_i])), (LAS unsigned*)(lds + (bufoff) + ldsw + _i * 8192), 16, 0, 0); } while (0)
; #define PG8_LDA(dst, b, h) do { _Pragma("unroll") for (int m = 0; m < 4; ++m) _Pragma("unroll") for (int k = 0; k < 2; ++k) dst[m][k] = *(const LAS bf16x8*)(lds + PG8_SA(b, h) + aoff + m * 2048 + k * 1024); } while (0)
; #define PG8_LDB(dst, b, h) do { _Pragma("unroll") for (int n = 0; n < 2; ++n) _Pragma("unroll") for (int k = 0; k < 2; ++k) dst[n][k] = *(const LAS bf16x8*)(lds + PG8_SB(b, h) + boff + n * 2048 + k * 1024); } while (0)
; #define PG8_MMA(ai, bj, At, Bt) do { __builtin_amdgcn_s_setprio(1); _Pragma("unroll") for (int m = 0; m < 4; ++m) _Pragma("unroll") for (int n = 0; n < 2; ++n) _Pragma("unroll") for (int k = 0; k < 2; ++k) \
;         acc[ai][bj][m][n] = __builtin_amdgcn_mfma_f32_16x16x32_bf16(Bt[n][k], At[m][k], acc[ai][bj][m][n], 0, 0, 0); __builtin_amdgcn_s_setprio(0); } while (0)
; #define PG8_WAIT_V(n) asm volatile("s_waitcnt vmcnt(" #n ")" ::: "memory")
; #define PG8_WAIT_L(n) asm volatile("s_waitcnt lgkmcnt(" #n ")" ::: "memory")
; #define PG8_BAR __builtin_amdgcn_s_barrier()
; #define PG8_SCHED __builtin_amdgcn_sched_barrier(0)
; template <class Desc, class Epi>
; __device__ __forceinline__ void gemm_phase(const int wv_, LAS unsigned char* lds, const Desc& d, const Epi& E) {
;     ...
;             PG8_LDB(B0, 1, 0); PG8_LDB(B1, 1, 1); PG8_SCHED; PG8_LDA(At, 1, 0); PG8_STAGE(PG8_SA(0, 1), a2, sA1);
;             PG8_WAIT_V(8); PG8_WAIT_L(0); PG8_BAR; PG8_MMA(0, 0, At, B0); PG8_MMA(0, 1, At, B1); PG8_BAR; PG8_SCHED;
	s_add_i32 s65, 0, 0x18000
	v_add_u32_e32 v96, s65, v197
	s_add_i32 s66, 0, 0x1c000
	ds_read_b128 v[130:133], v96
	ds_read_b128 v[134:137], v96 offset:1024
	ds_read_b128 v[138:141], v96 offset:2048
	ds_read_b128 v[142:145], v96 offset:3072
	v_add_u32_e32 v96, s66, v197
	ds_read_b128 v[146:149], v96
	ds_read_b128 v[150:153], v96 offset:1024
	ds_read_b128 v[154:157], v96 offset:2048
	ds_read_b128 v[158:161], v96 offset:3072
	s_mov_b32 m0, s57
	ds_read_b128 v[162:165], v228 offset:32768
	ds_read_b128 v[166:169], v228 offset:33792
	ds_read_b128 v[170:173], v228 offset:34816
	ds_read_b128 v[174:177], v228 offset:35840
	ds_read_b128 v[178:181], v228 offset:36864
	ds_read_b128 v[182:185], v228 offset:37888
	ds_read_b128 v[186:189], v228 offset:38912
	ds_read_b128 v[230:233], v228 offset:39936
	s_nop 0
	global_load_lds_dwordx4 v191, s[4:5]
	s_mov_b32 m0, s58
	s_nop 0
	global_load_lds_dwordx4 v194, s[4:5]
	s_waitcnt vmcnt(8)
	s_waitcnt lgkmcnt(0)
	s_barrier
	v_mfma_f32_16x16x32_bf16 v[126:129], v[130:133], v[162:165], v[126:129]
	v_mfma_f32_16x16x32_bf16 v[122:125], v[138:141], v[162:165], v[122:125]
	v_mfma_f32_16x16x32_bf16 v[114:117], v[130:133], v[170:173], v[114:117]
	v_mfma_f32_16x16x32_bf16 v[106:109], v[138:141], v[170:173], v[106:109]
	v_mfma_f32_16x16x32_bf16 v[98:101], v[130:133], v[178:181], v[98:101]
	v_mfma_f32_16x16x32_bf16 v[88:91], v[138:141], v[178:181], v[88:91]
	v_mfma_f32_16x16x32_bf16 v[80:83], v[130:133], v[186:189], v[80:83]
	v_mfma_f32_16x16x32_bf16 v[72:75], v[138:141], v[186:189], v[72:75]
	v_mfma_f32_16x16x32_bf16 v[126:129], v[134:137], v[166:169], v[126:129]
	v_mfma_f32_16x16x32_bf16 v[122:125], v[142:145], v[166:169], v[122:125]
	v_mfma_f32_16x16x32_bf16 v[114:117], v[134:137], v[174:177], v[114:117]
	v_mfma_f32_16x16x32_bf16 v[106:109], v[142:145], v[174:177], v[106:109]
	v_mfma_f32_16x16x32_bf16 v[98:101], v[134:137], v[182:185], v[98:101]
	v_mfma_f32_16x16x32_bf16 v[88:91], v[142:145], v[182:185], v[88:91]
	v_mfma_f32_16x16x32_bf16 v[80:83], v[134:137], v[230:233], v[80:83]
	v_mfma_f32_16x16x32_bf16 v[72:75], v[142:145], v[230:233], v[72:75]
	v_mfma_f32_16x16x32_bf16 v[118:121], v[146:149], v[162:165], v[118:121]
	v_mfma_f32_16x16x32_bf16 v[110:113], v[154:157], v[162:165], v[110:113]
	v_mfma_f32_16x16x32_bf16 v[102:105], v[146:149], v[170:173], v[102:105]
	v_mfma_f32_16x16x32_bf16 v[92:95], v[154:157], v[170:173], v[92:95]
	v_mfma_f32_16x16x32_bf16 v[84:87], v[146:149], v[178:181], v[84:87]
	v_mfma_f32_16x16x32_bf16 v[76:79], v[154:157], v[178:181], v[76:79]
	v_mfma_f32_16x16x32_bf16 v[68:71], v[146:149], v[186:189], v[68:71]
	v_mfma_f32_16x16x32_bf16 v[64:67], v[154:157], v[186:189], v[64:67]
	v_mfma_f32_16x16x32_bf16 v[118:121], v[150:153], v[166:169], v[118:121]
	v_mfma_f32_16x16x32_bf16 v[110:113], v[158:161], v[166:169], v[110:113]
	v_mfma_f32_16x16x32_bf16 v[102:105], v[150:153], v[174:177], v[102:105]
	v_mfma_f32_16x16x32_bf16 v[92:95], v[158:161], v[174:177], v[92:95]
	v_mfma_f32_16x16x32_bf16 v[84:87], v[150:153], v[182:185], v[84:87]
	v_mfma_f32_16x16x32_bf16 v[76:79], v[158:161], v[182:185], v[76:79]
	v_mfma_f32_16x16x32_bf16 v[68:71], v[150:153], v[230:233], v[68:71]
	v_mfma_f32_16x16x32_bf16 v[64:67], v[158:161], v[230:233], v[64:67]
	s_barrier
; #define PG8_STAGE(bufoff, gbase, voff) do { _Pragma("unroll") for (int _i = 0; _i < 2; ++_i) \
;         __builtin_amdgcn_global_load_lds((const __attribute__((address_space(1))) unsigned*)((const __attribute__((address_space(1))) char*)(gbase) + (unsigned)lnd_v((int)(voff)[_i])), (LAS unsigned*)(lds + (bufoff) + ldsw + _i * 8192), 16, 0, 0); } while (0)
; #define PG8_LDA(dst, b, h) do { _Pragma("unroll") for (int m = 0; m < 4; ++m) _Pragma("unroll") for (int k = 0; k < 2; ++k) dst[m][k] = *(const LAS bf16x8*)(lds + PG8_SA(b, h) + aoff + m * 2048 + k * 1024); } while (0)
; #define PG8_MMA(ai, bj, At, Bt) do { __builtin_amdgcn_s_setprio(1); _Pragma("unroll") for (int m = 0; m < 4; ++m) _Pragma("unroll") for (int n = 0; n < 2; ++n) _Pragma("unroll") for (int k = 0; k < 2; ++k) \
;         acc[ai][bj][m][n] = __builtin_amdgcn_mfma_f32_16x16x32_bf16(Bt[n][k], At[m][k], acc[ai][bj][m][n], 0, 0, 0); __builtin_amdgcn_s_setprio(0); } while (0)
; #define PG8_WAIT_V(n) asm volatile("s_waitcnt vmcnt(" #n ")" ::: "memory")
; #define PG8_WAIT_L(n) asm volatile("s_waitcnt lgkmcnt(" #n ")" ::: "memory")
; #define PG8_BAR __builtin_amdgcn_s_barrier()
; #define PG8_SCHED __builtin_amdgcn_sched_barrier(0)
; template <class Desc, class Epi>
; __device__ __forceinline__ void gemm_phase(const int wv_, LAS unsigned char* lds, const Desc& d, const Epi& E) {
;     ...
;             PG8_LDA(At, 1, 1); PG8_STAGE(PG8_SB(1, 0), b3, voffB); PG8_STAGE(PG8_SB(1, 1), b3 + hstepB, voffB); PG8_STAGE(PG8_SA(1, 0), a3, sA0);
;             PG8_WAIT_V(8); PG8_WAIT_L(0); PG8_BAR; PG8_MMA(1, 0, At, B0); PG8_MMA(1, 1, At, B1); PG8_BAR; PG8_SCHED;
;         }
;         if (wr == 0) PG8_BAR;
	v_mov_b32_e32 v96, v192
	ds_read_b128 v[162:165], v228 offset:49152
	ds_read_b128 v[166:169], v228 offset:50176
	ds_read_b128 v[170:173], v228 offset:51200
	ds_read_b128 v[174:177], v228 offset:52224
	ds_read_b128 v[178:181], v228 offset:53248
	ds_read_b128 v[182:185], v228 offset:54272
	ds_read_b128 v[186:189], v228 offset:55296
	ds_read_b128 v[230:233], v228 offset:56320
	s_add_i32 s65, s65, s54
	v_lshl_add_u64 v[234:235], s[20:21], 0, v[96:97]
	v_lshl_add_u64 v[234:235], v[234:235], 0, s[30:31]
	s_mov_b32 m0, s65
	v_mov_b32_e32 v96, v195
	global_load_lds_dwordx4 v[234:235], off
	s_add_i32 m0, s65, 0x2000
	s_nop 0
	v_lshl_add_u64 v[234:235], s[20:21], 0, v[96:97]
	s_add_u32 s20, s20, 0x40080
	v_lshl_add_u64 v[234:235], v[234:235], 0, s[30:31]
	s_addc_u32 s21, s21, 0
	s_add_i32 s65, s66, s54
	global_load_lds_dwordx4 v[234:235], off
	s_mov_b32 m0, s65
	s_nop 0
	global_load_lds_dwordx4 v192, s[20:21]
	s_add_i32 m0, s65, 0x2000
	s_nop 0
	global_load_lds_dwordx4 v195, s[20:21]
	v_mov_b32_e32 v96, v190
	s_mov_b32 m0, s59
	v_lshl_add_u64 v[234:235], s[4:5], 0, v[96:97]
	v_lshl_add_u64 v[234:235], v[234:235], 0, s[30:31]
	v_mov_b32_e32 v96, v193
	global_load_lds_dwordx4 v[234:235], off
	s_mov_b32 m0, s60
	v_lshl_add_u64 v[234:235], s[4:5], 0, v[96:97]
	v_lshl_add_u64 v[234:235], v[234:235], 0, s[30:31]
	global_load_lds_dwordx4 v[234:235], off
	s_waitcnt vmcnt(8)
	s_waitcnt lgkmcnt(0)
	s_barrier
	v_mfma_f32_16x16x32_bf16 v[60:63], v[130:133], v[162:165], v[60:63]
	v_mfma_f32_16x16x32_bf16 v[56:59], v[138:141], v[162:165], v[56:59]
	v_mfma_f32_16x16x32_bf16 v[40:43], v[130:133], v[170:173], v[40:43]
	v_mfma_f32_16x16x32_bf16 v[32:35], v[138:141], v[170:173], v[32:35]
	v_mfma_f32_16x16x32_bf16 v[16:19], v[130:133], v[178:181], v[16:19]
	v_mfma_f32_16x16x32_bf16 v[8:11], v[138:141], v[178:181], v[8:11]
	v_mfma_f32_16x16x32_bf16 v[4:7], v[130:133], v[186:189], v[4:7]
	v_mfma_f32_16x16x32_bf16 v[0:3], v[138:141], v[186:189], v[0:3]
	v_mfma_f32_16x16x32_bf16 v[60:63], v[134:137], v[166:169], v[60:63]
	v_mfma_f32_16x16x32_bf16 v[56:59], v[142:145], v[166:169], v[56:59]
	v_mfma_f32_16x16x32_bf16 v[40:43], v[134:137], v[174:177], v[40:43]
	v_mfma_f32_16x16x32_bf16 v[32:35], v[142:145], v[174:177], v[32:35]
	v_mfma_f32_16x16x32_bf16 v[16:19], v[134:137], v[182:185], v[16:19]
	v_mfma_f32_16x16x32_bf16 v[8:11], v[142:145], v[182:185], v[8:11]
	v_mfma_f32_16x16x32_bf16 v[4:7], v[134:137], v[230:233], v[4:7]
	v_mfma_f32_16x16x32_bf16 v[0:3], v[142:145], v[230:233], v[0:3]
	v_mfma_f32_16x16x32_bf16 v[44:47], v[146:149], v[162:165], v[44:47]
	v_mfma_f32_16x16x32_bf16 v[36:39], v[154:157], v[162:165], v[36:39]
	v_mfma_f32_16x16x32_bf16 v[20:23], v[146:149], v[170:173], v[20:23]
	v_mfma_f32_16x16x32_bf16 v[12:15], v[154:157], v[170:173], v[12:15]
	v_mfma_f32_16x16x32_bf16 v[52:55], v[146:149], v[178:181], v[52:55]
	v_mfma_f32_16x16x32_bf16 v[48:51], v[154:157], v[178:181], v[48:51]
	v_mfma_f32_16x16x32_bf16 v[28:31], v[146:149], v[186:189], v[28:31]
	v_mfma_f32_16x16x32_bf16 v[24:27], v[154:157], v[186:189], v[24:27]
	v_mfma_f32_16x16x32_bf16 v[44:47], v[150:153], v[166:169], v[44:47]
	v_mfma_f32_16x16x32_bf16 v[36:39], v[158:161], v[166:169], v[36:39]
	v_mfma_f32_16x16x32_bf16 v[20:23], v[150:153], v[174:177], v[20:23]
	v_mfma_f32_16x16x32_bf16 v[12:15], v[158:161], v[174:177], v[12:15]
	v_mfma_f32_16x16x32_bf16 v[52:55], v[150:153], v[182:185], v[52:55]
	v_mfma_f32_16x16x32_bf16 v[48:51], v[158:161], v[182:185], v[48:51]
	v_mfma_f32_16x16x32_bf16 v[28:31], v[150:153], v[230:233], v[28:31]
	v_mfma_f32_16x16x32_bf16 v[24:27], v[158:161], v[230:233], v[24:27]
	s_barrier
	s_add_i32 s45, s45, 2
	s_add_u32 s2, s2, 0x100
	s_addc_u32 s3, s3, 0
	s_add_u32 s1, s1, 0x100
	s_addc_u32 s29, s29, 0
	s_cmp_gt_u32 s45, 13
	s_cbranch_scc0 .LBB0_1161
	s_and_b64 vcc, exec, s[42:43]
	s_cbranch_vccz .LBB0_1164
	s_barrier

; #define PG8_STAGE(bufoff, gbase, voff) do { _Pragma("unroll") for (int _i = 0; _i < 2; ++_i) \
;         __builtin_amdgcn_global_load_lds((const __attribute__((address_space(1))) unsigned*)((const __attribute__((address_space(1))) char*)(gbase) + (unsigned)lnd_v((int)(voff)[_i])), (LAS unsigned*)(lds + (bufoff) + ldsw + _i * 8192), 16, 0, 0); } while (0)
; #define PG8_LDA(dst, b, h) do { _Pragma("unroll") for (int m = 0; m < 4; ++m) _Pragma("unroll") for (int k = 0; k < 2; ++k) dst[m][k] = *(const LAS bf16x8*)(lds + PG8_SA(b, h) + aoff + m * 2048 + k * 1024); } while (0)
; #define PG8_LDB(dst, b, h) do { _Pragma("unroll") for (int n = 0; n < 2; ++n) _Pragma("unroll") for (int k = 0; k < 2; ++k) dst[n][k] = *(const LAS bf16x8*)(lds + PG8_SB(b, h) + boff + n * 2048 + k * 1024); } while (0)
; #define PG8_MMA(ai, bj, At, Bt) do { __builtin_amdgcn_s_setprio(1); _Pragma("unroll") for (int m = 0; m < 4; ++m) _Pragma("unroll") for (int n = 0; n < 2; ++n) _Pragma("unroll") for (int k = 0; k < 2; ++k) \
;         acc[ai][bj][m][n] = __builtin_amdgcn_mfma_f32_16x16x32_bf16(Bt[n][k], At[m][k], acc[ai][bj][m][n], 0, 0, 0); __builtin_amdgcn_s_setprio(0); } while (0)
; #define PG8_WAIT_V(n) asm volatile("s_waitcnt vmcnt(" #n ")" ::: "memory")
; #define PG8_WAIT_L(n) asm volatile("s_waitcnt lgkmcnt(" #n ")" ::: "memory")
; #define PG8_BAR __builtin_amdgcn_s_barrier()
; #define PG8_SCHED __builtin_amdgcn_sched_barrier(0)
; template <class Desc, class Epi>
; __device__ __forceinline__ void gemm_phase(const int wv_, LAS unsigned char* lds, const Desc& d, const Epi& E) {
;     ...
;             const char* a1 = cA + (size_t)(t + 1) * kstep;
;             const char* a2 = last ? nA : cA + (size_t)(t + 2) * kstep; const char* b2 = last ? nB : cB + (size_t)(t + 2) * kstep;
;             const char* a3 = a2 + kstep; const char* b3 = b2 + kstep;
;             PG8_LDB(B0, 0, 0); PG8_LDB(B1, 0, 1); PG8_SCHED; PG8_LDA(At, 0, 0); PG8_STAGE(PG8_SA(1, 1), a1, voffA1);
;             PG8_WAIT_V(8); PG8_WAIT_L(0); PG8_BAR; PG8_MMA(0, 0, At, B0); PG8_MMA(0, 1, At, B1); PG8_BAR; PG8_SCHED;
;             PG8_LDA(At, 0, 1); PG8_STAGE(PG8_SB(0, 0), b2, voffB); PG8_STAGE(PG8_SB(0, 1), b2 + hstepB, voffB); PG8_STAGE(PG8_SA(0, 0), a2, sA0);
;             PG8_WAIT_V(8); PG8_WAIT_L(0); PG8_BAR; PG8_MMA(1, 0, At, B0); PG8_MMA(1, 1, At, B1); PG8_BAR; PG8_SCHED;
.LBB0_1262:
	s_add_u32 s4, s2, 0x80
	s_addc_u32 s5, s3, 0
	s_add_i32 s62, 0, 0x10000
	s_cmp_eq_u32 s61, 12
	s_cselect_b32 s5, s45, s5
	s_cselect_b32 s4, s44, s4
	v_add_u32_e32 v96, s62, v213
	s_cselect_b32 s21, s47, s43
	s_cselect_b32 s20, s46, s29
	s_add_i32 s64, 0, 0x14000
	ds_read_b128 v[130:133], v96
	ds_read_b128 v[134:137], v96 offset:1024
	ds_read_b128 v[138:141], v96 offset:2048
	ds_read_b128 v[142:145], v96 offset:3072
	v_add_u32_e32 v96, s64, v213
	ds_read_b128 v[146:149], v96
	ds_read_b128 v[150:153], v96 offset:1024
	ds_read_b128 v[154:157], v96 offset:2048
	ds_read_b128 v[158:161], v96 offset:3072
	ds_read_b128 v[162:165], v221
	ds_read_b128 v[166:169], v221 offset:1024
	ds_read_b128 v[170:173], v221 offset:2048
	ds_read_b128 v[174:177], v221 offset:3072
	ds_read_b128 v[178:181], v221 offset:4096
	ds_read_b128 v[182:185], v221 offset:5120
	ds_read_b128 v[186:189], v221 offset:6144
	ds_read_b128 v[190:193], v221 offset:7168
	s_add_i32 m0, s53, 0xc000
	s_nop 0
	global_load_lds_dwordx4 v207, s[2:3]
	s_add_i32 m0, s53, 0xe000
	s_nop 0
	global_load_lds_dwordx4 v210, s[2:3]
	s_waitcnt vmcnt(8)
	s_waitcnt lgkmcnt(0)
	s_barrier
	v_mfma_f32_16x16x32_bf16 v[126:129], v[130:133], v[162:165], v[126:129]
	v_mfma_f32_16x16x32_bf16 v[122:125], v[138:141], v[162:165], v[122:125]
	v_mfma_f32_16x16x32_bf16 v[110:113], v[130:133], v[170:173], v[110:113]
	v_mfma_f32_16x16x32_bf16 v[106:109], v[138:141], v[170:173], v[106:109]
	v_mfma_f32_16x16x32_bf16 v[92:95], v[130:133], v[178:181], v[92:95]
	v_mfma_f32_16x16x32_bf16 v[88:91], v[138:141], v[178:181], v[88:91]
	v_mfma_f32_16x16x32_bf16 v[76:79], v[130:133], v[186:189], v[76:79]
	v_mfma_f32_16x16x32_bf16 v[72:75], v[138:141], v[186:189], v[72:75]
	v_mfma_f32_16x16x32_bf16 v[126:129], v[134:137], v[166:169], v[126:129]
	v_mfma_f32_16x16x32_bf16 v[122:125], v[142:145], v[166:169], v[122:125]
	v_mfma_f32_16x16x32_bf16 v[110:113], v[134:137], v[174:177], v[110:113]
	v_mfma_f32_16x16x32_bf16 v[106:109], v[142:145], v[174:177], v[106:109]
	v_mfma_f32_16x16x32_bf16 v[92:95], v[134:137], v[182:185], v[92:95]
	v_mfma_f32_16x16x32_bf16 v[88:91], v[142:145], v[182:185], v[88:91]
	v_mfma_f32_16x16x32_bf16 v[76:79], v[134:137], v[190:193], v[76:79]
	v_mfma_f32_16x16x32_bf16 v[72:75], v[142:145], v[190:193], v[72:75]
	v_mfma_f32_16x16x32_bf16 v[118:121], v[146:149], v[162:165], v[118:121]
	v_mfma_f32_16x16x32_bf16 v[114:117], v[154:157], v[162:165], v[114:117]
	v_mfma_f32_16x16x32_bf16 v[102:105], v[146:149], v[170:173], v[102:105]
	v_mfma_f32_16x16x32_bf16 v[98:101], v[154:157], v[170:173], v[98:101]
	v_mfma_f32_16x16x32_bf16 v[84:87], v[146:149], v[178:181], v[84:87]
	v_mfma_f32_16x16x32_bf16 v[80:83], v[154:157], v[178:181], v[80:83]
	v_mfma_f32_16x16x32_bf16 v[68:71], v[146:149], v[186:189], v[68:71]
	v_mfma_f32_16x16x32_bf16 v[64:67], v[154:157], v[186:189], v[64:67]
	v_mfma_f32_16x16x32_bf16 v[118:121], v[150:153], v[166:169], v[118:121]
	v_mfma_f32_16x16x32_bf16 v[114:117], v[158:161], v[166:169], v[114:117]
	v_mfma_f32_16x16x32_bf16 v[102:105], v[150:153], v[174:177], v[102:105]
	v_mfma_f32_16x16x32_bf16 v[98:101], v[158:161], v[174:177], v[98:101]
	v_mfma_f32_16x16x32_bf16 v[84:87], v[150:153], v[182:185], v[84:87]
	v_mfma_f32_16x16x32_bf16 v[80:83], v[158:161], v[182:185], v[80:83]
	v_mfma_f32_16x16x32_bf16 v[68:71], v[150:153], v[190:193], v[68:71]
	v_mfma_f32_16x16x32_bf16 v[64:67], v[158:161], v[190:193], v[64:67]
	s_barrier
	s_add_i32 s62, s62, s52
	ds_read_b128 v[162:165], v221 offset:16384
	ds_read_b128 v[166:169], v221 offset:17408
	ds_read_b128 v[170:173], v221 offset:18432
	ds_read_b128 v[174:177], v221 offset:19456
	ds_read_b128 v[178:181], v221 offset:20480
	ds_read_b128 v[182:185], v221 offset:21504
	ds_read_b128 v[186:189], v221 offset:22528
	ds_read_b128 v[190:193], v221 offset:23552
	s_mov_b32 m0, s62
	s_nop 0
	global_load_lds_dwordx4 v208, s[20:21]
	s_add_i32 m0, s62, 0x2000
	s_add_u32 s62, s20, 0x40000
	global_load_lds_dwordx4 v211, s[20:21]
	s_addc_u32 s63, s21, 0
	s_add_i32 s64, s64, s52
	s_mov_b32 m0, s64
	s_nop 0
	global_load_lds_dwordx4 v208, s[62:63]
	s_add_i32 m0, s64, 0x2000
	s_nop 0
	global_load_lds_dwordx4 v211, s[62:63]
	s_mov_b32 m0, s53
	s_nop 0
	global_load_lds_dwordx4 v206, s[4:5]
	s_mov_b32 m0, s54
	s_nop 0
	global_load_lds_dwordx4 v209, s[4:5]
	s_waitcnt vmcnt(8)
	s_waitcnt lgkmcnt(0)
	s_barrier
	v_mfma_f32_16x16x32_bf16 v[60:63], v[130:133], v[162:165], v[60:63]
	v_mfma_f32_16x16x32_bf16 v[56:59], v[138:141], v[162:165], v[56:59]
	v_mfma_f32_16x16x32_bf16 v[44:47], v[130:133], v[170:173], v[44:47]
	v_mfma_f32_16x16x32_bf16 v[40:43], v[138:141], v[170:173], v[40:43]
	v_mfma_f32_16x16x32_bf16 v[24:27], v[130:133], v[178:181], v[24:27]
	v_mfma_f32_16x16x32_bf16 v[16:19], v[138:141], v[178:181], v[16:19]
	v_mfma_f32_16x16x32_bf16 v[4:7], v[130:133], v[186:189], v[4:7]
	v_mfma_f32_16x16x32_bf16 v[0:3], v[138:141], v[186:189], v[0:3]
	v_mfma_f32_16x16x32_bf16 v[60:63], v[134:137], v[166:169], v[60:63]
	v_mfma_f32_16x16x32_bf16 v[56:59], v[142:145], v[166:169], v[56:59]
	v_mfma_f32_16x16x32_bf16 v[44:47], v[134:137], v[174:177], v[44:47]
	v_mfma_f32_16x16x32_bf16 v[40:43], v[142:145], v[174:177], v[40:43]
	v_mfma_f32_16x16x32_bf16 v[24:27], v[134:137], v[182:185], v[24:27]
	v_mfma_f32_16x16x32_bf16 v[16:19], v[142:145], v[182:185], v[16:19]
	v_mfma_f32_16x16x32_bf16 v[4:7], v[134:137], v[190:193], v[4:7]
	v_mfma_f32_16x16x32_bf16 v[0:3], v[142:145], v[190:193], v[0:3]
	v_mfma_f32_16x16x32_bf16 v[52:55], v[146:149], v[162:165], v[52:55]
	v_mfma_f32_16x16x32_bf16 v[48:51], v[154:157], v[162:165], v[48:51]
	v_mfma_f32_16x16x32_bf16 v[28:31], v[146:149], v[170:173], v[28:31]
	v_mfma_f32_16x16x32_bf16 v[20:23], v[154:157], v[170:173], v[20:23]
	v_mfma_f32_16x16x32_bf16 v[36:39], v[146:149], v[178:181], v[36:39]
	v_mfma_f32_16x16x32_bf16 v[32:35], v[154:157], v[178:181], v[32:35]
	v_mfma_f32_16x16x32_bf16 v[12:15], v[146:149], v[186:189], v[12:15]
	v_mfma_f32_16x16x32_bf16 v[8:11], v[154:157], v[186:189], v[8:11]
	v_mfma_f32_16x16x32_bf16 v[52:55], v[150:153], v[166:169], v[52:55]
	v_mfma_f32_16x16x32_bf16 v[48:51], v[158:161], v[166:169], v[48:51]
	v_mfma_f32_16x16x32_bf16 v[28:31], v[150:153], v[174:177], v[28:31]
	v_mfma_f32_16x16x32_bf16 v[20:23], v[158:161], v[174:177], v[20:23]
	v_mfma_f32_16x16x32_bf16 v[36:39], v[150:153], v[182:185], v[36:39]
	v_mfma_f32_16x16x32_bf16 v[32:35], v[158:161], v[182:185], v[32:35]
	v_mfma_f32_16x16x32_bf16 v[12:15], v[150:153], v[190:193], v[12:15]
	v_mfma_f32_16x16x32_bf16 v[8:11], v[158:161], v[190:193], v[8:11]
	s_barrier
; #define PG8_STAGE(bufoff, gbase, voff) do { _Pragma("unroll") for (int _i = 0; _i < 2; ++_i) \
;         __builtin_amdgcn_global_load_lds((const __attribute__((address_space(1))) unsigned*)((const __attribute__((address_space(1))) char*)(gbase) + (unsigned)lnd_v((int)(voff)[_i])), (LAS unsigned*)(lds + (bufoff) + ldsw + _i * 8192), 16, 0, 0); } while (0)
; #define PG8_LDA(dst, b, h) do { _Pragma("unroll") for (int m = 0; m < 4; ++m) _Pragma("unroll") for (int k = 0; k < 2; ++k) dst[m][k] = *(const LAS bf16x8*)(lds + PG8_SA(b, h) + aoff + m * 2048 + k * 1024); } while (0)
; #define PG8_LDB(dst, b, h) do { _Pragma("unroll") for (int n = 0; n < 2; ++n) _Pragma("unroll") for (int k = 0; k < 2; ++k) dst[n][k] = *(const LAS bf16x8*)(lds + PG8_SB(b, h) + boff + n * 2048 + k * 1024); } while (0)
; #define PG8_MMA(ai, bj, At, Bt) do { __builtin_amdgcn_s_setprio(1); _Pragma("unroll") for (int m = 0; m < 4; ++m) _Pragma("unroll") for (int n = 0; n < 2; ++n) _Pragma("unroll") for (int k = 0; k < 2; ++k) \
;         acc[ai][bj][m][n] = __builtin_amdgcn_mfma_f32_16x16x32_bf16(Bt[n][k], At[m][k], acc[ai][bj][m][n], 0, 0, 0); __builtin_amdgcn_s_setprio(0); } while (0)
; #define PG8_WAIT_V(n) asm volatile("s_waitcnt vmcnt(" #n ")" ::: "memory")
; #define PG8_WAIT_L(n) asm volatile("s_waitcnt lgkmcnt(" #n ")" ::: "memory")
; #define PG8_BAR __builtin_amdgcn_s_barrier()
; #define PG8_SCHED __builtin_amdgcn_sched_barrier(0)
; template <class Desc, class Epi>
; __device__ __forceinline__ void gemm_phase(const int wv_, LAS unsigned char* lds, const Desc& d, const Epi& E) {
;     ...
;             PG8_LDB(B0, 1, 0); PG8_LDB(B1, 1, 1); PG8_SCHED; PG8_LDA(At, 1, 0); PG8_STAGE(PG8_SA(0, 1), a2, sA1);
;             PG8_WAIT_V(8); PG8_WAIT_L(0); PG8_BAR; PG8_MMA(0, 0, At, B0); PG8_MMA(0, 1, At, B1); PG8_BAR; PG8_SCHED;
	s_add_i32 s62, 0, 0x18000
	v_add_u32_e32 v96, s62, v213
	s_add_i32 s63, 0, 0x1c000
	ds_read_b128 v[130:133], v96
	ds_read_b128 v[134:137], v96 offset:1024
	ds_read_b128 v[138:141], v96 offset:2048
	ds_read_b128 v[142:145], v96 offset:3072
	v_add_u32_e32 v96, s63, v213
	ds_read_b128 v[146:149], v96
	ds_read_b128 v[150:153], v96 offset:1024
	ds_read_b128 v[154:157], v96 offset:2048
	ds_read_b128 v[158:161], v96 offset:3072
	s_mov_b32 m0, s55
	ds_read_b128 v[162:165], v221 offset:32768
	ds_read_b128 v[166:169], v221 offset:33792
	ds_read_b128 v[170:173], v221 offset:34816
	ds_read_b128 v[174:177], v221 offset:35840
	ds_read_b128 v[178:181], v221 offset:36864
	ds_read_b128 v[182:185], v221 offset:37888
	ds_read_b128 v[186:189], v221 offset:38912
	ds_read_b128 v[190:193], v221 offset:39936
	s_nop 0
	global_load_lds_dwordx4 v207, s[4:5]
	s_mov_b32 m0, s56
	s_nop 0
	global_load_lds_dwordx4 v210, s[4:5]
	s_waitcnt vmcnt(8)
	s_waitcnt lgkmcnt(0)
	s_barrier
	v_mfma_f32_16x16x32_bf16 v[126:129], v[130:133], v[162:165], v[126:129]
	v_mfma_f32_16x16x32_bf16 v[122:125], v[138:141], v[162:165], v[122:125]
	v_mfma_f32_16x16x32_bf16 v[110:113], v[130:133], v[170:173], v[110:113]
	v_mfma_f32_16x16x32_bf16 v[106:109], v[138:141], v[170:173], v[106:109]
	v_mfma_f32_16x16x32_bf16 v[92:95], v[130:133], v[178:181], v[92:95]
	v_mfma_f32_16x16x32_bf16 v[88:91], v[138:141], v[178:181], v[88:91]
	v_mfma_f32_16x16x32_bf16 v[76:79], v[130:133], v[186:189], v[76:79]
	v_mfma_f32_16x16x32_bf16 v[72:75], v[138:141], v[186:189], v[72:75]
	v_mfma_f32_16x16x32_bf16 v[126:129], v[134:137], v[166:169], v[126:129]
	v_mfma_f32_16x16x32_bf16 v[122:125], v[142:145], v[166:169], v[122:125]
	v_mfma_f32_16x16x32_bf16 v[110:113], v[134:137], v[174:177], v[110:113]
	v_mfma_f32_16x16x32_bf16 v[106:109], v[142:145], v[174:177], v[106:109]
	v_mfma_f32_16x16x32_bf16 v[92:95], v[134:137], v[182:185], v[92:95]
	v_mfma_f32_16x16x32_bf16 v[88:91], v[142:145], v[182:185], v[88:91]
	v_mfma_f32_16x16x32_bf16 v[76:79], v[134:137], v[190:193], v[76:79]
	v_mfma_f32_16x16x32_bf16 v[72:75], v[142:145], v[190:193], v[72:75]
	v_mfma_f32_16x16x32_bf16 v[118:121], v[146:149], v[162:165], v[118:121]
	v_mfma_f32_16x16x32_bf16 v[114:117], v[154:157], v[162:165], v[114:117]
	v_mfma_f32_16x16x32_bf16 v[102:105], v[146:149], v[170:173], v[102:105]
	v_mfma_f32_16x16x32_bf16 v[98:101], v[154:157], v[170:173], v[98:101]
	v_mfma_f32_16x16x32_bf16 v[84:87], v[146:149], v[178:181], v[84:87]
	v_mfma_f32_16x16x32_bf16 v[80:83], v[154:157], v[178:181], v[80:83]
	v_mfma_f32_16x16x32_bf16 v[68:71], v[146:149], v[186:189], v[68:71]
	v_mfma_f32_16x16x32_bf16 v[64:67], v[154:157], v[186:189], v[64:67]
	v_mfma_f32_16x16x32_bf16 v[118:121], v[150:153], v[166:169], v[118:121]
	v_mfma_f32_16x16x32_bf16 v[114:117], v[158:161], v[166:169], v[114:117]
	v_mfma_f32_16x16x32_bf16 v[102:105], v[150:153], v[174:177], v[102:105]
	v_mfma_f32_16x16x32_bf16 v[98:101], v[158:161], v[174:177], v[98:101]
	v_mfma_f32_16x16x32_bf16 v[84:87], v[150:153], v[182:185], v[84:87]
	v_mfma_f32_16x16x32_bf16 v[80:83], v[158:161], v[182:185], v[80:83]
	v_mfma_f32_16x16x32_bf16 v[68:71], v[150:153], v[190:193], v[68:71]
	v_mfma_f32_16x16x32_bf16 v[64:67], v[158:161], v[190:193], v[64:67]
	s_barrier
; #define PG8_STAGE(bufoff, gbase, voff) do { _Pragma("unroll") for (int _i = 0; _i < 2; ++_i) \
;         __builtin_amdgcn_global_load_lds((const __attribute__((address_space(1))) unsigned*)((const __attribute__((address_space(1))) char*)(gbase) + (unsigned)lnd_v((int)(voff)[_i])), (LAS unsigned*)(lds + (bufoff) + ldsw + _i * 8192), 16, 0, 0); } while (0)
; #define PG8_LDA(dst, b, h) do { _Pragma("unroll") for (int m = 0; m < 4; ++m) _Pragma("unroll") for (int k = 0; k < 2; ++k) dst[m][k] = *(const LAS bf16x8*)(lds + PG8_SA(b, h) + aoff + m * 2048 + k * 1024); } while (0)
; #define PG8_MMA(ai, bj, At, Bt) do { __builtin_amdgcn_s_setprio(1); _Pragma("unroll") for (int m = 0; m < 4; ++m) _Pragma("unroll") for (int n = 0; n < 2; ++n) _Pragma("unroll") for (int k = 0; k < 2; ++k) \
;         acc[ai][bj][m][n] = __builtin_amdgcn_mfma_f32_16x16x32_bf16(Bt[n][k], At[m][k], acc[ai][bj][m][n], 0, 0, 0); __builtin_amdgcn_s_setprio(0); } while (0)
; #define PG8_WAIT_V(n) asm volatile("s_waitcnt vmcnt(" #n ")" ::: "memory")
; #define PG8_WAIT_L(n) asm volatile("s_waitcnt lgkmcnt(" #n ")" ::: "memory")
; #define PG8_BAR __builtin_amdgcn_s_barrier()
; #define PG8_SCHED __builtin_amdgcn_sched_barrier(0)
; template <class Desc, class Epi>
; __device__ __forceinline__ void gemm_phase(const int wv_, LAS unsigned char* lds, const Desc& d, const Epi& E) {
;     ...
;             PG8_LDA(At, 1, 1); PG8_STAGE(PG8_SB(1, 0), b3, voffB); PG8_STAGE(PG8_SB(1, 1), b3 + hstepB, voffB); PG8_STAGE(PG8_SA(1, 0), a3, sA0);
;             PG8_WAIT_V(8); PG8_WAIT_L(0); PG8_BAR; PG8_MMA(1, 0, At, B0); PG8_MMA(1, 1, At, B1); PG8_BAR; PG8_SCHED;
;         }
;         if (wr == 0) PG8_BAR;
	v_mov_b32_e32 v96, v208
	ds_read_b128 v[162:165], v221 offset:49152
	ds_read_b128 v[166:169], v221 offset:50176
	ds_read_b128 v[170:173], v221 offset:51200
	ds_read_b128 v[174:177], v221 offset:52224
	ds_read_b128 v[178:181], v221 offset:53248
	ds_read_b128 v[182:185], v221 offset:54272
	ds_read_b128 v[186:189], v221 offset:55296
	ds_read_b128 v[190:193], v221 offset:56320
	s_add_i32 s62, s62, s52
	v_lshl_add_u64 v[194:195], s[20:21], 0, v[96:97]
	v_lshl_add_u64 v[194:195], v[194:195], 0, s[30:31]
	s_mov_b32 m0, s62
	v_mov_b32_e32 v96, v211
	global_load_lds_dwordx4 v[194:195], off
	s_add_i32 m0, s62, 0x2000
	s_nop 0
	v_lshl_add_u64 v[194:195], s[20:21], 0, v[96:97]
	s_add_u32 s20, s20, 0x40080
	v_lshl_add_u64 v[194:195], v[194:195], 0, s[30:31]
	s_addc_u32 s21, s21, 0
	s_add_i32 s62, s63, s52
	global_load_lds_dwordx4 v[194:195], off
	s_mov_b32 m0, s62
	s_nop 0
	global_load_lds_dwordx4 v208, s[20:21]
	s_add_i32 m0, s62, 0x2000
	s_nop 0
	global_load_lds_dwordx4 v211, s[20:21]
	v_mov_b32_e32 v96, v206
	s_mov_b32 m0, s57
	v_lshl_add_u64 v[194:195], s[4:5], 0, v[96:97]
	v_lshl_add_u64 v[194:195], v[194:195], 0, s[30:31]
	v_mov_b32_e32 v96, v209
	global_load_lds_dwordx4 v[194:195], off
	s_mov_b32 m0, s58
	v_lshl_add_u64 v[194:195], s[4:5], 0, v[96:97]
	v_lshl_add_u64 v[194:195], v[194:195], 0, s[30:31]
	global_load_lds_dwordx4 v[194:195], off
	s_waitcnt vmcnt(8)
	s_waitcnt lgkmcnt(0)
	s_barrier
	v_mfma_f32_16x16x32_bf16 v[60:63], v[130:133], v[162:165], v[60:63]
	v_mfma_f32_16x16x32_bf16 v[56:59], v[138:141], v[162:165], v[56:59]
	v_mfma_f32_16x16x32_bf16 v[44:47], v[130:133], v[170:173], v[44:47]
	v_mfma_f32_16x16x32_bf16 v[40:43], v[138:141], v[170:173], v[40:43]
	v_mfma_f32_16x16x32_bf16 v[24:27], v[130:133], v[178:181], v[24:27]
	v_mfma_f32_16x16x32_bf16 v[16:19], v[138:141], v[178:181], v[16:19]
	v_mfma_f32_16x16x32_bf16 v[4:7], v[130:133], v[186:189], v[4:7]
	v_mfma_f32_16x16x32_bf16 v[0:3], v[138:141], v[186:189], v[0:3]
	v_mfma_f32_16x16x32_bf16 v[60:63], v[134:137], v[166:169], v[60:63]
	v_mfma_f32_16x16x32_bf16 v[56:59], v[142:145], v[166:169], v[56:59]
	v_mfma_f32_16x16x32_bf16 v[44:47], v[134:137], v[174:177], v[44:47]
	v_mfma_f32_16x16x32_bf16 v[40:43], v[142:145], v[174:177], v[40:43]
	v_mfma_f32_16x16x32_bf16 v[24:27], v[134:137], v[182:185], v[24:27]
	v_mfma_f32_16x16x32_bf16 v[16:19], v[142:145], v[182:185], v[16:19]
	v_mfma_f32_16x16x32_bf16 v[4:7], v[134:137], v[190:193], v[4:7]
	v_mfma_f32_16x16x32_bf16 v[0:3], v[142:145], v[190:193], v[0:3]
	v_mfma_f32_16x16x32_bf16 v[52:55], v[146:149], v[162:165], v[52:55]
	v_mfma_f32_16x16x32_bf16 v[48:51], v[154:157], v[162:165], v[48:51]
	v_mfma_f32_16x16x32_bf16 v[28:31], v[146:149], v[170:173], v[28:31]
	v_mfma_f32_16x16x32_bf16 v[20:23], v[154:157], v[170:173], v[20:23]
	v_mfma_f32_16x16x32_bf16 v[36:39], v[146:149], v[178:181], v[36:39]
	v_mfma_f32_16x16x32_bf16 v[32:35], v[154:157], v[178:181], v[32:35]
	v_mfma_f32_16x16x32_bf16 v[12:15], v[146:149], v[186:189], v[12:15]
	v_mfma_f32_16x16x32_bf16 v[8:11], v[154:157], v[186:189], v[8:11]
	v_mfma_f32_16x16x32_bf16 v[52:55], v[150:153], v[166:169], v[52:55]
	v_mfma_f32_16x16x32_bf16 v[48:51], v[158:161], v[166:169], v[48:51]
	v_mfma_f32_16x16x32_bf16 v[28:31], v[150:153], v[174:177], v[28:31]
	v_mfma_f32_16x16x32_bf16 v[20:23], v[158:161], v[174:177], v[20:23]
	v_mfma_f32_16x16x32_bf16 v[36:39], v[150:153], v[182:185], v[36:39]
	v_mfma_f32_16x16x32_bf16 v[32:35], v[158:161], v[182:185], v[32:35]
	v_mfma_f32_16x16x32_bf16 v[12:15], v[150:153], v[190:193], v[12:15]
	v_mfma_f32_16x16x32_bf16 v[8:11], v[158:161], v[190:193], v[8:11]
	s_barrier
	s_add_i32 s61, s61, 2
	s_add_u32 s2, s2, 0x100
	s_addc_u32 s3, s3, 0
	s_add_u32 s29, s29, 0x100
	s_addc_u32 s43, s43, 0
	s_cmp_gt_u32 s61, 13
	s_cbranch_scc0 .LBB0_1262
	s_and_b64 vcc, exec, s[40:41]
	s_cbranch_vccz .LBB0_1265
	s_barrier

; #define PG8_STAGE(bufoff, gbase, voff) do { _Pragma("unroll") for (int _i = 0; _i < 2; ++_i) \
;         __builtin_amdgcn_global_load_lds((const __attribute__((address_space(1))) unsigned*)((const __attribute__((address_space(1))) char*)(gbase) + (unsigned)lnd_v((int)(voff)[_i])), (LAS unsigned*)(lds + (bufoff) + ldsw + _i * 8192), 16, 0, 0); } while (0)
; #define PG8_LDA(dst, b, h) do { _Pragma("unroll") for (int m = 0; m < 4; ++m) _Pragma("unroll") for (int k = 0; k < 2; ++k) dst[m][k] = *(const LAS bf16x8*)(lds + PG8_SA(b, h) + aoff + m * 2048 + k * 1024); } while (0)
; #define PG8_LDB(dst, b, h) do { _Pragma("unroll") for (int n = 0; n < 2; ++n) _Pragma("unroll") for (int k = 0; k < 2; ++k) dst[n][k] = *(const LAS bf16x8*)(lds + PG8_SB(b, h) + boff + n * 2048 + k * 1024); } while (0)
; #define PG8_WAIT_V(n) asm volatile("s_waitcnt vmcnt(" #n ")" ::: "memory")
; #define PG8_BAR __builtin_amdgcn_s_barrier()
; template <class Desc, class Epi>
; __device__ __forceinline__ void gemm_phase(const int wv_, LAS unsigned char* lds, const Desc& d, const Epi& E) {
;     ...
;         const char* nA = has_next ? (const char*)nxt.a : cA; const char* nB = has_next ? (const char*)nxt.b : cB;
;         for (int t = 0; t < nt; t += 2) {
;             const bool last = (t == nt - 2);
;             unsigned sA0[2], sA1[2];
;             if constexpr (Desc::GATHER) { sA0[0] = last ? voffAn[0] : voffA[0]; sA0[1] = last ? voffAn[1] : voffA[1]; sA1[0] = last ? voffAn1[0] : voffA1[0]; sA1[1] = last ? voffAn1[1] : voffA1[1]; }
;             else { sA0[0] = voffA[0]; sA0[1] = voffA[1]; sA1[0] = voffA1[0]; sA1[1] = voffA1[1]; }
;             const char* a1 = cA + (size_t)(t + 1) * kstep;
;             const char* a2 = last ? nA : cA + (size_t)(t + 2) * kstep; const char* b2 = last ? nB : cB + (size_t)(t + 2) * kstep;
;             const char* a3 = a2 + kstep; const char* b3 = b2 + kstep;
;             PG8_LDB(B0, 0, 0); PG8_LDB(B1, 0, 1); PG8_SCHED; PG8_LDA(At, 0, 0); PG8_STAGE(PG8_SA(1, 1), a1, voffA1);
;             PG8_WAIT_V(8); PG8_WAIT_L(0); PG8_BAR; PG8_MMA(0, 0, At, B0); PG8_MMA(0, 1, At, B1); PG8_BAR; PG8_SCHED;
;             PG8_LDA(At, 0, 1); PG8_STAGE(PG8_SB(0, 0), b2, voffB); PG8_STAGE(PG8_SB(0, 1), b2 + hstepB, voffB); PG8_STAGE(PG8_SA(0, 0), a2, sA0);
;             PG8_WAIT_V(8); PG8_WAIT_L(0); PG8_BAR; PG8_MMA(1, 0, At, B0); PG8_MMA(1, 1, At, B1); PG8_BAR; PG8_SCHED;
.LBB0_1481:
	s_add_u32 s52, s50, s22
	s_addc_u32 s53, s51, 0
	s_add_u32 s23, s52, 0x100
	s_addc_u32 s24, s53, 0
	s_and_b64 s[4:5], s[20:21], exec
	s_cselect_b32 s4, s42, s23
	s_cselect_b32 s5, s43, s24
	s_add_u32 s22, s48, s22
	s_addc_u32 s23, s49, 0
	s_add_u32 s22, s22, 0x100
	s_addc_u32 s23, s23, 0
	s_add_i32 s77, 0, 0x10000
	s_and_b64 s[20:21], s[20:21], exec
	s_cselect_b32 s21, s45, s23
	s_cselect_b32 s20, s44, s22
	s_add_i32 s23, 0, 0x14000
	v_add_u32_e32 v96, s77, v139
	s_add_i32 s79, s77, s59
	ds_read_b128 v[150:153], v96
	ds_read_b128 v[154:157], v96 offset:1024
	ds_read_b128 v[158:161], v96 offset:2048
	ds_read_b128 v[162:165], v96 offset:3072
	v_add_u32_e32 v96, s23, v139
	s_add_i32 m0, s60, 0xc000
	s_add_i32 s80, s60, 0xe000
	s_add_i32 s75, s79, 0x2000
	ds_read_b128 v[166:169], v96
	ds_read_b128 v[170:173], v96 offset:1024
	ds_read_b128 v[174:177], v96 offset:2048
	ds_read_b128 v[178:181], v96 offset:3072
	s_add_u32 s24, s20, 0x40000
	s_addc_u32 s25, s21, 0
	s_add_i32 s73, 0, 0x18000
	s_add_i32 s76, s23, s59
	s_add_i32 s71, s73, s59
	s_add_i32 s74, s76, 0x2000
	s_add_i32 s72, 0, 0x1c000
	s_add_i32 s29, s71, 0x2000
	s_add_u32 s22, s20, 0x40080
	s_addc_u32 s23, s21, 0
	s_add_i32 s78, s72, s59
	s_add_i32 s77, s78, 0x2000
	v_mov_b32_e32 v96, v133
	ds_read_b128 v[182:185], v149
	ds_read_b128 v[186:189], v149 offset:1024
	ds_read_b128 v[190:193], v149 offset:2048
	ds_read_b128 v[194:197], v149 offset:3072
	ds_read_b128 v[198:201], v149 offset:4096
	ds_read_b128 v[202:205], v149 offset:5120
	ds_read_b128 v[206:209], v149 offset:6144
	ds_read_b128 v[210:213], v149 offset:7168
	s_nop 0
	v_lshl_add_u64 v[130:131], s[52:53], 0, v[96:97]
	v_lshl_add_u64 v[130:131], v[130:131], 0, s[30:31]
	v_mov_b32_e32 v96, v136
	global_load_lds_dwordx4 v[130:131], off
	s_mov_b32 m0, s80
	v_lshl_add_u64 v[130:131], s[52:53], 0, v[96:97]
	v_lshl_add_u64 v[130:131], v[130:131], 0, s[30:31]
	global_load_lds_dwordx4 v[130:131], off
	s_waitcnt vmcnt(8)
	s_waitcnt lgkmcnt(0)
	s_barrier
	v_mfma_f32_16x16x32_bf16 v[126:129], v[150:153], v[182:185], v[126:129]
	v_mfma_f32_16x16x32_bf16 v[122:125], v[158:161], v[182:185], v[122:125]
	v_mfma_f32_16x16x32_bf16 v[110:113], v[150:153], v[190:193], v[110:113]
	v_mfma_f32_16x16x32_bf16 v[106:109], v[158:161], v[190:193], v[106:109]
	v_mfma_f32_16x16x32_bf16 v[92:95], v[150:153], v[198:201], v[92:95]
	v_mfma_f32_16x16x32_bf16 v[88:91], v[158:161], v[198:201], v[88:91]
	v_mfma_f32_16x16x32_bf16 v[76:79], v[150:153], v[206:209], v[76:79]
	v_mfma_f32_16x16x32_bf16 v[72:75], v[158:161], v[206:209], v[72:75]
	v_mfma_f32_16x16x32_bf16 v[126:129], v[154:157], v[186:189], v[126:129]
	v_mfma_f32_16x16x32_bf16 v[122:125], v[162:165], v[186:189], v[122:125]
	v_mfma_f32_16x16x32_bf16 v[110:113], v[154:157], v[194:197], v[110:113]
	v_mfma_f32_16x16x32_bf16 v[106:109], v[162:165], v[194:197], v[106:109]
	v_mfma_f32_16x16x32_bf16 v[92:95], v[154:157], v[202:205], v[92:95]
	v_mfma_f32_16x16x32_bf16 v[88:91], v[162:165], v[202:205], v[88:91]
	v_mfma_f32_16x16x32_bf16 v[76:79], v[154:157], v[210:213], v[76:79]
	v_mfma_f32_16x16x32_bf16 v[72:75], v[162:165], v[210:213], v[72:75]
	v_mfma_f32_16x16x32_bf16 v[118:121], v[166:169], v[182:185], v[118:121]
	v_mfma_f32_16x16x32_bf16 v[114:117], v[174:177], v[182:185], v[114:117]
	v_mfma_f32_16x16x32_bf16 v[102:105], v[166:169], v[190:193], v[102:105]
	v_mfma_f32_16x16x32_bf16 v[98:101], v[174:177], v[190:193], v[98:101]
	v_mfma_f32_16x16x32_bf16 v[84:87], v[166:169], v[198:201], v[84:87]
	v_mfma_f32_16x16x32_bf16 v[80:83], v[174:177], v[198:201], v[80:83]
	v_mfma_f32_16x16x32_bf16 v[68:71], v[166:169], v[206:209], v[68:71]
	v_mfma_f32_16x16x32_bf16 v[64:67], v[174:177], v[206:209], v[64:67]
	v_mfma_f32_16x16x32_bf16 v[118:121], v[170:173], v[186:189], v[118:121]
	v_mfma_f32_16x16x32_bf16 v[114:117], v[178:181], v[186:189], v[114:117]
	v_mfma_f32_16x16x32_bf16 v[102:105], v[170:173], v[194:197], v[102:105]
	v_mfma_f32_16x16x32_bf16 v[98:101], v[178:181], v[194:197], v[98:101]
	v_mfma_f32_16x16x32_bf16 v[84:87], v[170:173], v[202:205], v[84:87]
	v_mfma_f32_16x16x32_bf16 v[80:83], v[178:181], v[202:205], v[80:83]
	v_mfma_f32_16x16x32_bf16 v[68:71], v[170:173], v[210:213], v[68:71]
	v_mfma_f32_16x16x32_bf16 v[64:67], v[178:181], v[210:213], v[64:67]
	s_barrier
	s_mov_b32 m0, s79
	ds_read_b128 v[182:185], v149 offset:16384
	ds_read_b128 v[186:189], v149 offset:17408
	ds_read_b128 v[190:193], v149 offset:18432
	ds_read_b128 v[194:197], v149 offset:19456
	ds_read_b128 v[198:201], v149 offset:20480
	ds_read_b128 v[202:205], v149 offset:21504
	ds_read_b128 v[206:209], v149 offset:22528
	ds_read_b128 v[210:213], v149 offset:23552
	s_nop 0
	global_load_lds_dwordx4 v134, s[20:21]
	s_mov_b32 m0, s75
	s_nop 0
	global_load_lds_dwordx4 v137, s[20:21]
	s_mov_b32 m0, s76
	s_nop 0
	global_load_lds_dwordx4 v134, s[24:25]
	s_mov_b32 m0, s74
	s_nop 0
	global_load_lds_dwordx4 v137, s[24:25]
	s_mov_b32 m0, s60
	s_nop 0
	global_load_lds_dwordx4 v132, s[4:5]
	s_mov_b32 m0, s61
	s_nop 0
	global_load_lds_dwordx4 v135, s[4:5]
	s_waitcnt vmcnt(8)
	s_waitcnt lgkmcnt(0)
	s_barrier
; #define PG8_STAGE(bufoff, gbase, voff) do { _Pragma("unroll") for (int _i = 0; _i < 2; ++_i) \
;         __builtin_amdgcn_global_load_lds((const __attribute__((address_space(1))) unsigned*)((const __attribute__((address_space(1))) char*)(gbase) + (unsigned)lnd_v((int)(voff)[_i])), (LAS unsigned*)(lds + (bufoff) + ldsw + _i * 8192), 16, 0, 0); } while (0)
; #define PG8_LDA(dst, b, h) do { _Pragma("unroll") for (int m = 0; m < 4; ++m) _Pragma("unroll") for (int k = 0; k < 2; ++k) dst[m][k] = *(const LAS bf16x8*)(lds + PG8_SA(b, h) + aoff + m * 2048 + k * 1024); } while (0)
; #define PG8_LDB(dst, b, h) do { _Pragma("unroll") for (int n = 0; n < 2; ++n) _Pragma("unroll") for (int k = 0; k < 2; ++k) dst[n][k] = *(const LAS bf16x8*)(lds + PG8_SB(b, h) + boff + n * 2048 + k * 1024); } while (0)
; #define PG8_MMA(ai, bj, At, Bt) do { __builtin_amdgcn_s_setprio(1); _Pragma("unroll") for (int m = 0; m < 4; ++m) _Pragma("unroll") for (int n = 0; n < 2; ++n) _Pragma("unroll") for (int k = 0; k < 2; ++k) \
;         acc[ai][bj][m][n] = __builtin_amdgcn_mfma_f32_16x16x32_bf16(Bt[n][k], At[m][k], acc[ai][bj][m][n], 0, 0, 0); __builtin_amdgcn_s_setprio(0); } while (0)
; #define PG8_WAIT_V(n) asm volatile("s_waitcnt vmcnt(" #n ")" ::: "memory")
; #define PG8_WAIT_L(n) asm volatile("s_waitcnt lgkmcnt(" #n ")" ::: "memory")
; #define PG8_BAR __builtin_amdgcn_s_barrier()
; #define PG8_SCHED __builtin_amdgcn_sched_barrier(0)
; template <class Desc, class Epi>
; __device__ __forceinline__ void gemm_phase(const int wv_, LAS unsigned char* lds, const Desc& d, const Epi& E) {
;     ...
;             PG8_WAIT_V(8); PG8_WAIT_L(0); PG8_BAR; PG8_MMA(1, 0, At, B0); PG8_MMA(1, 1, At, B1); PG8_BAR; PG8_SCHED;
;             PG8_LDB(B0, 1, 0); PG8_LDB(B1, 1, 1); PG8_SCHED; PG8_LDA(At, 1, 0); PG8_STAGE(PG8_SA(0, 1), a2, sA1);
;             PG8_WAIT_V(8); PG8_WAIT_L(0); PG8_BAR; PG8_MMA(0, 0, At, B0); PG8_MMA(0, 1, At, B1); PG8_BAR; PG8_SCHED;
	v_mfma_f32_16x16x32_bf16 v[60:63], v[150:153], v[182:185], v[60:63]
	v_mfma_f32_16x16x32_bf16 v[56:59], v[158:161], v[182:185], v[56:59]
	v_mfma_f32_16x16x32_bf16 v[44:47], v[150:153], v[190:193], v[44:47]
	v_mfma_f32_16x16x32_bf16 v[32:35], v[158:161], v[190:193], v[32:35]
	v_mfma_f32_16x16x32_bf16 v[16:19], v[150:153], v[198:201], v[16:19]
	v_mfma_f32_16x16x32_bf16 v[8:11], v[158:161], v[198:201], v[8:11]
	v_mfma_f32_16x16x32_bf16 v[4:7], v[150:153], v[206:209], v[4:7]
	v_mfma_f32_16x16x32_bf16 v[0:3], v[158:161], v[206:209], v[0:3]
	v_mfma_f32_16x16x32_bf16 v[60:63], v[154:157], v[186:189], v[60:63]
	v_mfma_f32_16x16x32_bf16 v[56:59], v[162:165], v[186:189], v[56:59]
	v_mfma_f32_16x16x32_bf16 v[44:47], v[154:157], v[194:197], v[44:47]
	v_mfma_f32_16x16x32_bf16 v[32:35], v[162:165], v[194:197], v[32:35]
	v_mfma_f32_16x16x32_bf16 v[16:19], v[154:157], v[202:205], v[16:19]
	v_mfma_f32_16x16x32_bf16 v[8:11], v[162:165], v[202:205], v[8:11]
	v_mfma_f32_16x16x32_bf16 v[4:7], v[154:157], v[210:213], v[4:7]
	v_mfma_f32_16x16x32_bf16 v[0:3], v[162:165], v[210:213], v[0:3]
	v_mfma_f32_16x16x32_bf16 v[52:55], v[166:169], v[182:185], v[52:55]
	v_mfma_f32_16x16x32_bf16 v[48:51], v[174:177], v[182:185], v[48:51]
	v_mfma_f32_16x16x32_bf16 v[28:31], v[166:169], v[190:193], v[28:31]
	v_mfma_f32_16x16x32_bf16 v[12:15], v[174:177], v[190:193], v[12:15]
	v_mfma_f32_16x16x32_bf16 v[36:39], v[166:169], v[198:201], v[36:39]
	v_mfma_f32_16x16x32_bf16 v[40:43], v[174:177], v[198:201], v[40:43]
	v_mfma_f32_16x16x32_bf16 v[20:23], v[166:169], v[206:209], v[20:23]
	v_mfma_f32_16x16x32_bf16 v[24:27], v[174:177], v[206:209], v[24:27]
	v_mfma_f32_16x16x32_bf16 v[52:55], v[170:173], v[186:189], v[52:55]
	v_mfma_f32_16x16x32_bf16 v[48:51], v[178:181], v[186:189], v[48:51]
	v_mfma_f32_16x16x32_bf16 v[28:31], v[170:173], v[194:197], v[28:31]
	v_mfma_f32_16x16x32_bf16 v[12:15], v[178:181], v[194:197], v[12:15]
	v_mfma_f32_16x16x32_bf16 v[36:39], v[170:173], v[202:205], v[36:39]
	v_mfma_f32_16x16x32_bf16 v[40:43], v[178:181], v[202:205], v[40:43]
	v_mfma_f32_16x16x32_bf16 v[20:23], v[170:173], v[210:213], v[20:23]
	v_mfma_f32_16x16x32_bf16 v[24:27], v[178:181], v[210:213], v[24:27]
	s_barrier
	v_add_u32_e32 v96, s73, v139
	ds_read_b128 v[150:153], v96
	ds_read_b128 v[154:157], v96 offset:1024
	ds_read_b128 v[158:161], v96 offset:2048
	ds_read_b128 v[162:165], v96 offset:3072
	v_add_u32_e32 v96, s72, v139
	ds_read_b128 v[166:169], v96
	ds_read_b128 v[170:173], v96 offset:1024
	ds_read_b128 v[174:177], v96 offset:2048
	ds_read_b128 v[178:181], v96 offset:3072
	s_mov_b32 m0, s62
	ds_read_b128 v[182:185], v149 offset:32768
	ds_read_b128 v[186:189], v149 offset:33792
	ds_read_b128 v[190:193], v149 offset:34816
	ds_read_b128 v[194:197], v149 offset:35840
	ds_read_b128 v[198:201], v149 offset:36864
	ds_read_b128 v[202:205], v149 offset:37888
	ds_read_b128 v[206:209], v149 offset:38912
	ds_read_b128 v[210:213], v149 offset:39936
	s_nop 0
	global_load_lds_dwordx4 v133, s[4:5]
	s_mov_b32 m0, s63
	s_nop 0
	global_load_lds_dwordx4 v136, s[4:5]
	s_waitcnt vmcnt(8)
	s_waitcnt lgkmcnt(0)
	s_barrier
	v_mfma_f32_16x16x32_bf16 v[126:129], v[150:153], v[182:185], v[126:129]
	v_mfma_f32_16x16x32_bf16 v[122:125], v[158:161], v[182:185], v[122:125]
	v_mfma_f32_16x16x32_bf16 v[110:113], v[150:153], v[190:193], v[110:113]
	v_mfma_f32_16x16x32_bf16 v[106:109], v[158:161], v[190:193], v[106:109]
	v_mfma_f32_16x16x32_bf16 v[92:95], v[150:153], v[198:201], v[92:95]
	v_mfma_f32_16x16x32_bf16 v[88:91], v[158:161], v[198:201], v[88:91]
	v_mfma_f32_16x16x32_bf16 v[76:79], v[150:153], v[206:209], v[76:79]
	v_mfma_f32_16x16x32_bf16 v[72:75], v[158:161], v[206:209], v[72:75]
	v_mfma_f32_16x16x32_bf16 v[126:129], v[154:157], v[186:189], v[126:129]
	v_mfma_f32_16x16x32_bf16 v[122:125], v[162:165], v[186:189], v[122:125]
	v_mfma_f32_16x16x32_bf16 v[110:113], v[154:157], v[194:197], v[110:113]
	v_mfma_f32_16x16x32_bf16 v[106:109], v[162:165], v[194:197], v[106:109]
	v_mfma_f32_16x16x32_bf16 v[92:95], v[154:157], v[202:205], v[92:95]
	v_mfma_f32_16x16x32_bf16 v[88:91], v[162:165], v[202:205], v[88:91]
	v_mfma_f32_16x16x32_bf16 v[76:79], v[154:157], v[210:213], v[76:79]
	v_mfma_f32_16x16x32_bf16 v[72:75], v[162:165], v[210:213], v[72:75]
	v_mfma_f32_16x16x32_bf16 v[118:121], v[166:169], v[182:185], v[118:121]
	v_mfma_f32_16x16x32_bf16 v[114:117], v[174:177], v[182:185], v[114:117]
	v_mfma_f32_16x16x32_bf16 v[102:105], v[166:169], v[190:193], v[102:105]
	v_mfma_f32_16x16x32_bf16 v[98:101], v[174:177], v[190:193], v[98:101]
	v_mfma_f32_16x16x32_bf16 v[84:87], v[166:169], v[198:201], v[84:87]
	v_mfma_f32_16x16x32_bf16 v[80:83], v[174:177], v[198:201], v[80:83]
	v_mfma_f32_16x16x32_bf16 v[68:71], v[166:169], v[206:209], v[68:71]
	v_mfma_f32_16x16x32_bf16 v[64:67], v[174:177], v[206:209], v[64:67]
	v_mfma_f32_16x16x32_bf16 v[118:121], v[170:173], v[186:189], v[118:121]
	v_mfma_f32_16x16x32_bf16 v[114:117], v[178:181], v[186:189], v[114:117]
	v_mfma_f32_16x16x32_bf16 v[102:105], v[170:173], v[194:197], v[102:105]
	v_mfma_f32_16x16x32_bf16 v[98:101], v[178:181], v[194:197], v[98:101]
	v_mfma_f32_16x16x32_bf16 v[84:87], v[170:173], v[202:205], v[84:87]
	v_mfma_f32_16x16x32_bf16 v[80:83], v[178:181], v[202:205], v[80:83]
	v_mfma_f32_16x16x32_bf16 v[68:71], v[170:173], v[210:213], v[68:71]
	v_mfma_f32_16x16x32_bf16 v[64:67], v[178:181], v[210:213], v[64:67]
	s_barrier
; #define PG8_STAGE(bufoff, gbase, voff) do { _Pragma("unroll") for (int _i = 0; _i < 2; ++_i) \
;         __builtin_amdgcn_global_load_lds((const __attribute__((address_space(1))) unsigned*)((const __attribute__((address_space(1))) char*)(gbase) + (unsigned)lnd_v((int)(voff)[_i])), (LAS unsigned*)(lds + (bufoff) + ldsw + _i * 8192), 16, 0, 0); } while (0)
; #define PG8_LDA(dst, b, h) do { _Pragma("unroll") for (int m = 0; m < 4; ++m) _Pragma("unroll") for (int k = 0; k < 2; ++k) dst[m][k] = *(const LAS bf16x8*)(lds + PG8_SA(b, h) + aoff + m * 2048 + k * 1024); } while (0)
; #define PG8_MMA(ai, bj, At, Bt) do { __builtin_amdgcn_s_setprio(1); _Pragma("unroll") for (int m = 0; m < 4; ++m) _Pragma("unroll") for (int n = 0; n < 2; ++n) _Pragma("unroll") for (int k = 0; k < 2; ++k) \
;         acc[ai][bj][m][n] = __builtin_amdgcn_mfma_f32_16x16x32_bf16(Bt[n][k], At[m][k], acc[ai][bj][m][n], 0, 0, 0); __builtin_amdgcn_s_setprio(0); } while (0)
; #define PG8_WAIT_V(n) asm volatile("s_waitcnt vmcnt(" #n ")" ::: "memory")
; #define PG8_WAIT_L(n) asm volatile("s_waitcnt lgkmcnt(" #n ")" ::: "memory")
; #define PG8_BAR __builtin_amdgcn_s_barrier()
; #define PG8_SCHED __builtin_amdgcn_sched_barrier(0)
; template <class Desc, class Epi>
; __device__ __forceinline__ void gemm_phase(const int wv_, LAS unsigned char* lds, const Desc& d, const Epi& E) {
;     ...
;             PG8_LDA(At, 1, 1); PG8_STAGE(PG8_SB(1, 0), b3, voffB); PG8_STAGE(PG8_SB(1, 1), b3 + hstepB, voffB); PG8_STAGE(PG8_SA(1, 0), a3, sA0);
;             PG8_WAIT_V(8); PG8_WAIT_L(0); PG8_BAR; PG8_MMA(1, 0, At, B0); PG8_MMA(1, 1, At, B1); PG8_BAR; PG8_SCHED;
;         }
;         if (wr == 0) PG8_BAR;
	v_mov_b32_e32 v96, v134
	ds_read_b128 v[182:185], v149 offset:49152
	ds_read_b128 v[186:189], v149 offset:50176
	ds_read_b128 v[190:193], v149 offset:51200
	ds_read_b128 v[194:197], v149 offset:52224
	ds_read_b128 v[198:201], v149 offset:53248
	ds_read_b128 v[202:205], v149 offset:54272
	ds_read_b128 v[206:209], v149 offset:55296
	ds_read_b128 v[210:213], v149 offset:56320
	s_mov_b32 m0, s71
	v_lshl_add_u64 v[130:131], s[20:21], 0, v[96:97]
	v_lshl_add_u64 v[130:131], v[130:131], 0, s[30:31]
	v_mov_b32_e32 v96, v137
	global_load_lds_dwordx4 v[130:131], off
	s_mov_b32 m0, s29
	v_lshl_add_u64 v[130:131], s[20:21], 0, v[96:97]
	v_lshl_add_u64 v[130:131], v[130:131], 0, s[30:31]
	global_load_lds_dwordx4 v[130:131], off
	s_mov_b32 m0, s78
	s_nop 0
	global_load_lds_dwordx4 v134, s[22:23]
	s_mov_b32 m0, s77
	s_nop 0
	global_load_lds_dwordx4 v137, s[22:23]
	v_mov_b32_e32 v96, v132
	s_mov_b32 m0, s65
	v_lshl_add_u64 v[130:131], s[4:5], 0, v[96:97]
	v_lshl_add_u64 v[130:131], v[130:131], 0, s[30:31]
	v_mov_b32_e32 v96, v135
	global_load_lds_dwordx4 v[130:131], off
	s_mov_b32 m0, s66
	v_lshl_add_u64 v[130:131], s[4:5], 0, v[96:97]
	v_lshl_add_u64 v[130:131], v[130:131], 0, s[30:31]
	global_load_lds_dwordx4 v[130:131], off
	s_waitcnt vmcnt(8)
	s_waitcnt lgkmcnt(0)
	s_barrier
	v_mfma_f32_16x16x32_bf16 v[60:63], v[150:153], v[182:185], v[60:63]
	v_mfma_f32_16x16x32_bf16 v[56:59], v[158:161], v[182:185], v[56:59]
	v_mfma_f32_16x16x32_bf16 v[44:47], v[150:153], v[190:193], v[44:47]
	v_mfma_f32_16x16x32_bf16 v[32:35], v[158:161], v[190:193], v[32:35]
	v_mfma_f32_16x16x32_bf16 v[16:19], v[150:153], v[198:201], v[16:19]
	v_mfma_f32_16x16x32_bf16 v[8:11], v[158:161], v[198:201], v[8:11]
	v_mfma_f32_16x16x32_bf16 v[4:7], v[150:153], v[206:209], v[4:7]
	v_mfma_f32_16x16x32_bf16 v[0:3], v[158:161], v[206:209], v[0:3]
	v_mfma_f32_16x16x32_bf16 v[60:63], v[154:157], v[186:189], v[60:63]
	v_mfma_f32_16x16x32_bf16 v[56:59], v[162:165], v[186:189], v[56:59]
	v_mfma_f32_16x16x32_bf16 v[44:47], v[154:157], v[194:197], v[44:47]
	v_mfma_f32_16x16x32_bf16 v[32:35], v[162:165], v[194:197], v[32:35]
	v_mfma_f32_16x16x32_bf16 v[16:19], v[154:157], v[202:205], v[16:19]
	v_mfma_f32_16x16x32_bf16 v[8:11], v[162:165], v[202:205], v[8:11]
	v_mfma_f32_16x16x32_bf16 v[4:7], v[154:157], v[210:213], v[4:7]
	v_mfma_f32_16x16x32_bf16 v[0:3], v[162:165], v[210:213], v[0:3]
	v_mfma_f32_16x16x32_bf16 v[52:55], v[166:169], v[182:185], v[52:55]
	v_mfma_f32_16x16x32_bf16 v[48:51], v[174:177], v[182:185], v[48:51]
	v_mfma_f32_16x16x32_bf16 v[28:31], v[166:169], v[190:193], v[28:31]
	v_mfma_f32_16x16x32_bf16 v[12:15], v[174:177], v[190:193], v[12:15]
	v_mfma_f32_16x16x32_bf16 v[36:39], v[166:169], v[198:201], v[36:39]
	v_mfma_f32_16x16x32_bf16 v[40:43], v[174:177], v[198:201], v[40:43]
	v_mfma_f32_16x16x32_bf16 v[20:23], v[166:169], v[206:209], v[20:23]
	v_mfma_f32_16x16x32_bf16 v[24:27], v[174:177], v[206:209], v[24:27]
	v_mfma_f32_16x16x32_bf16 v[52:55], v[170:173], v[186:189], v[52:55]
	v_mfma_f32_16x16x32_bf16 v[48:51], v[178:181], v[186:189], v[48:51]
	v_mfma_f32_16x16x32_bf16 v[28:31], v[170:173], v[194:197], v[28:31]
	v_mfma_f32_16x16x32_bf16 v[12:15], v[178:181], v[194:197], v[12:15]
	v_mfma_f32_16x16x32_bf16 v[36:39], v[170:173], v[202:205], v[36:39]
	v_mfma_f32_16x16x32_bf16 v[40:43], v[178:181], v[202:205], v[40:43]
	v_mfma_f32_16x16x32_bf16 v[20:23], v[170:173], v[210:213], v[20:23]
	v_mfma_f32_16x16x32_bf16 v[24:27], v[178:181], v[210:213], v[24:27]
	s_barrier
	s_movk_i32 s22, 0x100
	s_andn2_b64 vcc, exec, s[2:3]
	s_mov_b64 s[20:21], -1
	s_mov_b64 s[2:3], 0
	s_cbranch_vccz .LBB0_1481
	s_and_b64 vcc, exec, s[40:41]
	s_cbranch_vccz .LBB0_1484
	s_barrier

; #define PG8_STAGE(bufoff, gbase, voff) do { _Pragma("unroll") for (int _i = 0; _i < 2; ++_i) \
;         __builtin_amdgcn_global_load_lds((const __attribute__((address_space(1))) unsigned*)((const __attribute__((address_space(1))) char*)(gbase) + (unsigned)lnd_v((int)(voff)[_i])), (LAS unsigned*)(lds + (bufoff) + ldsw + _i * 8192), 16, 0, 0); } while (0)
; #define PG8_LDA(dst, b, h) do { _Pragma("unroll") for (int m = 0; m < 4; ++m) _Pragma("unroll") for (int k = 0; k < 2; ++k) dst[m][k] = *(const LAS bf16x8*)(lds + PG8_SA(b, h) + aoff + m * 2048 + k * 1024); } while (0)
; #define PG8_LDB(dst, b, h) do { _Pragma("unroll") for (int n = 0; n < 2; ++n) _Pragma("unroll") for (int k = 0; k < 2; ++k) dst[n][k] = *(const LAS bf16x8*)(lds + PG8_SB(b, h) + boff + n * 2048 + k * 1024); } while (0)
; #define PG8_MMA(ai, bj, At, Bt) do { __builtin_amdgcn_s_setprio(1); _Pragma("unroll") for (int m = 0; m < 4; ++m) _Pragma("unroll") for (int n = 0; n < 2; ++n) _Pragma("unroll") for (int k = 0; k < 2; ++k) \
;         acc[ai][bj][m][n] = __builtin_amdgcn_mfma_f32_16x16x32_bf16(Bt[n][k], At[m][k], acc[ai][bj][m][n], 0, 0, 0); __builtin_amdgcn_s_setprio(0); } while (0)
; template <class Desc, class Epi>
; __device__ __forceinline__ void gemm_phase(const int wv_, LAS unsigned char* lds, const Desc& d, const Epi& E) {
;     ...
;             if constexpr (Desc::GATHER) { sA0[0] = last ? voffAn[0] : voffA[0]; sA0[1] = last ? voffAn[1] : voffA[1]; sA1[0] = last ? voffAn1[0] : voffA1[0]; sA1[1] = last ? voffAn1[1] : voffA1[1]; }
;             else { sA0[0] = voffA[0]; sA0[1] = voffA[1]; sA1[0] = voffA1[0]; sA1[1] = voffA1[1]; }
;             const char* a1 = cA + (size_t)(t + 1) * kstep;
;             const char* a2 = last ? nA : cA + (size_t)(t + 2) * kstep; const char* b2 = last ? nB : cB + (size_t)(t + 2) * kstep;
;             const char* a3 = a2 + kstep; const char* b3 = b2 + kstep;
;             PG8_LDB(B0, 0, 0); PG8_LDB(B1, 0, 1); PG8_SCHED; PG8_LDA(At, 0, 0); PG8_STAGE(PG8_SA(1, 1), a1, voffA1);
;             PG8_WAIT_V(8); PG8_WAIT_L(0); PG8_BAR; PG8_MMA(0, 0, At, B0); PG8_MMA(0, 1, At, B1); PG8_BAR; PG8_SCHED;
;             PG8_LDA(At, 0, 1); PG8_STAGE(PG8_SB(0, 0), b2, voffB); PG8_STAGE(PG8_SB(0, 1), b2 + hstepB, voffB); PG8_STAGE(PG8_SA(0, 0), a2, sA0);
;             PG8_WAIT_V(8); PG8_WAIT_L(0); PG8_BAR; PG8_MMA(1, 0, At, B0); PG8_MMA(1, 1, At, B1); PG8_BAR; PG8_SCHED;
.LBB0_1565:
	s_add_u32 s4, s2, 0x100
	s_addc_u32 s5, s3, 0
	s_add_u32 s22, s29, s2
	s_addc_u32 s23, s59, s3
	s_cmp_eq_u32 s75, 12
	s_cselect_b64 vcc, -1, 0
	s_and_b64 s[20:21], vcc, exec
	s_cselect_b32 s20, 0, s4
	s_cselect_b32 s21, 0, s5
	s_cselect_b32 s22, s54, s22
	s_cselect_b32 s23, s55, s23
	s_add_u32 s20, s42, s20
	s_addc_u32 s21, s43, s21
	s_add_i32 s76, 0, 0x10000
	v_add_u32_e32 v135, s76, v143
	s_add_i32 s77, 0, 0x14000
	ds_read_b128 v[160:163], v135
	ds_read_b128 v[164:167], v135 offset:1024
	ds_read_b128 v[168:171], v135 offset:2048
	ds_read_b128 v[172:175], v135 offset:3072
	v_add_u32_e32 v135, s77, v143
	ds_read_b128 v[176:179], v135
	ds_read_b128 v[180:183], v135 offset:1024
	ds_read_b128 v[184:187], v135 offset:2048
	ds_read_b128 v[188:191], v135 offset:3072
	v_cndmask_b32_e32 v134, v157, v153, vcc
	v_cndmask_b32_e32 v132, v159, v154, vcc
	v_cndmask_b32_e32 v96, v131, v155, vcc
	v_cndmask_b32_e32 v133, v158, v156, vcc
	s_add_i32 m0, s64, 0xc000
	s_add_u32 s2, s40, s2
	ds_read_b128 v[192:195], v152
	ds_read_b128 v[196:199], v152 offset:1024
	ds_read_b128 v[200:203], v152 offset:2048
	ds_read_b128 v[204:207], v152 offset:3072
	ds_read_b128 v[208:211], v152 offset:4096
	ds_read_b128 v[212:215], v152 offset:5120
	ds_read_b128 v[220:223], v152 offset:6144
	ds_read_b128 v[224:227], v152 offset:7168
	s_addc_u32 s3, s41, s3
	global_load_lds_dwordx4 v131, s[2:3]
	s_add_i32 m0, s64, 0xe000
	s_nop 0
	global_load_lds_dwordx4 v158, s[2:3]
	s_waitcnt vmcnt(8)
	s_waitcnt lgkmcnt(0)
	s_barrier
	v_mfma_f32_16x16x32_bf16 v[122:125], v[160:163], v[192:195], v[122:125]
	v_mfma_f32_16x16x32_bf16 v[114:117], v[168:171], v[192:195], v[114:117]
	v_mfma_f32_16x16x32_bf16 v[106:109], v[160:163], v[200:203], v[106:109]
	v_mfma_f32_16x16x32_bf16 v[98:101], v[168:171], v[200:203], v[98:101]
	v_mfma_f32_16x16x32_bf16 v[88:91], v[160:163], v[208:211], v[88:91]
	v_mfma_f32_16x16x32_bf16 v[80:83], v[168:171], v[208:211], v[80:83]
	v_mfma_f32_16x16x32_bf16 v[72:75], v[160:163], v[220:223], v[72:75]
	v_mfma_f32_16x16x32_bf16 v[64:67], v[168:171], v[220:223], v[64:67]
	v_mfma_f32_16x16x32_bf16 v[122:125], v[164:167], v[196:199], v[122:125]
	v_mfma_f32_16x16x32_bf16 v[114:117], v[172:175], v[196:199], v[114:117]
	v_mfma_f32_16x16x32_bf16 v[106:109], v[164:167], v[204:207], v[106:109]
	v_mfma_f32_16x16x32_bf16 v[98:101], v[172:175], v[204:207], v[98:101]
	v_mfma_f32_16x16x32_bf16 v[88:91], v[164:167], v[212:215], v[88:91]
	v_mfma_f32_16x16x32_bf16 v[80:83], v[172:175], v[212:215], v[80:83]
	v_mfma_f32_16x16x32_bf16 v[72:75], v[164:167], v[224:227], v[72:75]
	v_mfma_f32_16x16x32_bf16 v[64:67], v[172:175], v[224:227], v[64:67]
	v_mfma_f32_16x16x32_bf16 v[126:129], v[176:179], v[192:195], v[126:129]
	v_mfma_f32_16x16x32_bf16 v[118:121], v[184:187], v[192:195], v[118:121]
	v_mfma_f32_16x16x32_bf16 v[110:113], v[176:179], v[200:203], v[110:113]
	v_mfma_f32_16x16x32_bf16 v[102:105], v[184:187], v[200:203], v[102:105]
	v_mfma_f32_16x16x32_bf16 v[92:95], v[176:179], v[208:211], v[92:95]
	v_mfma_f32_16x16x32_bf16 v[84:87], v[184:187], v[208:211], v[84:87]
	v_mfma_f32_16x16x32_bf16 v[76:79], v[176:179], v[220:223], v[76:79]
	v_mfma_f32_16x16x32_bf16 v[68:71], v[184:187], v[220:223], v[68:71]
	v_mfma_f32_16x16x32_bf16 v[126:129], v[180:183], v[196:199], v[126:129]
	v_mfma_f32_16x16x32_bf16 v[118:121], v[188:191], v[196:199], v[118:121]
	v_mfma_f32_16x16x32_bf16 v[110:113], v[180:183], v[204:207], v[110:113]
	v_mfma_f32_16x16x32_bf16 v[102:105], v[188:191], v[204:207], v[102:105]
	v_mfma_f32_16x16x32_bf16 v[92:95], v[180:183], v[212:215], v[92:95]
	v_mfma_f32_16x16x32_bf16 v[84:87], v[188:191], v[212:215], v[84:87]
	v_mfma_f32_16x16x32_bf16 v[76:79], v[180:183], v[224:227], v[76:79]
	v_mfma_f32_16x16x32_bf16 v[68:71], v[188:191], v[224:227], v[68:71]
	s_barrier
	s_add_i32 s2, s76, s63
	ds_read_b128 v[192:195], v152 offset:16384
	ds_read_b128 v[196:199], v152 offset:17408
	ds_read_b128 v[200:203], v152 offset:18432
	ds_read_b128 v[204:207], v152 offset:19456
	ds_read_b128 v[208:211], v152 offset:20480
	ds_read_b128 v[212:215], v152 offset:21504
	ds_read_b128 v[220:223], v152 offset:22528
	ds_read_b128 v[224:227], v152 offset:23552
	s_mov_b32 m0, s2
	s_nop 0
	global_load_lds_dwordx4 v138, s[22:23]
	s_add_i32 m0, s2, 0x2000
	s_add_u32 s2, s22, 0x40000
	global_load_lds_dwordx4 v141, s[22:23]
	s_addc_u32 s3, s23, 0
	s_add_i32 s76, s77, s63
	s_mov_b32 m0, s76
	s_nop 0
	global_load_lds_dwordx4 v138, s[2:3]
	s_add_i32 m0, s76, 0x2000
	s_nop 0
	global_load_lds_dwordx4 v141, s[2:3]
	s_mov_b32 m0, s64
	s_nop 0
	global_load_lds_dwordx4 v134, s[20:21]
	s_mov_b32 m0, s65
	s_nop 0
	global_load_lds_dwordx4 v132, s[20:21]
	s_waitcnt vmcnt(8)
	s_waitcnt lgkmcnt(0)
	s_barrier
; #define PG8_STAGE(bufoff, gbase, voff) do { _Pragma("unroll") for (int _i = 0; _i < 2; ++_i) \
;         __builtin_amdgcn_global_load_lds((const __attribute__((address_space(1))) unsigned*)((const __attribute__((address_space(1))) char*)(gbase) + (unsigned)lnd_v((int)(voff)[_i])), (LAS unsigned*)(lds + (bufoff) + ldsw + _i * 8192), 16, 0, 0); } while (0)
; #define PG8_LDA(dst, b, h) do { _Pragma("unroll") for (int m = 0; m < 4; ++m) _Pragma("unroll") for (int k = 0; k < 2; ++k) dst[m][k] = *(const LAS bf16x8*)(lds + PG8_SA(b, h) + aoff + m * 2048 + k * 1024); } while (0)
; #define PG8_LDB(dst, b, h) do { _Pragma("unroll") for (int n = 0; n < 2; ++n) _Pragma("unroll") for (int k = 0; k < 2; ++k) dst[n][k] = *(const LAS bf16x8*)(lds + PG8_SB(b, h) + boff + n * 2048 + k * 1024); } while (0)
; #define PG8_MMA(ai, bj, At, Bt) do { __builtin_amdgcn_s_setprio(1); _Pragma("unroll") for (int m = 0; m < 4; ++m) _Pragma("unroll") for (int n = 0; n < 2; ++n) _Pragma("unroll") for (int k = 0; k < 2; ++k) \
;         acc[ai][bj][m][n] = __builtin_amdgcn_mfma_f32_16x16x32_bf16(Bt[n][k], At[m][k], acc[ai][bj][m][n], 0, 0, 0); __builtin_amdgcn_s_setprio(0); } while (0)
; #define PG8_WAIT_V(n) asm volatile("s_waitcnt vmcnt(" #n ")" ::: "memory")
; #define PG8_WAIT_L(n) asm volatile("s_waitcnt lgkmcnt(" #n ")" ::: "memory")
; #define PG8_BAR __builtin_amdgcn_s_barrier()
; #define PG8_SCHED __builtin_amdgcn_sched_barrier(0)
; template <class Desc, class Epi>
; __device__ __forceinline__ void gemm_phase(const int wv_, LAS unsigned char* lds, const Desc& d, const Epi& E) {
;     ...
;             PG8_WAIT_V(8); PG8_WAIT_L(0); PG8_BAR; PG8_MMA(1, 0, At, B0); PG8_MMA(1, 1, At, B1); PG8_BAR; PG8_SCHED;
;             PG8_LDB(B0, 1, 0); PG8_LDB(B1, 1, 1); PG8_SCHED; PG8_LDA(At, 1, 0); PG8_STAGE(PG8_SA(0, 1), a2, sA1);
;             PG8_WAIT_V(8); PG8_WAIT_L(0); PG8_BAR; PG8_MMA(0, 0, At, B0); PG8_MMA(0, 1, At, B1); PG8_BAR; PG8_SCHED;
	v_mfma_f32_16x16x32_bf16 v[56:59], v[160:163], v[192:195], v[56:59]
	v_mfma_f32_16x16x32_bf16 v[48:51], v[168:171], v[192:195], v[48:51]
	v_mfma_f32_16x16x32_bf16 v[40:43], v[160:163], v[200:203], v[40:43]
	v_mfma_f32_16x16x32_bf16 v[32:35], v[168:171], v[200:203], v[32:35]
	v_mfma_f32_16x16x32_bf16 v[24:27], v[160:163], v[208:211], v[24:27]
	v_mfma_f32_16x16x32_bf16 v[16:19], v[168:171], v[208:211], v[16:19]
	v_mfma_f32_16x16x32_bf16 v[8:11], v[160:163], v[220:223], v[8:11]
	v_mfma_f32_16x16x32_bf16 v[4:7], v[168:171], v[220:223], v[4:7]
	v_mfma_f32_16x16x32_bf16 v[56:59], v[164:167], v[196:199], v[56:59]
	v_mfma_f32_16x16x32_bf16 v[48:51], v[172:175], v[196:199], v[48:51]
	v_mfma_f32_16x16x32_bf16 v[40:43], v[164:167], v[204:207], v[40:43]
	v_mfma_f32_16x16x32_bf16 v[32:35], v[172:175], v[204:207], v[32:35]
	v_mfma_f32_16x16x32_bf16 v[24:27], v[164:167], v[212:215], v[24:27]
	v_mfma_f32_16x16x32_bf16 v[16:19], v[172:175], v[212:215], v[16:19]
	v_mfma_f32_16x16x32_bf16 v[8:11], v[164:167], v[224:227], v[8:11]
	v_mfma_f32_16x16x32_bf16 v[4:7], v[172:175], v[224:227], v[4:7]
	v_mfma_f32_16x16x32_bf16 v[60:63], v[176:179], v[192:195], v[60:63]
	v_mfma_f32_16x16x32_bf16 v[52:55], v[184:187], v[192:195], v[52:55]
	v_mfma_f32_16x16x32_bf16 v[44:47], v[176:179], v[200:203], v[44:47]
	v_mfma_f32_16x16x32_bf16 v[36:39], v[184:187], v[200:203], v[36:39]
	v_mfma_f32_16x16x32_bf16 v[28:31], v[176:179], v[208:211], v[28:31]
	v_mfma_f32_16x16x32_bf16 v[20:23], v[184:187], v[208:211], v[20:23]
	v_mfma_f32_16x16x32_bf16 v[12:15], v[176:179], v[220:223], v[12:15]
	v_mfma_f32_16x16x32_bf16 v[0:3], v[184:187], v[220:223], v[0:3]
	v_mfma_f32_16x16x32_bf16 v[60:63], v[180:183], v[196:199], v[60:63]
	v_mfma_f32_16x16x32_bf16 v[52:55], v[188:191], v[196:199], v[52:55]
	v_mfma_f32_16x16x32_bf16 v[44:47], v[180:183], v[204:207], v[44:47]
	v_mfma_f32_16x16x32_bf16 v[36:39], v[188:191], v[204:207], v[36:39]
	v_mfma_f32_16x16x32_bf16 v[28:31], v[180:183], v[212:215], v[28:31]
	v_mfma_f32_16x16x32_bf16 v[20:23], v[188:191], v[212:215], v[20:23]
	v_mfma_f32_16x16x32_bf16 v[12:15], v[180:183], v[224:227], v[12:15]
	v_mfma_f32_16x16x32_bf16 v[0:3], v[188:191], v[224:227], v[0:3]
	s_barrier
	s_add_i32 s2, 0, 0x18000
	v_add_u32_e32 v135, s2, v143
	s_add_i32 s76, 0, 0x1c000
	ds_read_b128 v[160:163], v135
	ds_read_b128 v[164:167], v135 offset:1024
	ds_read_b128 v[168:171], v135 offset:2048
	ds_read_b128 v[172:175], v135 offset:3072
	v_add_u32_e32 v135, s76, v143
	ds_read_b128 v[176:179], v135
	ds_read_b128 v[180:183], v135 offset:1024
	ds_read_b128 v[184:187], v135 offset:2048
	ds_read_b128 v[188:191], v135 offset:3072
	s_mov_b32 m0, s68
	ds_read_b128 v[192:195], v152 offset:32768
	ds_read_b128 v[196:199], v152 offset:33792
	ds_read_b128 v[200:203], v152 offset:34816
	ds_read_b128 v[204:207], v152 offset:35840
	ds_read_b128 v[208:211], v152 offset:36864
	ds_read_b128 v[212:215], v152 offset:37888
	ds_read_b128 v[220:223], v152 offset:38912
	ds_read_b128 v[224:227], v152 offset:39936
	s_nop 0
	global_load_lds_dwordx4 v96, s[20:21]
	s_mov_b32 m0, s69
	s_nop 0
	global_load_lds_dwordx4 v133, s[20:21]
	s_waitcnt vmcnt(8)
	s_waitcnt lgkmcnt(0)
	s_barrier
	v_mfma_f32_16x16x32_bf16 v[122:125], v[160:163], v[192:195], v[122:125]
	v_mfma_f32_16x16x32_bf16 v[114:117], v[168:171], v[192:195], v[114:117]
	v_mfma_f32_16x16x32_bf16 v[106:109], v[160:163], v[200:203], v[106:109]
	v_mfma_f32_16x16x32_bf16 v[98:101], v[168:171], v[200:203], v[98:101]
	v_mfma_f32_16x16x32_bf16 v[88:91], v[160:163], v[208:211], v[88:91]
	v_mfma_f32_16x16x32_bf16 v[80:83], v[168:171], v[208:211], v[80:83]
	v_mfma_f32_16x16x32_bf16 v[72:75], v[160:163], v[220:223], v[72:75]
	v_mfma_f32_16x16x32_bf16 v[64:67], v[168:171], v[220:223], v[64:67]
	v_mfma_f32_16x16x32_bf16 v[122:125], v[164:167], v[196:199], v[122:125]
	v_mfma_f32_16x16x32_bf16 v[114:117], v[172:175], v[196:199], v[114:117]
	v_mfma_f32_16x16x32_bf16 v[106:109], v[164:167], v[204:207], v[106:109]
	v_mfma_f32_16x16x32_bf16 v[98:101], v[172:175], v[204:207], v[98:101]
	v_mfma_f32_16x16x32_bf16 v[88:91], v[164:167], v[212:215], v[88:91]
	v_mfma_f32_16x16x32_bf16 v[80:83], v[172:175], v[212:215], v[80:83]
	v_mfma_f32_16x16x32_bf16 v[72:75], v[164:167], v[224:227], v[72:75]
	v_mfma_f32_16x16x32_bf16 v[64:67], v[172:175], v[224:227], v[64:67]
	v_mfma_f32_16x16x32_bf16 v[126:129], v[176:179], v[192:195], v[126:129]
	v_mfma_f32_16x16x32_bf16 v[118:121], v[184:187], v[192:195], v[118:121]
	v_mfma_f32_16x16x32_bf16 v[110:113], v[176:179], v[200:203], v[110:113]
	v_mfma_f32_16x16x32_bf16 v[102:105], v[184:187], v[200:203], v[102:105]
	v_mfma_f32_16x16x32_bf16 v[92:95], v[176:179], v[208:211], v[92:95]
	v_mfma_f32_16x16x32_bf16 v[84:87], v[184:187], v[208:211], v[84:87]
	v_mfma_f32_16x16x32_bf16 v[76:79], v[176:179], v[220:223], v[76:79]
	v_mfma_f32_16x16x32_bf16 v[68:71], v[184:187], v[220:223], v[68:71]
	v_mfma_f32_16x16x32_bf16 v[126:129], v[180:183], v[196:199], v[126:129]
	v_mfma_f32_16x16x32_bf16 v[118:121], v[188:191], v[196:199], v[118:121]
	v_mfma_f32_16x16x32_bf16 v[110:113], v[180:183], v[204:207], v[110:113]
	v_mfma_f32_16x16x32_bf16 v[102:105], v[188:191], v[204:207], v[102:105]
	v_mfma_f32_16x16x32_bf16 v[92:95], v[180:183], v[212:215], v[92:95]
	v_mfma_f32_16x16x32_bf16 v[84:87], v[188:191], v[212:215], v[84:87]
	v_mfma_f32_16x16x32_bf16 v[76:79], v[180:183], v[224:227], v[76:79]
	v_mfma_f32_16x16x32_bf16 v[68:71], v[188:191], v[224:227], v[68:71]
	s_barrier
; #define PG8_STAGE(bufoff, gbase, voff) do { _Pragma("unroll") for (int _i = 0; _i < 2; ++_i) \
;         __builtin_amdgcn_global_load_lds((const __attribute__((address_space(1))) unsigned*)((const __attribute__((address_space(1))) char*)(gbase) + (unsigned)lnd_v((int)(voff)[_i])), (LAS unsigned*)(lds + (bufoff) + ldsw + _i * 8192), 16, 0, 0); } while (0)
; #define PG8_LDA(dst, b, h) do { _Pragma("unroll") for (int m = 0; m < 4; ++m) _Pragma("unroll") for (int k = 0; k < 2; ++k) dst[m][k] = *(const LAS bf16x8*)(lds + PG8_SA(b, h) + aoff + m * 2048 + k * 1024); } while (0)
; #define PG8_MMA(ai, bj, At, Bt) do { __builtin_amdgcn_s_setprio(1); _Pragma("unroll") for (int m = 0; m < 4; ++m) _Pragma("unroll") for (int n = 0; n < 2; ++n) _Pragma("unroll") for (int k = 0; k < 2; ++k) \
;         acc[ai][bj][m][n] = __builtin_amdgcn_mfma_f32_16x16x32_bf16(Bt[n][k], At[m][k], acc[ai][bj][m][n], 0, 0, 0); __builtin_amdgcn_s_setprio(0); } while (0)
; #define PG8_WAIT_V(n) asm volatile("s_waitcnt vmcnt(" #n ")" ::: "memory")
; #define PG8_WAIT_L(n) asm volatile("s_waitcnt lgkmcnt(" #n ")" ::: "memory")
; #define PG8_BAR __builtin_amdgcn_s_barrier()
; #define PG8_SCHED __builtin_amdgcn_sched_barrier(0)
; template <class Desc, class Epi>
; __device__ __forceinline__ void gemm_phase(const int wv_, LAS unsigned char* lds, const Desc& d, const Epi& E) {
;     ...
;             PG8_LDA(At, 1, 1); PG8_STAGE(PG8_SB(1, 0), b3, voffB); PG8_STAGE(PG8_SB(1, 1), b3 + hstepB, voffB); PG8_STAGE(PG8_SA(1, 0), a3, sA0);
;             PG8_WAIT_V(8); PG8_WAIT_L(0); PG8_BAR; PG8_MMA(1, 0, At, B0); PG8_MMA(1, 1, At, B1); PG8_BAR; PG8_SCHED;
;         }
;         if (wr == 0) PG8_BAR;
	v_mov_b32_e32 v96, v138
	ds_read_b128 v[192:195], v152 offset:49152
	ds_read_b128 v[196:199], v152 offset:50176
	ds_read_b128 v[200:203], v152 offset:51200
	ds_read_b128 v[204:207], v152 offset:52224
	ds_read_b128 v[208:211], v152 offset:53248
	ds_read_b128 v[212:215], v152 offset:54272
	ds_read_b128 v[220:223], v152 offset:55296
	ds_read_b128 v[224:227], v152 offset:56320
	s_add_i32 s2, s2, s63
	v_lshl_add_u64 v[228:229], s[22:23], 0, v[96:97]
	v_lshl_add_u64 v[228:229], v[228:229], 0, s[30:31]
	s_mov_b32 m0, s2
	v_mov_b32_e32 v96, v141
	global_load_lds_dwordx4 v[228:229], off
	s_add_i32 m0, s2, 0x2000
	s_add_u32 s2, s22, 0x40080
	v_lshl_add_u64 v[228:229], s[22:23], 0, v[96:97]
	v_lshl_add_u64 v[228:229], v[228:229], 0, s[30:31]
	s_addc_u32 s3, s23, 0
	s_add_i32 s22, s76, s63
	global_load_lds_dwordx4 v[228:229], off
	s_mov_b32 m0, s22
	v_mov_b32_e32 v135, v97
	global_load_lds_dwordx4 v138, s[2:3]
	v_mov_b32_e32 v96, v141
	s_add_i32 m0, s22, 0x2000
	v_mov_b32_e32 v133, v97
	global_load_lds_dwordx4 v96, s[2:3]
	s_mov_b32 m0, s70
	v_lshl_add_u64 v[134:135], s[20:21], 0, v[134:135]
	v_lshl_add_u64 v[134:135], v[134:135], 0, s[30:31]
	global_load_lds_dwordx4 v[134:135], off
	s_mov_b32 m0, s71
	v_lshl_add_u64 v[132:133], s[20:21], 0, v[132:133]
	v_lshl_add_u64 v[132:133], v[132:133], 0, s[30:31]
	global_load_lds_dwordx4 v[132:133], off
	s_waitcnt vmcnt(8)
	s_waitcnt lgkmcnt(0)
	s_barrier
	v_mfma_f32_16x16x32_bf16 v[56:59], v[160:163], v[192:195], v[56:59]
	v_mfma_f32_16x16x32_bf16 v[48:51], v[168:171], v[192:195], v[48:51]
	v_mfma_f32_16x16x32_bf16 v[40:43], v[160:163], v[200:203], v[40:43]
	v_mfma_f32_16x16x32_bf16 v[32:35], v[168:171], v[200:203], v[32:35]
	v_mfma_f32_16x16x32_bf16 v[24:27], v[160:163], v[208:211], v[24:27]
	v_mfma_f32_16x16x32_bf16 v[16:19], v[168:171], v[208:211], v[16:19]
	v_mfma_f32_16x16x32_bf16 v[8:11], v[160:163], v[220:223], v[8:11]
	v_mfma_f32_16x16x32_bf16 v[4:7], v[168:171], v[220:223], v[4:7]
	v_mfma_f32_16x16x32_bf16 v[56:59], v[164:167], v[196:199], v[56:59]
	v_mfma_f32_16x16x32_bf16 v[48:51], v[172:175], v[196:199], v[48:51]
	v_mfma_f32_16x16x32_bf16 v[40:43], v[164:167], v[204:207], v[40:43]
	v_mfma_f32_16x16x32_bf16 v[32:35], v[172:175], v[204:207], v[32:35]
	v_mfma_f32_16x16x32_bf16 v[24:27], v[164:167], v[212:215], v[24:27]
	v_mfma_f32_16x16x32_bf16 v[16:19], v[172:175], v[212:215], v[16:19]
	v_mfma_f32_16x16x32_bf16 v[8:11], v[164:167], v[224:227], v[8:11]
	v_mfma_f32_16x16x32_bf16 v[4:7], v[172:175], v[224:227], v[4:7]
	v_mfma_f32_16x16x32_bf16 v[60:63], v[176:179], v[192:195], v[60:63]
	v_mfma_f32_16x16x32_bf16 v[52:55], v[184:187], v[192:195], v[52:55]
	v_mfma_f32_16x16x32_bf16 v[44:47], v[176:179], v[200:203], v[44:47]
	v_mfma_f32_16x16x32_bf16 v[36:39], v[184:187], v[200:203], v[36:39]
	v_mfma_f32_16x16x32_bf16 v[28:31], v[176:179], v[208:211], v[28:31]
	v_mfma_f32_16x16x32_bf16 v[20:23], v[184:187], v[208:211], v[20:23]
	v_mfma_f32_16x16x32_bf16 v[12:15], v[176:179], v[220:223], v[12:15]
	v_mfma_f32_16x16x32_bf16 v[0:3], v[184:187], v[220:223], v[0:3]
	v_mfma_f32_16x16x32_bf16 v[60:63], v[180:183], v[196:199], v[60:63]
	v_mfma_f32_16x16x32_bf16 v[52:55], v[188:191], v[196:199], v[52:55]
	v_mfma_f32_16x16x32_bf16 v[44:47], v[180:183], v[204:207], v[44:47]
	v_mfma_f32_16x16x32_bf16 v[36:39], v[188:191], v[204:207], v[36:39]
	v_mfma_f32_16x16x32_bf16 v[28:31], v[180:183], v[212:215], v[28:31]
	v_mfma_f32_16x16x32_bf16 v[20:23], v[188:191], v[212:215], v[20:23]
	v_mfma_f32_16x16x32_bf16 v[12:15], v[180:183], v[224:227], v[12:15]
	v_mfma_f32_16x16x32_bf16 v[0:3], v[188:191], v[224:227], v[0:3]
	s_barrier
	s_add_i32 s75, s75, 2
	s_cmp_gt_u32 s75, 13
	s_mov_b64 s[2:3], s[4:5]
	s_cbranch_scc0 .LBB0_1565
	s_and_b64 vcc, exec, s[52:53]
	s_cbranch_vccz .LBB0_1568
	s_barrier

; #define PG8_STAGE(bufoff, gbase, voff) do { _Pragma("unroll") for (int _i = 0; _i < 2; ++_i) \
;         __builtin_amdgcn_global_load_lds((const __attribute__((address_space(1))) unsigned*)((const __attribute__((address_space(1))) char*)(gbase) + (unsigned)lnd_v((int)(voff)[_i])), (LAS unsigned*)(lds + (bufoff) + ldsw + _i * 8192), 16, 0, 0); } while (0)
; #define PG8_LDA(dst, b, h) do { _Pragma("unroll") for (int m = 0; m < 4; ++m) _Pragma("unroll") for (int k = 0; k < 2; ++k) dst[m][k] = *(const LAS bf16x8*)(lds + PG8_SA(b, h) + aoff + m * 2048 + k * 1024); } while (0)
; #define PG8_LDB(dst, b, h) do { _Pragma("unroll") for (int n = 0; n < 2; ++n) _Pragma("unroll") for (int k = 0; k < 2; ++k) dst[n][k] = *(const LAS bf16x8*)(lds + PG8_SB(b, h) + boff + n * 2048 + k * 1024); } while (0)
; #define PG8_MMA(ai, bj, At, Bt) do { __builtin_amdgcn_s_setprio(1); _Pragma("unroll") for (int m = 0; m < 4; ++m) _Pragma("unroll") for (int n = 0; n < 2; ++n) _Pragma("unroll") for (int k = 0; k < 2; ++k) \
;         acc[ai][bj][m][n] = __builtin_amdgcn_mfma_f32_16x16x32_bf16(Bt[n][k], At[m][k], acc[ai][bj][m][n], 0, 0, 0); __builtin_amdgcn_s_setprio(0); } while (0)
; template <class Desc, class Epi>
; __device__ __forceinline__ void gemm_phase(const int wv_, LAS unsigned char* lds, const Desc& d, const Epi& E) {
;     ...
;             if constexpr (Desc::GATHER) { sA0[0] = last ? voffAn[0] : voffA[0]; sA0[1] = last ? voffAn[1] : voffA[1]; sA1[0] = last ? voffAn1[0] : voffA1[0]; sA1[1] = last ? voffAn1[1] : voffA1[1]; }
;             else { sA0[0] = voffA[0]; sA0[1] = voffA[1]; sA1[0] = voffA1[0]; sA1[1] = voffA1[1]; }
;             const char* a1 = cA + (size_t)(t + 1) * kstep;
;             const char* a2 = last ? nA : cA + (size_t)(t + 2) * kstep; const char* b2 = last ? nB : cB + (size_t)(t + 2) * kstep;
;             const char* a3 = a2 + kstep; const char* b3 = b2 + kstep;
;             PG8_LDB(B0, 0, 0); PG8_LDB(B1, 0, 1); PG8_SCHED; PG8_LDA(At, 0, 0); PG8_STAGE(PG8_SA(1, 1), a1, voffA1);
;             PG8_WAIT_V(8); PG8_WAIT_L(0); PG8_BAR; PG8_MMA(0, 0, At, B0); PG8_MMA(0, 1, At, B1); PG8_BAR; PG8_SCHED;
;             PG8_LDA(At, 0, 1); PG8_STAGE(PG8_SB(0, 0), b2, voffB); PG8_STAGE(PG8_SB(0, 1), b2 + hstepB, voffB); PG8_STAGE(PG8_SA(0, 0), a2, sA0);
;             PG8_WAIT_V(8); PG8_WAIT_L(0); PG8_BAR; PG8_MMA(1, 0, At, B0); PG8_MMA(1, 1, At, B1); PG8_BAR; PG8_SCHED;
.LBB0_1861:
	s_add_u32 s4, s2, 0x100
	s_addc_u32 s5, s3, 0
	s_add_u32 s22, s29, s2
	s_addc_u32 s23, s51, s3
	s_cmp_eq_u32 s66, 12
	s_cselect_b64 vcc, -1, 0
	s_and_b64 s[20:21], vcc, exec
	s_cselect_b32 s20, 0, s4
	s_cselect_b32 s21, 0, s5
	s_cselect_b32 s22, s46, s22
	s_cselect_b32 s23, s47, s23
	s_add_u32 s20, s42, s20
	s_addc_u32 s21, s43, s21
	s_add_i32 s67, 0, 0x10000
	v_add_u32_e32 v135, s67, v143
	s_add_i32 s68, 0, 0x14000
	ds_read_b128 v[160:163], v135
	ds_read_b128 v[164:167], v135 offset:1024
	ds_read_b128 v[168:171], v135 offset:2048
	ds_read_b128 v[172:175], v135 offset:3072
	v_add_u32_e32 v135, s68, v143
	ds_read_b128 v[176:179], v135
	ds_read_b128 v[180:183], v135 offset:1024
	ds_read_b128 v[184:187], v135 offset:2048
	ds_read_b128 v[188:191], v135 offset:3072
	v_cndmask_b32_e32 v134, v157, v153, vcc
	v_cndmask_b32_e32 v132, v159, v154, vcc
	v_cndmask_b32_e32 v96, v131, v155, vcc
	v_cndmask_b32_e32 v133, v158, v156, vcc
	s_add_i32 m0, s57, 0xc000
	s_add_u32 s2, s38, s2
	ds_read_b128 v[192:195], v152
	ds_read_b128 v[196:199], v152 offset:1024
	ds_read_b128 v[200:203], v152 offset:2048
	ds_read_b128 v[204:207], v152 offset:3072
	ds_read_b128 v[208:211], v152 offset:4096
	ds_read_b128 v[212:215], v152 offset:5120
	ds_read_b128 v[220:223], v152 offset:6144
	ds_read_b128 v[224:227], v152 offset:7168
	s_addc_u32 s3, s39, s3
	global_load_lds_dwordx4 v131, s[2:3]
	s_add_i32 m0, s57, 0xe000
	s_nop 0
	global_load_lds_dwordx4 v158, s[2:3]
	s_waitcnt vmcnt(8)
	s_waitcnt lgkmcnt(0)
	s_barrier
	v_mfma_f32_16x16x32_bf16 v[122:125], v[160:163], v[192:195], v[122:125]
	v_mfma_f32_16x16x32_bf16 v[114:117], v[168:171], v[192:195], v[114:117]
	v_mfma_f32_16x16x32_bf16 v[106:109], v[160:163], v[200:203], v[106:109]
	v_mfma_f32_16x16x32_bf16 v[98:101], v[168:171], v[200:203], v[98:101]
	v_mfma_f32_16x16x32_bf16 v[88:91], v[160:163], v[208:211], v[88:91]
	v_mfma_f32_16x16x32_bf16 v[80:83], v[168:171], v[208:211], v[80:83]
	v_mfma_f32_16x16x32_bf16 v[72:75], v[160:163], v[220:223], v[72:75]
	v_mfma_f32_16x16x32_bf16 v[64:67], v[168:171], v[220:223], v[64:67]
	v_mfma_f32_16x16x32_bf16 v[122:125], v[164:167], v[196:199], v[122:125]
	v_mfma_f32_16x16x32_bf16 v[114:117], v[172:175], v[196:199], v[114:117]
	v_mfma_f32_16x16x32_bf16 v[106:109], v[164:167], v[204:207], v[106:109]
	v_mfma_f32_16x16x32_bf16 v[98:101], v[172:175], v[204:207], v[98:101]
	v_mfma_f32_16x16x32_bf16 v[88:91], v[164:167], v[212:215], v[88:91]
	v_mfma_f32_16x16x32_bf16 v[80:83], v[172:175], v[212:215], v[80:83]
	v_mfma_f32_16x16x32_bf16 v[72:75], v[164:167], v[224:227], v[72:75]
	v_mfma_f32_16x16x32_bf16 v[64:67], v[172:175], v[224:227], v[64:67]
	v_mfma_f32_16x16x32_bf16 v[126:129], v[176:179], v[192:195], v[126:129]
	v_mfma_f32_16x16x32_bf16 v[118:121], v[184:187], v[192:195], v[118:121]
	v_mfma_f32_16x16x32_bf16 v[110:113], v[176:179], v[200:203], v[110:113]
	v_mfma_f32_16x16x32_bf16 v[102:105], v[184:187], v[200:203], v[102:105]
	v_mfma_f32_16x16x32_bf16 v[92:95], v[176:179], v[208:211], v[92:95]
	v_mfma_f32_16x16x32_bf16 v[84:87], v[184:187], v[208:211], v[84:87]
	v_mfma_f32_16x16x32_bf16 v[76:79], v[176:179], v[220:223], v[76:79]
	v_mfma_f32_16x16x32_bf16 v[68:71], v[184:187], v[220:223], v[68:71]
	v_mfma_f32_16x16x32_bf16 v[126:129], v[180:183], v[196:199], v[126:129]
	v_mfma_f32_16x16x32_bf16 v[118:121], v[188:191], v[196:199], v[118:121]
	v_mfma_f32_16x16x32_bf16 v[110:113], v[180:183], v[204:207], v[110:113]
	v_mfma_f32_16x16x32_bf16 v[102:105], v[188:191], v[204:207], v[102:105]
	v_mfma_f32_16x16x32_bf16 v[92:95], v[180:183], v[212:215], v[92:95]
	v_mfma_f32_16x16x32_bf16 v[84:87], v[188:191], v[212:215], v[84:87]
	v_mfma_f32_16x16x32_bf16 v[76:79], v[180:183], v[224:227], v[76:79]
	v_mfma_f32_16x16x32_bf16 v[68:71], v[188:191], v[224:227], v[68:71]
	s_barrier
	s_add_i32 s2, s67, s56
	ds_read_b128 v[192:195], v152 offset:16384
	ds_read_b128 v[196:199], v152 offset:17408
	ds_read_b128 v[200:203], v152 offset:18432
	ds_read_b128 v[204:207], v152 offset:19456
	ds_read_b128 v[208:211], v152 offset:20480
	ds_read_b128 v[212:215], v152 offset:21504
	ds_read_b128 v[220:223], v152 offset:22528
	ds_read_b128 v[224:227], v152 offset:23552
	s_mov_b32 m0, s2
	s_nop 0
	global_load_lds_dwordx4 v138, s[22:23]
	s_add_i32 m0, s2, 0x2000
	s_add_u32 s2, s22, 0x40000
	global_load_lds_dwordx4 v141, s[22:23]
	s_addc_u32 s3, s23, 0
	s_add_i32 s67, s68, s56
	s_mov_b32 m0, s67
	s_nop 0
	global_load_lds_dwordx4 v138, s[2:3]
	s_add_i32 m0, s67, 0x2000
	s_nop 0
	global_load_lds_dwordx4 v141, s[2:3]
	s_mov_b32 m0, s57
	s_nop 0
	global_load_lds_dwordx4 v134, s[20:21]
	s_mov_b32 m0, s58
	s_nop 0
	global_load_lds_dwordx4 v132, s[20:21]
	s_waitcnt vmcnt(8)
	s_waitcnt lgkmcnt(0)
	s_barrier
; #define PG8_STAGE(bufoff, gbase, voff) do { _Pragma("unroll") for (int _i = 0; _i < 2; ++_i) \
;         __builtin_amdgcn_global_load_lds((const __attribute__((address_space(1))) unsigned*)((const __attribute__((address_space(1))) char*)(gbase) + (unsigned)lnd_v((int)(voff)[_i])), (LAS unsigned*)(lds + (bufoff) + ldsw + _i * 8192), 16, 0, 0); } while (0)
; #define PG8_LDA(dst, b, h) do { _Pragma("unroll") for (int m = 0; m < 4; ++m) _Pragma("unroll") for (int k = 0; k < 2; ++k) dst[m][k] = *(const LAS bf16x8*)(lds + PG8_SA(b, h) + aoff + m * 2048 + k * 1024); } while (0)
; #define PG8_LDB(dst, b, h) do { _Pragma("unroll") for (int n = 0; n < 2; ++n) _Pragma("unroll") for (int k = 0; k < 2; ++k) dst[n][k] = *(const LAS bf16x8*)(lds + PG8_SB(b, h) + boff + n * 2048 + k * 1024); } while (0)
; #define PG8_MMA(ai, bj, At, Bt) do { __builtin_amdgcn_s_setprio(1); _Pragma("unroll") for (int m = 0; m < 4; ++m) _Pragma("unroll") for (int n = 0; n < 2; ++n) _Pragma("unroll") for (int k = 0; k < 2; ++k) \
;         acc[ai][bj][m][n] = __builtin_amdgcn_mfma_f32_16x16x32_bf16(Bt[n][k], At[m][k], acc[ai][bj][m][n], 0, 0, 0); __builtin_amdgcn_s_setprio(0); } while (0)
; #define PG8_WAIT_V(n) asm volatile("s_waitcnt vmcnt(" #n ")" ::: "memory")
; #define PG8_WAIT_L(n) asm volatile("s_waitcnt lgkmcnt(" #n ")" ::: "memory")
; #define PG8_BAR __builtin_amdgcn_s_barrier()
; #define PG8_SCHED __builtin_amdgcn_sched_barrier(0)
; template <class Desc, class Epi>
; __device__ __forceinline__ void gemm_phase(const int wv_, LAS unsigned char* lds, const Desc& d, const Epi& E) {
;     ...
;             PG8_WAIT_V(8); PG8_WAIT_L(0); PG8_BAR; PG8_MMA(1, 0, At, B0); PG8_MMA(1, 1, At, B1); PG8_BAR; PG8_SCHED;
;             PG8_LDB(B0, 1, 0); PG8_LDB(B1, 1, 1); PG8_SCHED; PG8_LDA(At, 1, 0); PG8_STAGE(PG8_SA(0, 1), a2, sA1);
;             PG8_WAIT_V(8); PG8_WAIT_L(0); PG8_BAR; PG8_MMA(0, 0, At, B0); PG8_MMA(0, 1, At, B1); PG8_BAR; PG8_SCHED;
	v_mfma_f32_16x16x32_bf16 v[56:59], v[160:163], v[192:195], v[56:59]
	v_mfma_f32_16x16x32_bf16 v[48:51], v[168:171], v[192:195], v[48:51]
	v_mfma_f32_16x16x32_bf16 v[40:43], v[160:163], v[200:203], v[40:43]
	v_mfma_f32_16x16x32_bf16 v[32:35], v[168:171], v[200:203], v[32:35]
	v_mfma_f32_16x16x32_bf16 v[24:27], v[160:163], v[208:211], v[24:27]
	v_mfma_f32_16x16x32_bf16 v[16:19], v[168:171], v[208:211], v[16:19]
	v_mfma_f32_16x16x32_bf16 v[8:11], v[160:163], v[220:223], v[8:11]
	v_mfma_f32_16x16x32_bf16 v[4:7], v[168:171], v[220:223], v[4:7]
	v_mfma_f32_16x16x32_bf16 v[56:59], v[164:167], v[196:199], v[56:59]
	v_mfma_f32_16x16x32_bf16 v[48:51], v[172:175], v[196:199], v[48:51]
	v_mfma_f32_16x16x32_bf16 v[40:43], v[164:167], v[204:207], v[40:43]
	v_mfma_f32_16x16x32_bf16 v[32:35], v[172:175], v[204:207], v[32:35]
	v_mfma_f32_16x16x32_bf16 v[24:27], v[164:167], v[212:215], v[24:27]
	v_mfma_f32_16x16x32_bf16 v[16:19], v[172:175], v[212:215], v[16:19]
	v_mfma_f32_16x16x32_bf16 v[8:11], v[164:167], v[224:227], v[8:11]
	v_mfma_f32_16x16x32_bf16 v[4:7], v[172:175], v[224:227], v[4:7]
	v_mfma_f32_16x16x32_bf16 v[60:63], v[176:179], v[192:195], v[60:63]
	v_mfma_f32_16x16x32_bf16 v[52:55], v[184:187], v[192:195], v[52:55]
	v_mfma_f32_16x16x32_bf16 v[44:47], v[176:179], v[200:203], v[44:47]
	v_mfma_f32_16x16x32_bf16 v[36:39], v[184:187], v[200:203], v[36:39]
	v_mfma_f32_16x16x32_bf16 v[28:31], v[176:179], v[208:211], v[28:31]
	v_mfma_f32_16x16x32_bf16 v[20:23], v[184:187], v[208:211], v[20:23]
	v_mfma_f32_16x16x32_bf16 v[12:15], v[176:179], v[220:223], v[12:15]
	v_mfma_f32_16x16x32_bf16 v[0:3], v[184:187], v[220:223], v[0:3]
	v_mfma_f32_16x16x32_bf16 v[60:63], v[180:183], v[196:199], v[60:63]
	v_mfma_f32_16x16x32_bf16 v[52:55], v[188:191], v[196:199], v[52:55]
	v_mfma_f32_16x16x32_bf16 v[44:47], v[180:183], v[204:207], v[44:47]
	v_mfma_f32_16x16x32_bf16 v[36:39], v[188:191], v[204:207], v[36:39]
	v_mfma_f32_16x16x32_bf16 v[28:31], v[180:183], v[212:215], v[28:31]
	v_mfma_f32_16x16x32_bf16 v[20:23], v[188:191], v[212:215], v[20:23]
	v_mfma_f32_16x16x32_bf16 v[12:15], v[180:183], v[224:227], v[12:15]
	v_mfma_f32_16x16x32_bf16 v[0:3], v[188:191], v[224:227], v[0:3]
	s_barrier
	s_add_i32 s2, 0, 0x18000
	v_add_u32_e32 v135, s2, v143
	s_add_i32 s67, 0, 0x1c000
	ds_read_b128 v[160:163], v135
	ds_read_b128 v[164:167], v135 offset:1024
	ds_read_b128 v[168:171], v135 offset:2048
	ds_read_b128 v[172:175], v135 offset:3072
	v_add_u32_e32 v135, s67, v143
	ds_read_b128 v[176:179], v135
	ds_read_b128 v[180:183], v135 offset:1024
	ds_read_b128 v[184:187], v135 offset:2048
	ds_read_b128 v[188:191], v135 offset:3072
	s_mov_b32 m0, s59
	ds_read_b128 v[192:195], v152 offset:32768
	ds_read_b128 v[196:199], v152 offset:33792
	ds_read_b128 v[200:203], v152 offset:34816
	ds_read_b128 v[204:207], v152 offset:35840
	ds_read_b128 v[208:211], v152 offset:36864
	ds_read_b128 v[212:215], v152 offset:37888
	ds_read_b128 v[220:223], v152 offset:38912
	ds_read_b128 v[224:227], v152 offset:39936
	s_nop 0
	global_load_lds_dwordx4 v96, s[20:21]
	s_mov_b32 m0, s60
	s_nop 0
	global_load_lds_dwordx4 v133, s[20:21]
	s_waitcnt vmcnt(8)
	s_waitcnt lgkmcnt(0)
	s_barrier
	v_mfma_f32_16x16x32_bf16 v[122:125], v[160:163], v[192:195], v[122:125]
	v_mfma_f32_16x16x32_bf16 v[114:117], v[168:171], v[192:195], v[114:117]
	v_mfma_f32_16x16x32_bf16 v[106:109], v[160:163], v[200:203], v[106:109]
	v_mfma_f32_16x16x32_bf16 v[98:101], v[168:171], v[200:203], v[98:101]
	v_mfma_f32_16x16x32_bf16 v[88:91], v[160:163], v[208:211], v[88:91]
	v_mfma_f32_16x16x32_bf16 v[80:83], v[168:171], v[208:211], v[80:83]
	v_mfma_f32_16x16x32_bf16 v[72:75], v[160:163], v[220:223], v[72:75]
	v_mfma_f32_16x16x32_bf16 v[64:67], v[168:171], v[220:223], v[64:67]
	v_mfma_f32_16x16x32_bf16 v[122:125], v[164:167], v[196:199], v[122:125]
	v_mfma_f32_16x16x32_bf16 v[114:117], v[172:175], v[196:199], v[114:117]
	v_mfma_f32_16x16x32_bf16 v[106:109], v[164:167], v[204:207], v[106:109]
	v_mfma_f32_16x16x32_bf16 v[98:101], v[172:175], v[204:207], v[98:101]
	v_mfma_f32_16x16x32_bf16 v[88:91], v[164:167], v[212:215], v[88:91]
	v_mfma_f32_16x16x32_bf16 v[80:83], v[172:175], v[212:215], v[80:83]
	v_mfma_f32_16x16x32_bf16 v[72:75], v[164:167], v[224:227], v[72:75]
	v_mfma_f32_16x16x32_bf16 v[64:67], v[172:175], v[224:227], v[64:67]
	v_mfma_f32_16x16x32_bf16 v[126:129], v[176:179], v[192:195], v[126:129]
	v_mfma_f32_16x16x32_bf16 v[118:121], v[184:187], v[192:195], v[118:121]
	v_mfma_f32_16x16x32_bf16 v[110:113], v[176:179], v[200:203], v[110:113]
	v_mfma_f32_16x16x32_bf16 v[102:105], v[184:187], v[200:203], v[102:105]
	v_mfma_f32_16x16x32_bf16 v[92:95], v[176:179], v[208:211], v[92:95]
	v_mfma_f32_16x16x32_bf16 v[84:87], v[184:187], v[208:211], v[84:87]
	v_mfma_f32_16x16x32_bf16 v[76:79], v[176:179], v[220:223], v[76:79]
	v_mfma_f32_16x16x32_bf16 v[68:71], v[184:187], v[220:223], v[68:71]
	v_mfma_f32_16x16x32_bf16 v[126:129], v[180:183], v[196:199], v[126:129]
	v_mfma_f32_16x16x32_bf16 v[118:121], v[188:191], v[196:199], v[118:121]
	v_mfma_f32_16x16x32_bf16 v[110:113], v[180:183], v[204:207], v[110:113]
	v_mfma_f32_16x16x32_bf16 v[102:105], v[188:191], v[204:207], v[102:105]
	v_mfma_f32_16x16x32_bf16 v[92:95], v[180:183], v[212:215], v[92:95]
	v_mfma_f32_16x16x32_bf16 v[84:87], v[188:191], v[212:215], v[84:87]
	v_mfma_f32_16x16x32_bf16 v[76:79], v[180:183], v[224:227], v[76:79]
	v_mfma_f32_16x16x32_bf16 v[68:71], v[188:191], v[224:227], v[68:71]
	s_barrier
; #define PG8_STAGE(bufoff, gbase, voff) do { _Pragma("unroll") for (int _i = 0; _i < 2; ++_i) \
;         __builtin_amdgcn_global_load_lds((const __attribute__((address_space(1))) unsigned*)((const __attribute__((address_space(1))) char*)(gbase) + (unsigned)lnd_v((int)(voff)[_i])), (LAS unsigned*)(lds + (bufoff) + ldsw + _i * 8192), 16, 0, 0); } while (0)
; #define PG8_LDA(dst, b, h) do { _Pragma("unroll") for (int m = 0; m < 4; ++m) _Pragma("unroll") for (int k = 0; k < 2; ++k) dst[m][k] = *(const LAS bf16x8*)(lds + PG8_SA(b, h) + aoff + m * 2048 + k * 1024); } while (0)
; #define PG8_MMA(ai, bj, At, Bt) do { __builtin_amdgcn_s_setprio(1); _Pragma("unroll") for (int m = 0; m < 4; ++m) _Pragma("unroll") for (int n = 0; n < 2; ++n) _Pragma("unroll") for (int k = 0; k < 2; ++k) \
;         acc[ai][bj][m][n] = __builtin_amdgcn_mfma_f32_16x16x32_bf16(Bt[n][k], At[m][k], acc[ai][bj][m][n], 0, 0, 0); __builtin_amdgcn_s_setprio(0); } while (0)
; #define PG8_WAIT_V(n) asm volatile("s_waitcnt vmcnt(" #n ")" ::: "memory")
; #define PG8_WAIT_L(n) asm volatile("s_waitcnt lgkmcnt(" #n ")" ::: "memory")
; #define PG8_BAR __builtin_amdgcn_s_barrier()
; #define PG8_SCHED __builtin_amdgcn_sched_barrier(0)
; template <class Desc, class Epi>
; __device__ __forceinline__ void gemm_phase(const int wv_, LAS unsigned char* lds, const Desc& d, const Epi& E) {
;     ...
;             PG8_LDA(At, 1, 1); PG8_STAGE(PG8_SB(1, 0), b3, voffB); PG8_STAGE(PG8_SB(1, 1), b3 + hstepB, voffB); PG8_STAGE(PG8_SA(1, 0), a3, sA0);
;             PG8_WAIT_V(8); PG8_WAIT_L(0); PG8_BAR; PG8_MMA(1, 0, At, B0); PG8_MMA(1, 1, At, B1); PG8_BAR; PG8_SCHED;
;         }
;         if (wr == 0) PG8_BAR;
	v_mov_b32_e32 v96, v138
	ds_read_b128 v[192:195], v152 offset:49152
	ds_read_b128 v[196:199], v152 offset:50176
	ds_read_b128 v[200:203], v152 offset:51200
	ds_read_b128 v[204:207], v152 offset:52224
	ds_read_b128 v[208:211], v152 offset:53248
	ds_read_b128 v[212:215], v152 offset:54272
	ds_read_b128 v[220:223], v152 offset:55296
	ds_read_b128 v[224:227], v152 offset:56320
	s_add_i32 s2, s2, s56
	v_lshl_add_u64 v[228:229], s[22:23], 0, v[96:97]
	v_lshl_add_u64 v[228:229], v[228:229], 0, s[30:31]
	s_mov_b32 m0, s2
	v_mov_b32_e32 v96, v141
	global_load_lds_dwordx4 v[228:229], off
	s_add_i32 m0, s2, 0x2000
	s_add_u32 s2, s22, 0x40080
	v_lshl_add_u64 v[228:229], s[22:23], 0, v[96:97]
	v_lshl_add_u64 v[228:229], v[228:229], 0, s[30:31]
	s_addc_u32 s3, s23, 0
	s_add_i32 s22, s67, s56
	global_load_lds_dwordx4 v[228:229], off
	s_mov_b32 m0, s22
	v_mov_b32_e32 v135, v97
	global_load_lds_dwordx4 v138, s[2:3]
	v_mov_b32_e32 v96, v141
	s_add_i32 m0, s22, 0x2000
	v_mov_b32_e32 v133, v97
	global_load_lds_dwordx4 v96, s[2:3]
	s_mov_b32 m0, s61
	v_lshl_add_u64 v[134:135], s[20:21], 0, v[134:135]
	v_lshl_add_u64 v[134:135], v[134:135], 0, s[30:31]
	global_load_lds_dwordx4 v[134:135], off
	s_mov_b32 m0, s62
	v_lshl_add_u64 v[132:133], s[20:21], 0, v[132:133]
	v_lshl_add_u64 v[132:133], v[132:133], 0, s[30:31]
	global_load_lds_dwordx4 v[132:133], off
	s_waitcnt vmcnt(8)
	s_waitcnt lgkmcnt(0)
	s_barrier
	v_mfma_f32_16x16x32_bf16 v[56:59], v[160:163], v[192:195], v[56:59]
	v_mfma_f32_16x16x32_bf16 v[48:51], v[168:171], v[192:195], v[48:51]
	v_mfma_f32_16x16x32_bf16 v[40:43], v[160:163], v[200:203], v[40:43]
	v_mfma_f32_16x16x32_bf16 v[32:35], v[168:171], v[200:203], v[32:35]
	v_mfma_f32_16x16x32_bf16 v[24:27], v[160:163], v[208:211], v[24:27]
	v_mfma_f32_16x16x32_bf16 v[16:19], v[168:171], v[208:211], v[16:19]
	v_mfma_f32_16x16x32_bf16 v[8:11], v[160:163], v[220:223], v[8:11]
	v_mfma_f32_16x16x32_bf16 v[4:7], v[168:171], v[220:223], v[4:7]
	v_mfma_f32_16x16x32_bf16 v[56:59], v[164:167], v[196:199], v[56:59]
	v_mfma_f32_16x16x32_bf16 v[48:51], v[172:175], v[196:199], v[48:51]
	v_mfma_f32_16x16x32_bf16 v[40:43], v[164:167], v[204:207], v[40:43]
	v_mfma_f32_16x16x32_bf16 v[32:35], v[172:175], v[204:207], v[32:35]
	v_mfma_f32_16x16x32_bf16 v[24:27], v[164:167], v[212:215], v[24:27]
	v_mfma_f32_16x16x32_bf16 v[16:19], v[172:175], v[212:215], v[16:19]
	v_mfma_f32_16x16x32_bf16 v[8:11], v[164:167], v[224:227], v[8:11]
	v_mfma_f32_16x16x32_bf16 v[4:7], v[172:175], v[224:227], v[4:7]
	v_mfma_f32_16x16x32_bf16 v[60:63], v[176:179], v[192:195], v[60:63]
	v_mfma_f32_16x16x32_bf16 v[52:55], v[184:187], v[192:195], v[52:55]
	v_mfma_f32_16x16x32_bf16 v[44:47], v[176:179], v[200:203], v[44:47]
	v_mfma_f32_16x16x32_bf16 v[36:39], v[184:187], v[200:203], v[36:39]
	v_mfma_f32_16x16x32_bf16 v[28:31], v[176:179], v[208:211], v[28:31]
	v_mfma_f32_16x16x32_bf16 v[20:23], v[184:187], v[208:211], v[20:23]
	v_mfma_f32_16x16x32_bf16 v[12:15], v[176:179], v[220:223], v[12:15]
	v_mfma_f32_16x16x32_bf16 v[0:3], v[184:187], v[220:223], v[0:3]
	v_mfma_f32_16x16x32_bf16 v[60:63], v[180:183], v[196:199], v[60:63]
	v_mfma_f32_16x16x32_bf16 v[52:55], v[188:191], v[196:199], v[52:55]
	v_mfma_f32_16x16x32_bf16 v[44:47], v[180:183], v[204:207], v[44:47]
	v_mfma_f32_16x16x32_bf16 v[36:39], v[188:191], v[204:207], v[36:39]
	v_mfma_f32_16x16x32_bf16 v[28:31], v[180:183], v[212:215], v[28:31]
	v_mfma_f32_16x16x32_bf16 v[20:23], v[188:191], v[212:215], v[20:23]
	v_mfma_f32_16x16x32_bf16 v[12:15], v[180:183], v[224:227], v[12:15]
	v_mfma_f32_16x16x32_bf16 v[0:3], v[188:191], v[224:227], v[0:3]
	s_barrier
	s_add_i32 s66, s66, 2
	s_cmp_gt_u32 s66, 13
	s_mov_b64 s[2:3], s[4:5]
	s_cbranch_scc0 .LBB0_1861
	s_and_b64 vcc, exec, s[40:41]
	s_cbranch_vccz .LBB0_1864
	s_barrier

; #define PG8_STAGE(bufoff, gbase, voff) do { _Pragma("unroll") for (int _i = 0; _i < 2; ++_i) \
;         __builtin_amdgcn_global_load_lds((const __attribute__((address_space(1))) unsigned*)((const __attribute__((address_space(1))) char*)(gbase) + (unsigned)lnd_v((int)(voff)[_i])), (LAS unsigned*)(lds + (bufoff) + ldsw + _i * 8192), 16, 0, 0); } while (0)
; #define PG8_LDA(dst, b, h) do { _Pragma("unroll") for (int m = 0; m < 4; ++m) _Pragma("unroll") for (int k = 0; k < 2; ++k) dst[m][k] = *(const LAS bf16x8*)(lds + PG8_SA(b, h) + aoff + m * 2048 + k * 1024); } while (0)
; #define PG8_LDB(dst, b, h) do { _Pragma("unroll") for (int n = 0; n < 2; ++n) _Pragma("unroll") for (int k = 0; k < 2; ++k) dst[n][k] = *(const LAS bf16x8*)(lds + PG8_SB(b, h) + boff + n * 2048 + k * 1024); } while (0)
; #define PG8_MMA(ai, bj, At, Bt) do { __builtin_amdgcn_s_setprio(1); _Pragma("unroll") for (int m = 0; m < 4; ++m) _Pragma("unroll") for (int n = 0; n < 2; ++n) _Pragma("unroll") for (int k = 0; k < 2; ++k) \
;         acc[ai][bj][m][n] = __builtin_amdgcn_mfma_f32_16x16x32_bf16(Bt[n][k], At[m][k], acc[ai][bj][m][n], 0, 0, 0); __builtin_amdgcn_s_setprio(0); } while (0)
; #define PG8_WAIT_V(n) asm volatile("s_waitcnt vmcnt(" #n ")" ::: "memory")
; #define PG8_WAIT_L(n) asm volatile("s_waitcnt lgkmcnt(" #n ")" ::: "memory")
; #define PG8_BAR __builtin_amdgcn_s_barrier()
; #define PG8_SCHED __builtin_amdgcn_sched_barrier(0)
; template <class Desc, class Epi>
; __device__ __forceinline__ void gemm_phase(const int wv_, LAS unsigned char* lds, const Desc& d, const Epi& E) {
;     ...
;             const char* a1 = cA + (size_t)(t + 1) * kstep;
;             const char* a2 = last ? nA : cA + (size_t)(t + 2) * kstep; const char* b2 = last ? nB : cB + (size_t)(t + 2) * kstep;
;             const char* a3 = a2 + kstep; const char* b3 = b2 + kstep;
;             PG8_LDB(B0, 0, 0); PG8_LDB(B1, 0, 1); PG8_SCHED; PG8_LDA(At, 0, 0); PG8_STAGE(PG8_SA(1, 1), a1, voffA1);
;             PG8_WAIT_V(8); PG8_WAIT_L(0); PG8_BAR; PG8_MMA(0, 0, At, B0); PG8_MMA(0, 1, At, B1); PG8_BAR; PG8_SCHED;
;             PG8_LDA(At, 0, 1); PG8_STAGE(PG8_SB(0, 0), b2, voffB); PG8_STAGE(PG8_SB(0, 1), b2 + hstepB, voffB); PG8_STAGE(PG8_SA(0, 0), a2, sA0);
;             PG8_WAIT_V(8); PG8_WAIT_L(0); PG8_BAR; PG8_MMA(1, 0, At, B0); PG8_MMA(1, 1, At, B1); PG8_BAR; PG8_SCHED;
.LBB0_1942:
	s_add_u32 s4, s2, 0x80
	s_addc_u32 s5, s3, 0
	s_add_i32 s63, 0, 0x10000
	s_cmp_eq_u32 s62, 28
	s_cselect_b32 s5, s47, s5
	s_cselect_b32 s4, s46, s4
	v_add_u32_e32 v96, s63, v139
	s_cselect_b32 s21, s45, s43
	s_cselect_b32 s20, s44, s29
	s_add_i32 s66, 0, 0x14000
	ds_read_b128 v[150:153], v96
	ds_read_b128 v[154:157], v96 offset:1024
	ds_read_b128 v[158:161], v96 offset:2048
	ds_read_b128 v[162:165], v96 offset:3072
	v_add_u32_e32 v96, s66, v139
	ds_read_b128 v[166:169], v96
	ds_read_b128 v[170:173], v96 offset:1024
	ds_read_b128 v[174:177], v96 offset:2048
	ds_read_b128 v[178:181], v96 offset:3072
	ds_read_b128 v[182:185], v149
	ds_read_b128 v[186:189], v149 offset:1024
	ds_read_b128 v[190:193], v149 offset:2048
	ds_read_b128 v[194:197], v149 offset:3072
	ds_read_b128 v[198:201], v149 offset:4096
	ds_read_b128 v[202:205], v149 offset:5120
	ds_read_b128 v[206:209], v149 offset:6144
	ds_read_b128 v[210:213], v149 offset:7168
	s_add_i32 m0, s53, 0xc000
	s_nop 0
	global_load_lds_dwordx4 v133, s[2:3]
	s_add_i32 m0, s53, 0xe000
	s_nop 0
	global_load_lds_dwordx4 v136, s[2:3]
	s_waitcnt vmcnt(8)
	s_waitcnt lgkmcnt(0)
	s_barrier
	v_mfma_f32_16x16x32_bf16 v[126:129], v[150:153], v[182:185], v[126:129]
	v_mfma_f32_16x16x32_bf16 v[122:125], v[158:161], v[182:185], v[122:125]
	v_mfma_f32_16x16x32_bf16 v[110:113], v[150:153], v[190:193], v[110:113]
	v_mfma_f32_16x16x32_bf16 v[106:109], v[158:161], v[190:193], v[106:109]
	v_mfma_f32_16x16x32_bf16 v[92:95], v[150:153], v[198:201], v[92:95]
	v_mfma_f32_16x16x32_bf16 v[88:91], v[158:161], v[198:201], v[88:91]
	v_mfma_f32_16x16x32_bf16 v[76:79], v[150:153], v[206:209], v[76:79]
	v_mfma_f32_16x16x32_bf16 v[72:75], v[158:161], v[206:209], v[72:75]
	v_mfma_f32_16x16x32_bf16 v[126:129], v[154:157], v[186:189], v[126:129]
	v_mfma_f32_16x16x32_bf16 v[122:125], v[162:165], v[186:189], v[122:125]
	v_mfma_f32_16x16x32_bf16 v[110:113], v[154:157], v[194:197], v[110:113]
	v_mfma_f32_16x16x32_bf16 v[106:109], v[162:165], v[194:197], v[106:109]
	v_mfma_f32_16x16x32_bf16 v[92:95], v[154:157], v[202:205], v[92:95]
	v_mfma_f32_16x16x32_bf16 v[88:91], v[162:165], v[202:205], v[88:91]
	v_mfma_f32_16x16x32_bf16 v[76:79], v[154:157], v[210:213], v[76:79]
	v_mfma_f32_16x16x32_bf16 v[72:75], v[162:165], v[210:213], v[72:75]
	v_mfma_f32_16x16x32_bf16 v[118:121], v[166:169], v[182:185], v[118:121]
	v_mfma_f32_16x16x32_bf16 v[114:117], v[174:177], v[182:185], v[114:117]
	v_mfma_f32_16x16x32_bf16 v[102:105], v[166:169], v[190:193], v[102:105]
	v_mfma_f32_16x16x32_bf16 v[98:101], v[174:177], v[190:193], v[98:101]
	v_mfma_f32_16x16x32_bf16 v[84:87], v[166:169], v[198:201], v[84:87]
	v_mfma_f32_16x16x32_bf16 v[80:83], v[174:177], v[198:201], v[80:83]
	v_mfma_f32_16x16x32_bf16 v[68:71], v[166:169], v[206:209], v[68:71]
	v_mfma_f32_16x16x32_bf16 v[64:67], v[174:177], v[206:209], v[64:67]
	v_mfma_f32_16x16x32_bf16 v[118:121], v[170:173], v[186:189], v[118:121]
	v_mfma_f32_16x16x32_bf16 v[114:117], v[178:181], v[186:189], v[114:117]
	v_mfma_f32_16x16x32_bf16 v[102:105], v[170:173], v[194:197], v[102:105]
	v_mfma_f32_16x16x32_bf16 v[98:101], v[178:181], v[194:197], v[98:101]
	v_mfma_f32_16x16x32_bf16 v[84:87], v[170:173], v[202:205], v[84:87]
	v_mfma_f32_16x16x32_bf16 v[80:83], v[178:181], v[202:205], v[80:83]
	v_mfma_f32_16x16x32_bf16 v[68:71], v[170:173], v[210:213], v[68:71]
	v_mfma_f32_16x16x32_bf16 v[64:67], v[178:181], v[210:213], v[64:67]
	s_barrier
	s_add_i32 s63, s63, s52
	ds_read_b128 v[182:185], v149 offset:16384
	ds_read_b128 v[186:189], v149 offset:17408
	ds_read_b128 v[190:193], v149 offset:18432
	ds_read_b128 v[194:197], v149 offset:19456
	ds_read_b128 v[198:201], v149 offset:20480
	ds_read_b128 v[202:205], v149 offset:21504
	ds_read_b128 v[206:209], v149 offset:22528
	ds_read_b128 v[210:213], v149 offset:23552
	s_mov_b32 m0, s63
	s_nop 0
	global_load_lds_dwordx4 v134, s[20:21]
	s_add_i32 m0, s63, 0x2000
	s_add_u32 s64, s20, 0x80000
	global_load_lds_dwordx4 v137, s[20:21]
	s_addc_u32 s65, s21, 0
	s_add_i32 s63, s66, s52
	s_mov_b32 m0, s63
	s_nop 0
	global_load_lds_dwordx4 v134, s[64:65]
	s_add_i32 m0, s63, 0x2000
	s_nop 0
	global_load_lds_dwordx4 v137, s[64:65]
	s_mov_b32 m0, s53
	s_nop 0
	global_load_lds_dwordx4 v132, s[4:5]
	s_mov_b32 m0, s54
	s_nop 0
	global_load_lds_dwordx4 v135, s[4:5]
	s_waitcnt vmcnt(8)
	s_waitcnt lgkmcnt(0)
	s_barrier
	v_mfma_f32_16x16x32_bf16 v[60:63], v[150:153], v[182:185], v[60:63]
	v_mfma_f32_16x16x32_bf16 v[56:59], v[158:161], v[182:185], v[56:59]
	v_mfma_f32_16x16x32_bf16 v[44:47], v[150:153], v[190:193], v[44:47]
	v_mfma_f32_16x16x32_bf16 v[32:35], v[158:161], v[190:193], v[32:35]
	v_mfma_f32_16x16x32_bf16 v[16:19], v[150:153], v[198:201], v[16:19]
	v_mfma_f32_16x16x32_bf16 v[8:11], v[158:161], v[198:201], v[8:11]
	v_mfma_f32_16x16x32_bf16 v[4:7], v[150:153], v[206:209], v[4:7]
	v_mfma_f32_16x16x32_bf16 v[0:3], v[158:161], v[206:209], v[0:3]
	v_mfma_f32_16x16x32_bf16 v[60:63], v[154:157], v[186:189], v[60:63]
	v_mfma_f32_16x16x32_bf16 v[56:59], v[162:165], v[186:189], v[56:59]
	v_mfma_f32_16x16x32_bf16 v[44:47], v[154:157], v[194:197], v[44:47]
	v_mfma_f32_16x16x32_bf16 v[32:35], v[162:165], v[194:197], v[32:35]
	v_mfma_f32_16x16x32_bf16 v[16:19], v[154:157], v[202:205], v[16:19]
	v_mfma_f32_16x16x32_bf16 v[8:11], v[162:165], v[202:205], v[8:11]
	v_mfma_f32_16x16x32_bf16 v[4:7], v[154:157], v[210:213], v[4:7]
	v_mfma_f32_16x16x32_bf16 v[0:3], v[162:165], v[210:213], v[0:3]
	v_mfma_f32_16x16x32_bf16 v[52:55], v[166:169], v[182:185], v[52:55]
	v_mfma_f32_16x16x32_bf16 v[48:51], v[174:177], v[182:185], v[48:51]
	v_mfma_f32_16x16x32_bf16 v[28:31], v[166:169], v[190:193], v[28:31]
	v_mfma_f32_16x16x32_bf16 v[12:15], v[174:177], v[190:193], v[12:15]
	v_mfma_f32_16x16x32_bf16 v[36:39], v[166:169], v[198:201], v[36:39]
	v_mfma_f32_16x16x32_bf16 v[40:43], v[174:177], v[198:201], v[40:43]
	v_mfma_f32_16x16x32_bf16 v[20:23], v[166:169], v[206:209], v[20:23]
	v_mfma_f32_16x16x32_bf16 v[24:27], v[174:177], v[206:209], v[24:27]
	v_mfma_f32_16x16x32_bf16 v[52:55], v[170:173], v[186:189], v[52:55]
	v_mfma_f32_16x16x32_bf16 v[48:51], v[178:181], v[186:189], v[48:51]
	v_mfma_f32_16x16x32_bf16 v[28:31], v[170:173], v[194:197], v[28:31]
	v_mfma_f32_16x16x32_bf16 v[12:15], v[178:181], v[194:197], v[12:15]
	v_mfma_f32_16x16x32_bf16 v[36:39], v[170:173], v[202:205], v[36:39]
	v_mfma_f32_16x16x32_bf16 v[40:43], v[178:181], v[202:205], v[40:43]
	v_mfma_f32_16x16x32_bf16 v[20:23], v[170:173], v[210:213], v[20:23]
	v_mfma_f32_16x16x32_bf16 v[24:27], v[178:181], v[210:213], v[24:27]
	s_barrier
; #define PG8_STAGE(bufoff, gbase, voff) do { _Pragma("unroll") for (int _i = 0; _i < 2; ++_i) \
;         __builtin_amdgcn_global_load_lds((const __attribute__((address_space(1))) unsigned*)((const __attribute__((address_space(1))) char*)(gbase) + (unsigned)lnd_v((int)(voff)[_i])), (LAS unsigned*)(lds + (bufoff) + ldsw + _i * 8192), 16, 0, 0); } while (0)
; #define PG8_LDA(dst, b, h) do { _Pragma("unroll") for (int m = 0; m < 4; ++m) _Pragma("unroll") for (int k = 0; k < 2; ++k) dst[m][k] = *(const LAS bf16x8*)(lds + PG8_SA(b, h) + aoff + m * 2048 + k * 1024); } while (0)
; #define PG8_LDB(dst, b, h) do { _Pragma("unroll") for (int n = 0; n < 2; ++n) _Pragma("unroll") for (int k = 0; k < 2; ++k) dst[n][k] = *(const LAS bf16x8*)(lds + PG8_SB(b, h) + boff + n * 2048 + k * 1024); } while (0)
; #define PG8_MMA(ai, bj, At, Bt) do { __builtin_amdgcn_s_setprio(1); _Pragma("unroll") for (int m = 0; m < 4; ++m) _Pragma("unroll") for (int n = 0; n < 2; ++n) _Pragma("unroll") for (int k = 0; k < 2; ++k) \
;         acc[ai][bj][m][n] = __builtin_amdgcn_mfma_f32_16x16x32_bf16(Bt[n][k], At[m][k], acc[ai][bj][m][n], 0, 0, 0); __builtin_amdgcn_s_setprio(0); } while (0)
; #define PG8_WAIT_V(n) asm volatile("s_waitcnt vmcnt(" #n ")" ::: "memory")
; #define PG8_WAIT_L(n) asm volatile("s_waitcnt lgkmcnt(" #n ")" ::: "memory")
; #define PG8_BAR __builtin_amdgcn_s_barrier()
; #define PG8_SCHED __builtin_amdgcn_sched_barrier(0)
; template <class Desc, class Epi>
; __device__ __forceinline__ void gemm_phase(const int wv_, LAS unsigned char* lds, const Desc& d, const Epi& E) {
;     ...
;             PG8_LDB(B0, 1, 0); PG8_LDB(B1, 1, 1); PG8_SCHED; PG8_LDA(At, 1, 0); PG8_STAGE(PG8_SA(0, 1), a2, sA1);
;             PG8_WAIT_V(8); PG8_WAIT_L(0); PG8_BAR; PG8_MMA(0, 0, At, B0); PG8_MMA(0, 1, At, B1); PG8_BAR; PG8_SCHED;
	s_add_i32 s63, 0, 0x18000
	v_add_u32_e32 v96, s63, v139
	s_add_i32 s64, 0, 0x1c000
	ds_read_b128 v[150:153], v96
	ds_read_b128 v[154:157], v96 offset:1024
	ds_read_b128 v[158:161], v96 offset:2048
	ds_read_b128 v[162:165], v96 offset:3072
	v_add_u32_e32 v96, s64, v139
	ds_read_b128 v[166:169], v96
	ds_read_b128 v[170:173], v96 offset:1024
	ds_read_b128 v[174:177], v96 offset:2048
	ds_read_b128 v[178:181], v96 offset:3072
	s_mov_b32 m0, s55
	ds_read_b128 v[182:185], v149 offset:32768
	ds_read_b128 v[186:189], v149 offset:33792
	ds_read_b128 v[190:193], v149 offset:34816
	ds_read_b128 v[194:197], v149 offset:35840
	ds_read_b128 v[198:201], v149 offset:36864
	ds_read_b128 v[202:205], v149 offset:37888
	ds_read_b128 v[206:209], v149 offset:38912
	ds_read_b128 v[210:213], v149 offset:39936
	s_nop 0
	global_load_lds_dwordx4 v133, s[4:5]
	s_mov_b32 m0, s56
	s_nop 0
	global_load_lds_dwordx4 v136, s[4:5]
	s_waitcnt vmcnt(8)
	s_waitcnt lgkmcnt(0)
	s_barrier
	v_mfma_f32_16x16x32_bf16 v[126:129], v[150:153], v[182:185], v[126:129]
	v_mfma_f32_16x16x32_bf16 v[122:125], v[158:161], v[182:185], v[122:125]
	v_mfma_f32_16x16x32_bf16 v[110:113], v[150:153], v[190:193], v[110:113]
	v_mfma_f32_16x16x32_bf16 v[106:109], v[158:161], v[190:193], v[106:109]
	v_mfma_f32_16x16x32_bf16 v[92:95], v[150:153], v[198:201], v[92:95]
	v_mfma_f32_16x16x32_bf16 v[88:91], v[158:161], v[198:201], v[88:91]
	v_mfma_f32_16x16x32_bf16 v[76:79], v[150:153], v[206:209], v[76:79]
	v_mfma_f32_16x16x32_bf16 v[72:75], v[158:161], v[206:209], v[72:75]
	v_mfma_f32_16x16x32_bf16 v[126:129], v[154:157], v[186:189], v[126:129]
	v_mfma_f32_16x16x32_bf16 v[122:125], v[162:165], v[186:189], v[122:125]
	v_mfma_f32_16x16x32_bf16 v[110:113], v[154:157], v[194:197], v[110:113]
	v_mfma_f32_16x16x32_bf16 v[106:109], v[162:165], v[194:197], v[106:109]
	v_mfma_f32_16x16x32_bf16 v[92:95], v[154:157], v[202:205], v[92:95]
	v_mfma_f32_16x16x32_bf16 v[88:91], v[162:165], v[202:205], v[88:91]
	v_mfma_f32_16x16x32_bf16 v[76:79], v[154:157], v[210:213], v[76:79]
	v_mfma_f32_16x16x32_bf16 v[72:75], v[162:165], v[210:213], v[72:75]
	v_mfma_f32_16x16x32_bf16 v[118:121], v[166:169], v[182:185], v[118:121]
	v_mfma_f32_16x16x32_bf16 v[114:117], v[174:177], v[182:185], v[114:117]
	v_mfma_f32_16x16x32_bf16 v[102:105], v[166:169], v[190:193], v[102:105]
	v_mfma_f32_16x16x32_bf16 v[98:101], v[174:177], v[190:193], v[98:101]
	v_mfma_f32_16x16x32_bf16 v[84:87], v[166:169], v[198:201], v[84:87]
	v_mfma_f32_16x16x32_bf16 v[80:83], v[174:177], v[198:201], v[80:83]
	v_mfma_f32_16x16x32_bf16 v[68:71], v[166:169], v[206:209], v[68:71]
	v_mfma_f32_16x16x32_bf16 v[64:67], v[174:177], v[206:209], v[64:67]
	v_mfma_f32_16x16x32_bf16 v[118:121], v[170:173], v[186:189], v[118:121]
	v_mfma_f32_16x16x32_bf16 v[114:117], v[178:181], v[186:189], v[114:117]
	v_mfma_f32_16x16x32_bf16 v[102:105], v[170:173], v[194:197], v[102:105]
	v_mfma_f32_16x16x32_bf16 v[98:101], v[178:181], v[194:197], v[98:101]
	v_mfma_f32_16x16x32_bf16 v[84:87], v[170:173], v[202:205], v[84:87]
	v_mfma_f32_16x16x32_bf16 v[80:83], v[178:181], v[202:205], v[80:83]
	v_mfma_f32_16x16x32_bf16 v[68:71], v[170:173], v[210:213], v[68:71]
	v_mfma_f32_16x16x32_bf16 v[64:67], v[178:181], v[210:213], v[64:67]
	s_barrier
; #define PG8_STAGE(bufoff, gbase, voff) do { _Pragma("unroll") for (int _i = 0; _i < 2; ++_i) \
;         __builtin_amdgcn_global_load_lds((const __attribute__((address_space(1))) unsigned*)((const __attribute__((address_space(1))) char*)(gbase) + (unsigned)lnd_v((int)(voff)[_i])), (LAS unsigned*)(lds + (bufoff) + ldsw + _i * 8192), 16, 0, 0); } while (0)
; #define PG8_LDA(dst, b, h) do { _Pragma("unroll") for (int m = 0; m < 4; ++m) _Pragma("unroll") for (int k = 0; k < 2; ++k) dst[m][k] = *(const LAS bf16x8*)(lds + PG8_SA(b, h) + aoff + m * 2048 + k * 1024); } while (0)
; #define PG8_MMA(ai, bj, At, Bt) do { __builtin_amdgcn_s_setprio(1); _Pragma("unroll") for (int m = 0; m < 4; ++m) _Pragma("unroll") for (int n = 0; n < 2; ++n) _Pragma("unroll") for (int k = 0; k < 2; ++k) \
;         acc[ai][bj][m][n] = __builtin_amdgcn_mfma_f32_16x16x32_bf16(Bt[n][k], At[m][k], acc[ai][bj][m][n], 0, 0, 0); __builtin_amdgcn_s_setprio(0); } while (0)
; #define PG8_WAIT_V(n) asm volatile("s_waitcnt vmcnt(" #n ")" ::: "memory")
; #define PG8_WAIT_L(n) asm volatile("s_waitcnt lgkmcnt(" #n ")" ::: "memory")
; #define PG8_BAR __builtin_amdgcn_s_barrier()
; #define PG8_SCHED __builtin_amdgcn_sched_barrier(0)
; template <class Desc, class Epi>
; __device__ __forceinline__ void gemm_phase(const int wv_, LAS unsigned char* lds, const Desc& d, const Epi& E) {
;     ...
;             PG8_LDA(At, 1, 1); PG8_STAGE(PG8_SB(1, 0), b3, voffB); PG8_STAGE(PG8_SB(1, 1), b3 + hstepB, voffB); PG8_STAGE(PG8_SA(1, 0), a3, sA0);
;             PG8_WAIT_V(8); PG8_WAIT_L(0); PG8_BAR; PG8_MMA(1, 0, At, B0); PG8_MMA(1, 1, At, B1); PG8_BAR; PG8_SCHED;
;         }
;         if (wr == 0) PG8_BAR;
	v_mov_b32_e32 v96, v134
	ds_read_b128 v[182:185], v149 offset:49152
	ds_read_b128 v[186:189], v149 offset:50176
	ds_read_b128 v[190:193], v149 offset:51200
	ds_read_b128 v[194:197], v149 offset:52224
	ds_read_b128 v[198:201], v149 offset:53248
	ds_read_b128 v[202:205], v149 offset:54272
	ds_read_b128 v[206:209], v149 offset:55296
	ds_read_b128 v[210:213], v149 offset:56320
	s_add_i32 s63, s63, s52
	v_lshl_add_u64 v[130:131], s[20:21], 0, v[96:97]
	v_lshl_add_u64 v[130:131], v[130:131], 0, s[30:31]
	s_mov_b32 m0, s63
	v_mov_b32_e32 v96, v137
	global_load_lds_dwordx4 v[130:131], off
	s_add_i32 m0, s63, 0x2000
	s_nop 0
	v_lshl_add_u64 v[130:131], s[20:21], 0, v[96:97]
	s_add_u32 s20, s20, 0x80080
	v_lshl_add_u64 v[130:131], v[130:131], 0, s[30:31]
	s_addc_u32 s21, s21, 0
	s_add_i32 s63, s64, s52
	global_load_lds_dwordx4 v[130:131], off
	s_mov_b32 m0, s63
	s_nop 0
	global_load_lds_dwordx4 v134, s[20:21]
	s_add_i32 m0, s63, 0x2000
	s_nop 0
	global_load_lds_dwordx4 v137, s[20:21]
	v_mov_b32_e32 v96, v132
	s_mov_b32 m0, s57
	v_lshl_add_u64 v[130:131], s[4:5], 0, v[96:97]
	v_lshl_add_u64 v[130:131], v[130:131], 0, s[30:31]
	v_mov_b32_e32 v96, v135
	global_load_lds_dwordx4 v[130:131], off
	s_mov_b32 m0, s58
	v_lshl_add_u64 v[130:131], s[4:5], 0, v[96:97]
	v_lshl_add_u64 v[130:131], v[130:131], 0, s[30:31]
	global_load_lds_dwordx4 v[130:131], off
	s_waitcnt vmcnt(8)
	s_waitcnt lgkmcnt(0)
	s_barrier
	v_mfma_f32_16x16x32_bf16 v[60:63], v[150:153], v[182:185], v[60:63]
	v_mfma_f32_16x16x32_bf16 v[56:59], v[158:161], v[182:185], v[56:59]
	v_mfma_f32_16x16x32_bf16 v[44:47], v[150:153], v[190:193], v[44:47]
	v_mfma_f32_16x16x32_bf16 v[32:35], v[158:161], v[190:193], v[32:35]
	v_mfma_f32_16x16x32_bf16 v[16:19], v[150:153], v[198:201], v[16:19]
	v_mfma_f32_16x16x32_bf16 v[8:11], v[158:161], v[198:201], v[8:11]
	v_mfma_f32_16x16x32_bf16 v[4:7], v[150:153], v[206:209], v[4:7]
	v_mfma_f32_16x16x32_bf16 v[0:3], v[158:161], v[206:209], v[0:3]
	v_mfma_f32_16x16x32_bf16 v[60:63], v[154:157], v[186:189], v[60:63]
	v_mfma_f32_16x16x32_bf16 v[56:59], v[162:165], v[186:189], v[56:59]
	v_mfma_f32_16x16x32_bf16 v[44:47], v[154:157], v[194:197], v[44:47]
	v_mfma_f32_16x16x32_bf16 v[32:35], v[162:165], v[194:197], v[32:35]
	v_mfma_f32_16x16x32_bf16 v[16:19], v[154:157], v[202:205], v[16:19]
	v_mfma_f32_16x16x32_bf16 v[8:11], v[162:165], v[202:205], v[8:11]
	v_mfma_f32_16x16x32_bf16 v[4:7], v[154:157], v[210:213], v[4:7]
	v_mfma_f32_16x16x32_bf16 v[0:3], v[162:165], v[210:213], v[0:3]
	v_mfma_f32_16x16x32_bf16 v[52:55], v[166:169], v[182:185], v[52:55]
	v_mfma_f32_16x16x32_bf16 v[48:51], v[174:177], v[182:185], v[48:51]
	v_mfma_f32_16x16x32_bf16 v[28:31], v[166:169], v[190:193], v[28:31]
	v_mfma_f32_16x16x32_bf16 v[12:15], v[174:177], v[190:193], v[12:15]
	v_mfma_f32_16x16x32_bf16 v[36:39], v[166:169], v[198:201], v[36:39]
	v_mfma_f32_16x16x32_bf16 v[40:43], v[174:177], v[198:201], v[40:43]
	v_mfma_f32_16x16x32_bf16 v[20:23], v[166:169], v[206:209], v[20:23]
	v_mfma_f32_16x16x32_bf16 v[24:27], v[174:177], v[206:209], v[24:27]
	v_mfma_f32_16x16x32_bf16 v[52:55], v[170:173], v[186:189], v[52:55]
	v_mfma_f32_16x16x32_bf16 v[48:51], v[178:181], v[186:189], v[48:51]
	v_mfma_f32_16x16x32_bf16 v[28:31], v[170:173], v[194:197], v[28:31]
	v_mfma_f32_16x16x32_bf16 v[12:15], v[178:181], v[194:197], v[12:15]
	v_mfma_f32_16x16x32_bf16 v[36:39], v[170:173], v[202:205], v[36:39]
	v_mfma_f32_16x16x32_bf16 v[40:43], v[178:181], v[202:205], v[40:43]
	v_mfma_f32_16x16x32_bf16 v[20:23], v[170:173], v[210:213], v[20:23]
	v_mfma_f32_16x16x32_bf16 v[24:27], v[178:181], v[210:213], v[24:27]
	s_barrier
	s_add_i32 s62, s62, 2
	s_add_u32 s2, s2, 0x100
	s_addc_u32 s3, s3, 0
	s_add_u32 s29, s29, 0x100
	s_addc_u32 s43, s43, 0
	s_cmp_gt_u32 s62, 29
	s_cbranch_scc0 .LBB0_1942
	s_and_b64 vcc, exec, s[40:41]
	s_cbranch_vccz .LBB0_1945
	s_barrier
